# rotation with the end-of-tile barrier as the loop head: the exit test and back branch run before the barrier, the first LDS reads directly after it (eight K-loops)
# baseline (speedup 1.0000x reference)
.LBB0_430:
	s_add_i32 s9, s6, 0xffff8000
	s_and_b32 s9, s9, 0x8000
	s_add_i32 s9, s9, 0
	s_add_i32 s8, s5, 0
	s_add_i32 s9, s9, 0x18000
	v_add_u32_e32 v204, s9, v153
	v_add_u32_e32 v206, s8, v169
	v_add_u32_e32 v212, s9, v151
	v_add_u32_e32 v208, s9, v152
	s_branch .Lrot_ip

.Lrot_ip:
	ds_read_b64_tr_b16 v[174:175], v204
	ds_read_b64_tr_b16 v[176:177], v204 offset:2048
	ds_read_b64_tr_b16 v[178:179], v208
	ds_read_b64_tr_b16 v[180:181], v208 offset:2048
	ds_read_b128 v[182:185], v206
	ds_read_b128 v[186:189], v206 offset:2048
	ds_read_b64_tr_b16 v[190:191], v212
	ds_read_b64_tr_b16 v[192:193], v212 offset:2048
	v_add_u32_e32 v214, s9, v146
	ds_read_b64_tr_b16 v[194:195], v214
	ds_read_b64_tr_b16 v[196:197], v214 offset:2048
	ds_read_b128 v[198:201], v206 offset:4096
	s_waitcnt lgkmcnt(6)
	v_mfma_f32_16x16x32_bf16 v[62:65], v[174:177], v[182:185], v[62:65]
	v_add_u32_e32 v202, 0xfff40000, v173
	s_add_i32 s9, s2, s7
	s_mov_b32 s14, m0
	s_mov_b32 m0, s9
	s_nop 0
	global_load_lds_dwordx4 v202, s[16:17]
	s_mov_b32 m0, s14
	v_mfma_f32_16x16x32_bf16 v[46:49], v[178:181], v[182:185], v[46:49]
	s_waitcnt lgkmcnt(3)
	v_mfma_f32_16x16x32_bf16 v[38:41], v[190:193], v[182:185], v[38:41]
	s_waitcnt lgkmcnt(1)
	v_mfma_f32_16x16x32_bf16 v[34:37], v[194:197], v[182:185], v[34:37]
	v_mfma_f32_16x16x32_bf16 v[30:33], v[174:177], v[186:189], v[30:33]
	ds_read_b128 v[182:185], v206 offset:6144
	v_add_u32_e32 v202, 0xfff80000, v173
	s_add_i32 s14, s9, 0x2000
	v_mfma_f32_16x16x32_bf16 v[26:29], v[178:181], v[186:189], v[26:29]
	s_mov_b32 s30, m0
	s_mov_b32 m0, s14
	s_nop 0
	global_load_lds_dwordx4 v202, s[16:17]
	s_mov_b32 m0, s30
	v_mfma_f32_16x16x32_bf16 v[22:25], v[190:193], v[186:189], v[22:25]
	v_mfma_f32_16x16x32_bf16 v[18:21], v[194:197], v[186:189], v[18:21]
	s_waitcnt lgkmcnt(1)
	v_mfma_f32_16x16x32_bf16 v[66:69], v[174:177], v[198:201], v[66:69]
	ds_read_b128 v[186:189], v206 offset:8192
	v_add_u32_e32 v202, 0xfffc0000, v173
	s_add_i32 s14, s9, 0x4000
	v_mfma_f32_16x16x32_bf16 v[78:81], v[178:181], v[198:201], v[78:81]
	s_mov_b32 s30, m0
	s_mov_b32 m0, s14
	s_nop 0
	global_load_lds_dwordx4 v202, s[16:17]
	s_mov_b32 m0, s30
	v_mfma_f32_16x16x32_bf16 v[90:93], v[190:193], v[198:201], v[90:93]
	v_mfma_f32_16x16x32_bf16 v[94:97], v[194:197], v[198:201], v[94:97]
	s_waitcnt lgkmcnt(1)
	v_mfma_f32_16x16x32_bf16 v[114:117], v[174:177], v[182:185], v[114:117]
	ds_read_b128 v[198:201], v206 offset:10240
	s_addk_i32 s9, 0x6000
	s_mov_b32 s14, m0
	s_mov_b32 m0, s9
	s_nop 0
	global_load_lds_dwordx4 v173, s[16:17]
	s_mov_b32 m0, s14
	v_mfma_f32_16x16x32_bf16 v[122:125], v[178:181], v[182:185], v[122:125]
	v_mfma_f32_16x16x32_bf16 v[138:141], v[190:193], v[182:185], v[138:141]
	v_mfma_f32_16x16x32_bf16 v[142:145], v[194:197], v[182:185], v[142:145]
	ds_read_b128 v[182:185], v206 offset:12288
	ds_read_b64_tr_b16 v[202:203], v204 offset:16384
	ds_read_b64_tr_b16 v[204:205], v204 offset:18432
	s_waitcnt lgkmcnt(4)
	v_mfma_f32_16x16x32_bf16 v[118:121], v[174:177], v[186:189], v[118:121]
	v_mfma_f32_16x16x32_bf16 v[126:129], v[178:181], v[186:189], v[126:129]
	v_mfma_f32_16x16x32_bf16 v[134:137], v[190:193], v[186:189], v[134:137]
	v_mfma_f32_16x16x32_bf16 v[130:133], v[194:197], v[186:189], v[130:133]
	ds_read_b128 v[186:189], v206 offset:14336
	ds_read_b64_tr_b16 v[206:207], v208 offset:16384
	ds_read_b64_tr_b16 v[208:209], v208 offset:18432
	s_waitcnt lgkmcnt(6)
	v_mfma_f32_16x16x32_bf16 v[98:101], v[174:177], v[198:201], v[98:101]
	v_mfma_f32_16x16x32_bf16 v[102:105], v[178:181], v[198:201], v[102:105]
	v_mfma_f32_16x16x32_bf16 v[110:113], v[190:193], v[198:201], v[110:113]
	v_mfma_f32_16x16x32_bf16 v[106:109], v[194:197], v[198:201], v[106:109]
	v_add_u32_e32 v215, s8, v171
	ds_read_b128 v[198:201], v215
	ds_read_b64_tr_b16 v[210:211], v212 offset:16384
	ds_read_b64_tr_b16 v[212:213], v212 offset:18432
	s_waitcnt lgkmcnt(8)
	v_mfma_f32_16x16x32_bf16 v[70:73], v[174:177], v[182:185], v[70:73]
	v_mfma_f32_16x16x32_bf16 v[82:85], v[178:181], v[182:185], v[82:85]
	v_mfma_f32_16x16x32_bf16 v[86:89], v[190:193], v[182:185], v[86:89]
	v_mfma_f32_16x16x32_bf16 v[74:77], v[194:197], v[182:185], v[74:77]
	s_waitcnt lgkmcnt(5)
	v_mfma_f32_16x16x32_bf16 v[42:45], v[174:177], v[186:189], v[42:45]
	ds_read_b128 v[174:177], v215 offset:2048
	s_and_b32 s8, s6, 0x8000
	v_mfma_f32_16x16x32_bf16 v[54:57], v[178:181], v[186:189], v[54:57]
	ds_read_b64_tr_b16 v[178:179], v214 offset:16384
	ds_read_b64_tr_b16 v[180:181], v214 offset:18432
	v_mfma_f32_16x16x32_bf16 v[58:61], v[190:193], v[186:189], v[58:61]
	v_mfma_f32_16x16x32_bf16 v[50:53], v[194:197], v[186:189], v[50:53]
	s_waitcnt lgkmcnt(5)
	v_mfma_f32_16x16x32_bf16 v[62:65], v[202:205], v[198:201], v[62:65]
	ds_read_b128 v[182:185], v215 offset:4096
	s_add_u32 s14, s3, s0
	s_addc_u32 s30, s4, s1
	v_mfma_f32_16x16x32_bf16 v[46:49], v[206:209], v[198:201], v[46:49]
	s_waitcnt vmcnt(7)
	v_add_u32_e32 v190, s8, v172
	s_add_u32 s8, s14, 0x100000
	s_waitcnt lgkmcnt(4)
	v_mfma_f32_16x16x32_bf16 v[38:41], v[210:213], v[198:201], v[38:41]
	ds_write_b128 v190, v[14:17]
	s_addc_u32 s9, s30, 0
	global_load_dwordx4 v[14:17], v162, s[8:9]
	s_waitcnt lgkmcnt(2)
	v_mfma_f32_16x16x32_bf16 v[34:37], v[178:181], v[198:201], v[34:37]
	v_mfma_f32_16x16x32_bf16 v[30:33], v[202:205], v[174:177], v[30:33]
	ds_read_b128 v[186:189], v215 offset:6144
	s_waitcnt vmcnt(7)
	s_add_u32 s8, s14, 0x120000
	v_mfma_f32_16x16x32_bf16 v[26:29], v[206:209], v[174:177], v[26:29]
	ds_write_b128 v190, v[10:13] offset:8192
	s_addc_u32 s9, s30, 0
	global_load_dwordx4 v[10:13], v162, s[8:9]
	v_mfma_f32_16x16x32_bf16 v[22:25], v[210:213], v[174:177], v[22:25]
	v_mfma_f32_16x16x32_bf16 v[18:21], v[178:181], v[174:177], v[18:21]
	s_waitcnt lgkmcnt(3)
	v_mfma_f32_16x16x32_bf16 v[66:69], v[202:205], v[182:185], v[66:69]
	ds_read_b128 v[174:177], v215 offset:8192
	s_waitcnt vmcnt(7)
	s_add_u32 s8, s14, 0x140000
	v_mfma_f32_16x16x32_bf16 v[78:81], v[206:209], v[182:185], v[78:81]
	ds_write_b128 v190, v[6:9] offset:16384
	s_addc_u32 s9, s30, 0
	global_load_dwordx4 v[6:9], v162, s[8:9]
	v_mfma_f32_16x16x32_bf16 v[90:93], v[210:213], v[182:185], v[90:93]
	v_mfma_f32_16x16x32_bf16 v[94:97], v[178:181], v[182:185], v[94:97]
	s_waitcnt lgkmcnt(3)
	v_mfma_f32_16x16x32_bf16 v[114:117], v[202:205], v[186:189], v[114:117]
	ds_read_b128 v[182:185], v215 offset:10240
	s_waitcnt vmcnt(7)
	s_add_u32 s8, s14, 0x160000
	v_mfma_f32_16x16x32_bf16 v[122:125], v[206:209], v[186:189], v[122:125]
	ds_write_b128 v190, v[2:5] offset:24576
	s_addc_u32 s9, s30, 0
	global_load_dwordx4 v[2:5], v162, s[8:9]
	v_mfma_f32_16x16x32_bf16 v[138:141], v[210:213], v[186:189], v[138:141]
	v_mfma_f32_16x16x32_bf16 v[142:145], v[178:181], v[186:189], v[142:145]
	s_waitcnt lgkmcnt(3)
	v_mfma_f32_16x16x32_bf16 v[118:121], v[202:205], v[174:177], v[118:121]
	ds_read_b128 v[186:189], v215 offset:12288
	v_mfma_f32_16x16x32_bf16 v[126:129], v[206:209], v[174:177], v[126:129]
	v_mfma_f32_16x16x32_bf16 v[134:137], v[210:213], v[174:177], v[134:137]
	v_mfma_f32_16x16x32_bf16 v[130:133], v[178:181], v[174:177], v[130:133]
	s_waitcnt lgkmcnt(2)
	v_mfma_f32_16x16x32_bf16 v[98:101], v[202:205], v[182:185], v[98:101]
	ds_read_b128 v[174:177], v215 offset:14336
	v_mfma_f32_16x16x32_bf16 v[102:105], v[206:209], v[182:185], v[102:105]
	v_mfma_f32_16x16x32_bf16 v[110:113], v[210:213], v[182:185], v[110:113]
	v_mfma_f32_16x16x32_bf16 v[106:109], v[178:181], v[182:185], v[106:109]
	s_waitcnt lgkmcnt(1)
	v_mfma_f32_16x16x32_bf16 v[70:73], v[202:205], v[186:189], v[70:73]
	v_mfma_f32_16x16x32_bf16 v[82:85], v[206:209], v[186:189], v[82:85]
	v_mfma_f32_16x16x32_bf16 v[86:89], v[210:213], v[186:189], v[86:89]
	v_mfma_f32_16x16x32_bf16 v[74:77], v[178:181], v[186:189], v[74:77]
	s_waitcnt lgkmcnt(0)
	v_mfma_f32_16x16x32_bf16 v[42:45], v[202:205], v[174:177], v[42:45]
	v_mfma_f32_16x16x32_bf16 v[54:57], v[206:209], v[174:177], v[54:57]
	v_mfma_f32_16x16x32_bf16 v[58:61], v[210:213], v[174:177], v[58:61]
	v_mfma_f32_16x16x32_bf16 v[50:53], v[178:181], v[174:177], v[50:53]
	s_add_i32 s8, s5, 0x8000
	s_cmp_lg_u32 s5, 0x10000
	s_cselect_b32 s5, s8, 0
	s_add_i32 s8, s7, 0x8000
	s_cmp_lg_u32 s7, 0x10000
	s_cselect_b32 s7, s8, 0
	s_add_u32 s0, s0, 0x80000
	s_addc_u32 s1, s1, 0
	s_add_i32 s6, s6, 0x8000
	v_add_u32_e32 v173, 0x80, v173
	s_add_i32 s9, s6, 0xffff8000
	s_and_b32 s9, s9, 0x8000
	s_add_i32 s9, s9, 0
	s_add_i32 s8, s5, 0
	s_add_i32 s9, s9, 0x18000
	v_add_u32_e32 v204, s9, v153
	v_add_u32_e32 v206, s8, v169
	v_add_u32_e32 v212, s9, v151
	v_add_u32_e32 v208, s9, v152
	s_waitcnt lgkmcnt(0)
	s_cmp_lg_u32 s0, 0xf00000
	s_cbranch_scc1 .Lrot_ip_head
	s_barrier
	s_add_i32 s0, 0, 0x18000
	v_add_u32_e32 v202, s0, v153
	v_add_u32_e32 v169, 0, v169
	v_add_u32_e32 v210, s0, v151
	v_add_u32_e32 v212, s0, v146
	ds_read_b64_tr_b16 v[172:173], v202
	ds_read_b64_tr_b16 v[174:175], v202 offset:2048
	v_add_u32_e32 v206, s0, v152
	ds_read_b128 v[176:179], v169
	ds_read_b64_tr_b16 v[180:181], v206
	ds_read_b64_tr_b16 v[182:183], v206 offset:2048
	ds_read_b128 v[184:187], v169 offset:2048
	ds_read_b64_tr_b16 v[188:189], v210
	ds_read_b64_tr_b16 v[190:191], v210 offset:2048
	ds_read_b64_tr_b16 v[192:193], v212
	ds_read_b64_tr_b16 v[194:195], v212 offset:2048
	s_waitcnt lgkmcnt(7)
	v_mfma_f32_16x16x32_bf16 v[62:65], v[172:175], v[176:179], v[62:65]
	ds_read_b128 v[196:199], v169 offset:4096
	s_waitcnt lgkmcnt(6)
	v_mfma_f32_16x16x32_bf16 v[46:49], v[180:183], v[176:179], v[46:49]
	s_waitcnt lgkmcnt(3)
	v_mfma_f32_16x16x32_bf16 v[38:41], v[188:191], v[176:179], v[38:41]
	s_waitcnt lgkmcnt(1)
	v_mfma_f32_16x16x32_bf16 v[34:37], v[192:195], v[176:179], v[34:37]
	v_mfma_f32_16x16x32_bf16 v[30:33], v[172:175], v[184:187], v[30:33]
	ds_read_b128 v[176:179], v169 offset:6144
	v_mfma_f32_16x16x32_bf16 v[26:29], v[180:183], v[184:187], v[26:29]
	v_mfma_f32_16x16x32_bf16 v[22:25], v[188:191], v[184:187], v[22:25]
	v_mfma_f32_16x16x32_bf16 v[18:21], v[192:195], v[184:187], v[18:21]
	s_waitcnt lgkmcnt(1)
	v_mfma_f32_16x16x32_bf16 v[66:69], v[172:175], v[196:199], v[66:69]
	ds_read_b128 v[184:187], v169 offset:8192
	v_mfma_f32_16x16x32_bf16 v[78:81], v[180:183], v[196:199], v[78:81]
	v_mfma_f32_16x16x32_bf16 v[90:93], v[188:191], v[196:199], v[90:93]
	v_mfma_f32_16x16x32_bf16 v[94:97], v[192:195], v[196:199], v[94:97]
	s_waitcnt lgkmcnt(1)
	v_mfma_f32_16x16x32_bf16 v[114:117], v[172:175], v[176:179], v[114:117]
	ds_read_b128 v[196:199], v169 offset:10240
	v_mfma_f32_16x16x32_bf16 v[122:125], v[180:183], v[176:179], v[122:125]
	v_mfma_f32_16x16x32_bf16 v[138:141], v[188:191], v[176:179], v[138:141]
	v_mfma_f32_16x16x32_bf16 v[142:145], v[192:195], v[176:179], v[142:145]
	ds_read_b128 v[176:179], v169 offset:12288
	ds_read_b64_tr_b16 v[200:201], v202 offset:16384
	ds_read_b64_tr_b16 v[202:203], v202 offset:18432
	s_waitcnt lgkmcnt(4)
	v_mfma_f32_16x16x32_bf16 v[118:121], v[172:175], v[184:187], v[118:121]
	v_mfma_f32_16x16x32_bf16 v[126:129], v[180:183], v[184:187], v[126:129]
	v_mfma_f32_16x16x32_bf16 v[134:137], v[188:191], v[184:187], v[134:137]
	v_mfma_f32_16x16x32_bf16 v[130:133], v[192:195], v[184:187], v[130:133]
	ds_read_b128 v[184:187], v169 offset:14336
	ds_read_b64_tr_b16 v[204:205], v206 offset:16384
	ds_read_b64_tr_b16 v[206:207], v206 offset:18432
	s_waitcnt lgkmcnt(6)
	v_mfma_f32_16x16x32_bf16 v[98:101], v[172:175], v[196:199], v[98:101]
	v_mfma_f32_16x16x32_bf16 v[102:105], v[180:183], v[196:199], v[102:105]
	v_mfma_f32_16x16x32_bf16 v[110:113], v[188:191], v[196:199], v[110:113]
	v_mfma_f32_16x16x32_bf16 v[106:109], v[192:195], v[196:199], v[106:109]
	v_add_u32_e32 v171, 0, v171
	ds_read_b128 v[196:199], v171
	ds_read_b64_tr_b16 v[208:209], v210 offset:16384
	ds_read_b64_tr_b16 v[210:211], v210 offset:18432
	s_waitcnt lgkmcnt(8)
	v_mfma_f32_16x16x32_bf16 v[70:73], v[172:175], v[176:179], v[70:73]
	v_mfma_f32_16x16x32_bf16 v[82:85], v[180:183], v[176:179], v[82:85]
	v_mfma_f32_16x16x32_bf16 v[86:89], v[188:191], v[176:179], v[86:89]
	v_mfma_f32_16x16x32_bf16 v[74:77], v[192:195], v[176:179], v[74:77]
	s_waitcnt lgkmcnt(5)
	v_mfma_f32_16x16x32_bf16 v[42:45], v[172:175], v[184:187], v[42:45]
	ds_read_b128 v[172:175], v171 offset:2048
	ds_read_b64_tr_b16 v[176:177], v212 offset:16384
	ds_read_b64_tr_b16 v[178:179], v212 offset:18432
	v_mfma_f32_16x16x32_bf16 v[54:57], v[180:183], v[184:187], v[54:57]
	v_mfma_f32_16x16x32_bf16 v[58:61], v[188:191], v[184:187], v[58:61]
	v_mfma_f32_16x16x32_bf16 v[50:53], v[192:195], v[184:187], v[50:53]
	ds_read_b128 v[180:183], v171 offset:4096
	s_waitcnt vmcnt(3)
	v_add_u32_e32 v168, s38, v168
	s_waitcnt lgkmcnt(6)
	v_mfma_f32_16x16x32_bf16 v[62:65], v[200:203], v[196:199], v[62:65]
	ds_write_b128 v168, v[14:17]
	v_mfma_f32_16x16x32_bf16 v[46:49], v[204:207], v[196:199], v[46:49]
	s_waitcnt lgkmcnt(5)
	v_mfma_f32_16x16x32_bf16 v[38:41], v[208:211], v[196:199], v[38:41]
	s_waitcnt lgkmcnt(2)
	v_mfma_f32_16x16x32_bf16 v[14:17], v[176:179], v[196:199], v[34:37]
	s_nop 2
	ds_read_b128 v[34:37], v171 offset:6144
	s_waitcnt vmcnt(2)
	v_mfma_f32_16x16x32_bf16 v[30:33], v[200:203], v[172:175], v[30:33]
	ds_write_b128 v168, v[10:13] offset:8192
	v_mfma_f32_16x16x32_bf16 v[26:29], v[204:207], v[172:175], v[26:29]
	v_mfma_f32_16x16x32_bf16 v[22:25], v[208:211], v[172:175], v[22:25]
	v_mfma_f32_16x16x32_bf16 v[10:13], v[176:179], v[172:175], v[18:21]
	s_waitcnt lgkmcnt(3)
	v_mfma_f32_16x16x32_bf16 v[18:21], v[200:203], v[180:183], v[66:69]
	v_mfma_f32_16x16x32_bf16 v[66:69], v[204:207], v[180:183], v[78:81]
	v_mfma_f32_16x16x32_bf16 v[78:81], v[208:211], v[180:183], v[90:93]
	s_nop 2
	ds_read_b128 v[90:93], v171 offset:8192
	s_waitcnt vmcnt(1)
	ds_write_b128 v168, v[6:9] offset:16384
	v_mfma_f32_16x16x32_bf16 v[6:9], v[176:179], v[180:183], v[94:97]
	s_waitcnt lgkmcnt(3)
	v_mfma_f32_16x16x32_bf16 v[94:97], v[200:203], v[34:37], v[114:117]
	v_mfma_f32_16x16x32_bf16 v[114:117], v[204:207], v[34:37], v[122:125]
	v_mfma_f32_16x16x32_bf16 v[122:125], v[208:211], v[34:37], v[138:141]
	s_nop 2
	ds_read_b128 v[138:141], v171 offset:10240
	s_waitcnt vmcnt(0)
	ds_write_b128 v168, v[2:5] offset:24576
	v_mfma_f32_16x16x32_bf16 v[2:5], v[176:179], v[34:37], v[142:145]
	s_waitcnt lgkmcnt(3)
	v_mfma_f32_16x16x32_bf16 v[34:37], v[200:203], v[90:93], v[118:121]
	v_mfma_f32_16x16x32_bf16 v[118:121], v[204:207], v[90:93], v[126:129]
	v_mfma_f32_16x16x32_bf16 v[126:129], v[208:211], v[90:93], v[134:137]
	s_nop 2
	ds_read_b128 v[134:137], v171 offset:12288
	v_mfma_f32_16x16x32_bf16 v[90:93], v[176:179], v[90:93], v[130:133]
	s_waitcnt lgkmcnt(2)
	v_mfma_f32_16x16x32_bf16 v[98:101], v[200:203], v[138:141], v[98:101]
	s_nop 0
	ds_read_b128 v[130:133], v171 offset:14336
	v_mfma_f32_16x16x32_bf16 v[102:105], v[204:207], v[138:141], v[102:105]
	v_mfma_f32_16x16x32_bf16 v[110:113], v[208:211], v[138:141], v[110:113]
	v_mfma_f32_16x16x32_bf16 v[106:109], v[176:179], v[138:141], v[106:109]
	s_waitcnt lgkmcnt(1)
	v_mfma_f32_16x16x32_bf16 v[70:73], v[200:203], v[134:137], v[70:73]
	v_mfma_f32_16x16x32_bf16 v[82:85], v[204:207], v[134:137], v[82:85]
	v_mfma_f32_16x16x32_bf16 v[86:89], v[208:211], v[134:137], v[86:89]
	v_mfma_f32_16x16x32_bf16 v[74:77], v[176:179], v[134:137], v[74:77]
	s_waitcnt lgkmcnt(0)
	v_mfma_f32_16x16x32_bf16 v[42:45], v[200:203], v[130:133], v[42:45]
	v_mfma_f32_16x16x32_bf16 v[54:57], v[204:207], v[130:133], v[54:57]
	v_mfma_f32_16x16x32_bf16 v[58:61], v[208:211], v[130:133], v[58:61]
	v_mfma_f32_16x16x32_bf16 v[50:53], v[176:179], v[130:133], v[50:53]
	s_waitcnt lgkmcnt(0)
	s_barrier
	v_add_u32_e32 v153, s38, v153
	v_add_u32_e32 v152, s38, v152
	v_add_u32_e32 v151, s38, v151
	ds_read_b64_tr_b16 v[130:131], v153
	ds_read_b64_tr_b16 v[132:133], v153 offset:2048
	ds_read_b64_tr_b16 v[134:135], v152
	ds_read_b64_tr_b16 v[136:137], v152 offset:2048
	ds_read_b128 v[138:141], v169 offset:32768
	ds_read_b64_tr_b16 v[142:143], v151
	ds_read_b128 v[172:175], v169 offset:34816
	ds_read_b128 v[176:179], v169 offset:36864
	ds_read_b64_tr_b16 v[144:145], v151 offset:2048
	v_add_u32_e32 v146, s38, v146
	ds_read_b64_tr_b16 v[180:181], v146
	ds_read_b64_tr_b16 v[182:183], v146 offset:2048
	s_waitcnt lgkmcnt(6)
	v_mfma_f32_16x16x32_bf16 v[62:65], v[130:133], v[138:141], v[62:65]
	v_mfma_f32_16x16x32_bf16 v[46:49], v[134:137], v[138:141], v[46:49]
	s_waitcnt lgkmcnt(2)
	v_mfma_f32_16x16x32_bf16 v[38:41], v[142:145], v[138:141], v[38:41]
	s_waitcnt lgkmcnt(0)
	v_mfma_f32_16x16x32_bf16 v[14:17], v[180:183], v[138:141], v[14:17]
	v_mfma_f32_16x16x32_bf16 v[30:33], v[130:133], v[172:175], v[30:33]
	ds_read_b128 v[138:141], v169 offset:38912
	v_mfma_f32_16x16x32_bf16 v[26:29], v[134:137], v[172:175], v[26:29]
	v_mfma_f32_16x16x32_bf16 v[22:25], v[142:145], v[172:175], v[22:25]
	v_mfma_f32_16x16x32_bf16 v[10:13], v[180:183], v[172:175], v[10:13]
	v_mfma_f32_16x16x32_bf16 v[18:21], v[130:133], v[176:179], v[18:21]
	ds_read_b128 v[172:175], v169 offset:40960
	v_mfma_f32_16x16x32_bf16 v[66:69], v[134:137], v[176:179], v[66:69]
	v_mfma_f32_16x16x32_bf16 v[78:81], v[142:145], v[176:179], v[78:81]
	v_mfma_f32_16x16x32_bf16 v[6:9], v[180:183], v[176:179], v[6:9]
	s_waitcnt lgkmcnt(1)
	v_mfma_f32_16x16x32_bf16 v[176:179], v[130:133], v[138:141], v[94:97]
	s_nop 2
	ds_read_b128 v[94:97], v169 offset:43008
	v_mfma_f32_16x16x32_bf16 v[2:5], v[180:183], v[138:141], v[2:5]
	v_mfma_f32_16x16x32_bf16 v[184:187], v[134:137], v[138:141], v[114:117]
	v_mfma_f32_16x16x32_bf16 v[188:191], v[142:145], v[138:141], v[122:125]
	s_nop 1
	ds_read_b128 v[114:117], v169 offset:45056
	ds_read_b64_tr_b16 v[196:197], v153 offset:16384
	ds_read_b64_tr_b16 v[198:199], v153 offset:18432
	s_waitcnt lgkmcnt(4)
	v_mfma_f32_16x16x32_bf16 v[34:37], v[130:133], v[172:175], v[34:37]
	v_mfma_f32_16x16x32_bf16 v[138:141], v[134:137], v[172:175], v[118:121]
	v_mfma_f32_16x16x32_bf16 v[192:195], v[142:145], v[172:175], v[126:129]
	v_mfma_f32_16x16x32_bf16 v[172:175], v[180:183], v[172:175], v[90:93]
	s_nop 2
	ds_read_b128 v[90:93], v169 offset:47104
	ds_read_b64_tr_b16 v[212:213], v152 offset:16384
	ds_read_b64_tr_b16 v[214:215], v152 offset:18432
	s_waitcnt lgkmcnt(6)
	v_mfma_f32_16x16x32_bf16 v[200:203], v[130:133], v[94:97], v[98:101]
	v_mfma_f32_16x16x32_bf16 v[204:207], v[134:137], v[94:97], v[102:105]
	v_mfma_f32_16x16x32_bf16 v[208:211], v[142:145], v[94:97], v[110:113]
	v_mfma_f32_16x16x32_bf16 v[216:219], v[180:183], v[94:97], v[106:109]
	s_waitcnt lgkmcnt(5)
	v_mfma_f32_16x16x32_bf16 v[220:223], v[130:133], v[114:117], v[70:73]
	s_nop 2
	ds_read_b128 v[70:73], v171 offset:32768
	ds_read_b64_tr_b16 v[232:233], v151 offset:16384
	ds_read_b64_tr_b16 v[234:235], v151 offset:18432
	v_mfma_f32_16x16x32_bf16 v[224:227], v[134:137], v[114:117], v[82:85]
	v_mfma_f32_16x16x32_bf16 v[228:231], v[142:145], v[114:117], v[86:89]
	v_mfma_f32_16x16x32_bf16 v[236:239], v[180:183], v[114:117], v[74:77]
	s_waitcnt lgkmcnt(5)
	v_mfma_f32_16x16x32_bf16 v[130:133], v[130:133], v[90:93], v[42:45]
	s_nop 2
	ds_read_b128 v[42:45], v171 offset:34816
	ds_read_b64_tr_b16 v[240:241], v146 offset:16384
	ds_read_b64_tr_b16 v[242:243], v146 offset:18432
	v_mfma_f32_16x16x32_bf16 v[134:137], v[134:137], v[90:93], v[54:57]
	v_mfma_f32_16x16x32_bf16 v[142:145], v[142:145], v[90:93], v[58:61]
	v_mfma_f32_16x16x32_bf16 v[180:183], v[180:183], v[90:93], v[50:53]
	s_waitcnt lgkmcnt(3)
	v_mfma_f32_16x16x32_bf16 v[118:121], v[232:235], v[70:73], v[38:41]
	s_nop 2
	ds_read_b128 v[38:41], v171 offset:36864
	v_mfma_f32_16x16x32_bf16 v[126:129], v[196:199], v[70:73], v[62:65]
	v_mfma_f32_16x16x32_bf16 v[122:125], v[212:215], v[70:73], v[46:49]
	s_waitcnt lgkmcnt(1)
	v_mfma_f32_16x16x32_bf16 v[114:117], v[240:243], v[70:73], v[14:17]
	s_nop 2
	ds_read_b128 v[14:17], v171 offset:38912
	v_mfma_f32_16x16x32_bf16 v[110:113], v[196:199], v[42:45], v[30:33]
	v_mfma_f32_16x16x32_bf16 v[106:109], v[212:215], v[42:45], v[26:29]
	v_mfma_f32_16x16x32_bf16 v[102:105], v[232:235], v[42:45], v[22:25]
	v_mfma_f32_16x16x32_bf16 v[98:101], v[240:243], v[42:45], v[10:13]
	s_nop 2
	ds_read_b128 v[10:13], v171 offset:40960
	s_waitcnt lgkmcnt(2)
	v_mfma_f32_16x16x32_bf16 v[94:97], v[196:199], v[38:41], v[18:21]
	v_mfma_f32_16x16x32_bf16 v[90:93], v[212:215], v[38:41], v[66:69]
	v_mfma_f32_16x16x32_bf16 v[86:89], v[232:235], v[38:41], v[78:81]
	v_mfma_f32_16x16x32_bf16 v[82:85], v[240:243], v[38:41], v[6:9]
	s_nop 2
	ds_read_b128 v[6:9], v171 offset:43008
	s_waitcnt lgkmcnt(2)
	v_mfma_f32_16x16x32_bf16 v[78:81], v[196:199], v[14:17], v[176:179]
	v_mfma_f32_16x16x32_bf16 v[74:77], v[212:215], v[14:17], v[184:187]
	v_mfma_f32_16x16x32_bf16 v[70:73], v[232:235], v[14:17], v[188:191]
	v_mfma_f32_16x16x32_bf16 v[66:69], v[240:243], v[14:17], v[2:5]
	s_nop 2
	ds_read_b128 v[2:5], v171 offset:45056
	s_waitcnt lgkmcnt(2)
	v_mfma_f32_16x16x32_bf16 v[62:65], v[196:199], v[10:13], v[34:37]
	v_mfma_f32_16x16x32_bf16 v[58:61], v[212:215], v[10:13], v[138:141]
	v_mfma_f32_16x16x32_bf16 v[54:57], v[232:235], v[10:13], v[192:195]
	v_mfma_f32_16x16x32_bf16 v[50:53], v[240:243], v[10:13], v[172:175]
	s_waitcnt lgkmcnt(1)
	v_mfma_f32_16x16x32_bf16 v[46:49], v[196:199], v[6:9], v[200:203]
	ds_read_b128 v[138:141], v171 offset:47104
	v_mfma_f32_16x16x32_bf16 v[42:45], v[212:215], v[6:9], v[204:207]
	v_mfma_f32_16x16x32_bf16 v[38:41], v[232:235], v[6:9], v[208:211]
	v_mfma_f32_16x16x32_bf16 v[34:37], v[240:243], v[6:9], v[216:219]
	s_waitcnt lgkmcnt(1)
	v_mfma_f32_16x16x32_bf16 v[30:33], v[196:199], v[2:5], v[220:223]
	v_mfma_f32_16x16x32_bf16 v[26:29], v[212:215], v[2:5], v[224:227]
	v_mfma_f32_16x16x32_bf16 v[22:25], v[232:235], v[2:5], v[228:231]
	v_mfma_f32_16x16x32_bf16 v[18:21], v[240:243], v[2:5], v[236:239]
	s_waitcnt lgkmcnt(0)
	v_mfma_f32_16x16x32_bf16 v[14:17], v[196:199], v[138:141], v[130:133]
	v_mfma_f32_16x16x32_bf16 v[10:13], v[212:215], v[138:141], v[134:137]
	v_mfma_f32_16x16x32_bf16 v[6:9], v[232:235], v[138:141], v[142:145]
	v_mfma_f32_16x16x32_bf16 v[2:5], v[240:243], v[138:141], v[180:183]
	s_waitcnt lgkmcnt(0)
	s_barrier
	v_mov_b32_e32 v151, v155
	v_mov_b32_e32 v168, v1
	s_cmpk_gt_i32 s28, 0x3ff
	s_mov_b64 s[0:1], -1
	s_cbranch_scc1 .LBB0_607
	s_add_i32 s0, s52, s50
	v_add_u32_e32 v140, s0, v168
	s_lshl_b32 s0, s51, 6
	s_or_b32 s0, s0, s28
	v_lshlrev_b32_e32 v132, 2, v151
	v_add_u32_e32 v146, s0, v132
	v_ashrrev_i32_e32 v141, 31, v140
	v_lshlrev_b64 v[142:143], 11, v[140:141]
	v_cmp_lt_i32_e64 s[4:5], s39, v146
	s_and_saveexec_b64 s[0:1], s[4:5]
	s_xor_b64 s[0:1], exec, s[0:1]
	s_cbranch_execz .LBB0_442
	v_cmp_lt_u32_e32 vcc, s41, v146
	s_and_saveexec_b64 s[2:3], vcc
	s_xor_b64 s[2:3], exec, s[2:3]
	s_cbranch_execz .LBB0_439
	v_cmp_lt_u32_e32 vcc, s42, v146
	v_cvt_pk_bf16_f32 v130, v126, v127
	v_cvt_pk_bf16_f32 v131, v128, v129
	s_and_saveexec_b64 s[6:7], vcc
	s_xor_b64 s[6:7], exec, s[6:7]
	s_cbranch_execz .LBB0_436
	v_lshl_add_u64 v[134:135], s[24:25], 0, v[142:143]
	v_lshl_add_u64 v[134:135], v[146:147], 1, v[134:135]
	v_add_co_u32_e32 v134, vcc, 0xfffff000, v134
	s_nop 1
	v_addc_co_u32_e32 v135, vcc, -1, v135, vcc
	global_store_dwordx2 v[134:135], v[130:131], off offset:-2048

.LBB0_1039:
	s_add_i32 s34, s29, 0xffff8000
	s_and_b32 s34, s34, 0x8000
	s_add_i32 s34, s34, 0
	s_add_i32 s33, s30, 0
	s_add_i32 s34, s34, 0x18000
	v_add_u32_e32 v157, s34, v152
	v_add_u32_e32 v169, s33, v150
	v_add_u32_e32 v200, s34, v149
	v_add_u32_e32 v168, s34, v151
	s_branch .Lrot_gl

.Lrot_gl:
	ds_read_b64_tr_b16 v[160:161], v157
	ds_read_b64_tr_b16 v[162:163], v157 offset:2048
	ds_read_b64_tr_b16 v[164:165], v168
	ds_read_b64_tr_b16 v[166:167], v168 offset:2048
	ds_read_b128 v[172:175], v169
	ds_read_b128 v[176:179], v169 offset:2048
	ds_read_b64_tr_b16 v[180:181], v200
	ds_read_b64_tr_b16 v[182:183], v200 offset:2048
	v_add_u32_e32 v201, s34, v148
	ds_read_b64_tr_b16 v[184:185], v201
	ds_read_b64_tr_b16 v[186:187], v201 offset:2048
	ds_read_b128 v[188:191], v169 offset:4096
	s_waitcnt lgkmcnt(6)
	v_mfma_f32_16x16x32_bf16 v[18:21], v[160:163], v[172:175], v[18:21]
	v_add_u32_e32 v192, 0xfffa0000, v156
	s_add_i32 s34, s27, s31
	s_mov_b32 s35, m0
	s_mov_b32 m0, s34
	s_nop 0
	global_load_lds_dwordx4 v192, s[6:7]
	s_mov_b32 m0, s35
	v_mfma_f32_16x16x32_bf16 v[22:25], v[164:167], v[172:175], v[22:25]
	s_waitcnt lgkmcnt(3)
	v_mfma_f32_16x16x32_bf16 v[26:29], v[180:183], v[172:175], v[26:29]
	s_waitcnt lgkmcnt(1)
	v_mfma_f32_16x16x32_bf16 v[30:33], v[184:187], v[172:175], v[30:33]
	v_mfma_f32_16x16x32_bf16 v[34:37], v[160:163], v[176:179], v[34:37]
	ds_read_b128 v[172:175], v169 offset:6144
	v_add_u32_e32 v192, 0xfffc0000, v156
	s_add_i32 s35, s34, 0x2000
	v_mfma_f32_16x16x32_bf16 v[38:41], v[164:167], v[176:179], v[38:41]
	s_mov_b32 s36, m0
	s_mov_b32 m0, s35
	s_nop 0
	global_load_lds_dwordx4 v192, s[6:7]
	s_mov_b32 m0, s36
	v_mfma_f32_16x16x32_bf16 v[42:45], v[180:183], v[176:179], v[42:45]
	v_mfma_f32_16x16x32_bf16 v[54:57], v[184:187], v[176:179], v[54:57]
	s_waitcnt lgkmcnt(1)
	v_mfma_f32_16x16x32_bf16 v[66:69], v[160:163], v[188:191], v[66:69]
	ds_read_b128 v[176:179], v169 offset:8192
	v_add_u32_e32 v192, 0xfffe0000, v156
	s_add_i32 s35, s34, 0x4000
	v_mfma_f32_16x16x32_bf16 v[78:81], v[164:167], v[188:191], v[78:81]
	s_mov_b32 s36, m0
	s_mov_b32 m0, s35
	s_nop 0
	global_load_lds_dwordx4 v192, s[6:7]
	s_mov_b32 m0, s36
	v_mfma_f32_16x16x32_bf16 v[90:93], v[180:183], v[188:191], v[90:93]
	v_mfma_f32_16x16x32_bf16 v[94:97], v[184:187], v[188:191], v[94:97]
	s_waitcnt lgkmcnt(1)
	v_mfma_f32_16x16x32_bf16 v[114:117], v[160:163], v[172:175], v[114:117]
	ds_read_b128 v[188:191], v169 offset:10240
	s_addk_i32 s34, 0x6000
	s_mov_b32 s35, m0
	s_mov_b32 m0, s34
	s_nop 0
	global_load_lds_dwordx4 v156, s[6:7]
	s_mov_b32 m0, s35
	v_mfma_f32_16x16x32_bf16 v[122:125], v[164:167], v[172:175], v[122:125]
	v_mfma_f32_16x16x32_bf16 v[138:141], v[180:183], v[172:175], v[138:141]
	v_mfma_f32_16x16x32_bf16 v[142:145], v[184:187], v[172:175], v[142:145]
	ds_read_b128 v[172:175], v169 offset:12288
	ds_read_b64_tr_b16 v[192:193], v157 offset:16384
	ds_read_b64_tr_b16 v[194:195], v157 offset:18432
	s_waitcnt lgkmcnt(4)
	v_mfma_f32_16x16x32_bf16 v[118:121], v[160:163], v[176:179], v[118:121]
	v_mfma_f32_16x16x32_bf16 v[126:129], v[164:167], v[176:179], v[126:129]
	v_mfma_f32_16x16x32_bf16 v[134:137], v[180:183], v[176:179], v[134:137]
	v_mfma_f32_16x16x32_bf16 v[130:133], v[184:187], v[176:179], v[130:133]
	ds_read_b128 v[176:179], v169 offset:14336
	ds_read_b64_tr_b16 v[196:197], v168 offset:16384
	ds_read_b64_tr_b16 v[198:199], v168 offset:18432
	s_waitcnt lgkmcnt(6)
	v_mfma_f32_16x16x32_bf16 v[98:101], v[160:163], v[188:191], v[98:101]
	v_mfma_f32_16x16x32_bf16 v[102:105], v[164:167], v[188:191], v[102:105]
	v_mfma_f32_16x16x32_bf16 v[110:113], v[180:183], v[188:191], v[110:113]
	v_mfma_f32_16x16x32_bf16 v[106:109], v[184:187], v[188:191], v[106:109]
	v_add_u32_e32 v157, s33, v153
	ds_read_b128 v[188:191], v157
	ds_read_b64_tr_b16 v[216:217], v200 offset:16384
	ds_read_b64_tr_b16 v[218:219], v200 offset:18432
	s_waitcnt lgkmcnt(8)
	v_mfma_f32_16x16x32_bf16 v[70:73], v[160:163], v[172:175], v[70:73]
	v_mfma_f32_16x16x32_bf16 v[82:85], v[164:167], v[172:175], v[82:85]
	v_mfma_f32_16x16x32_bf16 v[86:89], v[180:183], v[172:175], v[86:89]
	v_mfma_f32_16x16x32_bf16 v[74:77], v[184:187], v[172:175], v[74:77]
	s_waitcnt lgkmcnt(5)
	v_mfma_f32_16x16x32_bf16 v[46:49], v[160:163], v[176:179], v[46:49]
	ds_read_b128 v[160:163], v157 offset:2048
	s_and_b32 s33, s29, 0x8000
	v_mfma_f32_16x16x32_bf16 v[58:61], v[164:167], v[176:179], v[58:61]
	ds_read_b64_tr_b16 v[164:165], v201 offset:16384
	ds_read_b64_tr_b16 v[166:167], v201 offset:18432
	v_mfma_f32_16x16x32_bf16 v[62:65], v[180:183], v[176:179], v[62:65]
	v_mfma_f32_16x16x32_bf16 v[50:53], v[184:187], v[176:179], v[50:53]
	s_waitcnt lgkmcnt(5)
	v_mfma_f32_16x16x32_bf16 v[18:21], v[192:195], v[188:191], v[18:21]
	ds_read_b128 v[172:175], v157 offset:4096
	v_add_u32_e32 v168, s33, v155
	s_add_u32 s33, s2, s0
	v_mfma_f32_16x16x32_bf16 v[22:25], v[196:199], v[188:191], v[22:25]
	s_addc_u32 s36, s28, s1
	s_waitcnt vmcnt(7)
	s_add_u32 s34, s33, 0x40000
	s_waitcnt lgkmcnt(4)
	v_mfma_f32_16x16x32_bf16 v[26:29], v[216:219], v[188:191], v[26:29]
	ds_write_b128 v168, v[14:17]
	s_addc_u32 s35, s36, 0
	global_load_dwordx4 v[14:17], v208, s[34:35]
	s_waitcnt lgkmcnt(2)
	v_mfma_f32_16x16x32_bf16 v[30:33], v[164:167], v[188:191], v[30:33]
	v_mfma_f32_16x16x32_bf16 v[34:37], v[192:195], v[160:163], v[34:37]
	ds_read_b128 v[176:179], v157 offset:6144
	s_waitcnt vmcnt(7)
	s_add_u32 s34, s33, 0x48000
	v_mfma_f32_16x16x32_bf16 v[38:41], v[196:199], v[160:163], v[38:41]
	ds_write_b128 v168, v[10:13] offset:8192
	s_addc_u32 s35, s36, 0
	global_load_dwordx4 v[10:13], v208, s[34:35]
	v_mfma_f32_16x16x32_bf16 v[42:45], v[216:219], v[160:163], v[42:45]
	v_mfma_f32_16x16x32_bf16 v[54:57], v[164:167], v[160:163], v[54:57]
	s_waitcnt lgkmcnt(3)
	v_mfma_f32_16x16x32_bf16 v[66:69], v[192:195], v[172:175], v[66:69]
	ds_read_b128 v[160:163], v157 offset:8192
	s_waitcnt vmcnt(7)
	s_add_u32 s34, s33, 0x50000
	v_mfma_f32_16x16x32_bf16 v[78:81], v[196:199], v[172:175], v[78:81]
	ds_write_b128 v168, v[6:9] offset:16384
	s_addc_u32 s35, s36, 0
	global_load_dwordx4 v[6:9], v208, s[34:35]
	v_mfma_f32_16x16x32_bf16 v[90:93], v[216:219], v[172:175], v[90:93]
	v_mfma_f32_16x16x32_bf16 v[94:97], v[164:167], v[172:175], v[94:97]
	s_waitcnt lgkmcnt(3)
	v_mfma_f32_16x16x32_bf16 v[114:117], v[192:195], v[176:179], v[114:117]
	ds_read_b128 v[172:175], v157 offset:10240
	s_waitcnt vmcnt(7)
	s_add_u32 s34, s33, 0x58000
	v_mfma_f32_16x16x32_bf16 v[122:125], v[196:199], v[176:179], v[122:125]
	ds_write_b128 v168, v[2:5] offset:24576
	s_addc_u32 s35, s36, 0
	global_load_dwordx4 v[2:5], v208, s[34:35]
	v_mfma_f32_16x16x32_bf16 v[138:141], v[216:219], v[176:179], v[138:141]
	v_mfma_f32_16x16x32_bf16 v[142:145], v[164:167], v[176:179], v[142:145]
	s_waitcnt lgkmcnt(3)
	v_mfma_f32_16x16x32_bf16 v[118:121], v[192:195], v[160:163], v[118:121]
	ds_read_b128 v[176:179], v157 offset:12288
	v_mfma_f32_16x16x32_bf16 v[126:129], v[196:199], v[160:163], v[126:129]
	v_mfma_f32_16x16x32_bf16 v[134:137], v[216:219], v[160:163], v[134:137]
	v_mfma_f32_16x16x32_bf16 v[130:133], v[164:167], v[160:163], v[130:133]
	s_waitcnt lgkmcnt(2)
	v_mfma_f32_16x16x32_bf16 v[98:101], v[192:195], v[172:175], v[98:101]
	ds_read_b128 v[160:163], v157 offset:14336
	v_mfma_f32_16x16x32_bf16 v[102:105], v[196:199], v[172:175], v[102:105]
	v_mfma_f32_16x16x32_bf16 v[110:113], v[216:219], v[172:175], v[110:113]
	v_mfma_f32_16x16x32_bf16 v[106:109], v[164:167], v[172:175], v[106:109]
	s_waitcnt lgkmcnt(1)
	v_mfma_f32_16x16x32_bf16 v[70:73], v[192:195], v[176:179], v[70:73]
	v_mfma_f32_16x16x32_bf16 v[82:85], v[196:199], v[176:179], v[82:85]
	v_mfma_f32_16x16x32_bf16 v[86:89], v[216:219], v[176:179], v[86:89]
	v_mfma_f32_16x16x32_bf16 v[74:77], v[164:167], v[176:179], v[74:77]
	s_waitcnt lgkmcnt(0)
	v_mfma_f32_16x16x32_bf16 v[46:49], v[192:195], v[160:163], v[46:49]
	v_mfma_f32_16x16x32_bf16 v[58:61], v[196:199], v[160:163], v[58:61]
	v_mfma_f32_16x16x32_bf16 v[62:65], v[216:219], v[160:163], v[62:65]
	v_mfma_f32_16x16x32_bf16 v[50:53], v[164:167], v[160:163], v[50:53]
	s_add_i32 s33, s30, 0x8000
	s_cmp_lg_u32 s30, 0x10000
	s_cselect_b32 s30, s33, 0
	s_add_i32 s33, s31, 0x8000
	s_cmp_lg_u32 s31, 0x10000
	s_cselect_b32 s31, s33, 0
	s_add_u32 s0, s0, 0x20000
	s_addc_u32 s1, s1, 0
	s_add_i32 s29, s29, 0x8000
	v_add_u32_e32 v156, 0x80, v156
	s_add_i32 s34, s29, 0xffff8000
	s_and_b32 s34, s34, 0x8000
	s_add_i32 s34, s34, 0
	s_add_i32 s33, s30, 0
	s_add_i32 s34, s34, 0x18000
	v_add_u32_e32 v157, s34, v152
	v_add_u32_e32 v169, s33, v150
	v_add_u32_e32 v200, s34, v149
	v_add_u32_e32 v168, s34, v151
	s_waitcnt lgkmcnt(0)
	s_cmp_lg_u32 s0, 0x1c0000
	s_cbranch_scc1 .Lrot_gl_head
	s_barrier
	s_add_i32 s0, 0, 0x18000
	s_add_i32 s1, 0, 0x10000
	v_add_u32_e32 v155, s0, v152
	v_add_u32_e32 v157, s1, v150
	v_add_u32_e32 v168, s0, v149
	v_add_u32_e32 v169, s0, v148
	v_add_u32_e32 v156, s0, v151
	ds_read_b64_tr_b16 v[160:161], v155
	ds_read_b64_tr_b16 v[162:163], v155 offset:2048
	ds_read_b64_tr_b16 v[164:165], v156
	ds_read_b64_tr_b16 v[166:167], v156 offset:2048
	ds_read_b128 v[172:175], v157
	ds_read_b128 v[176:179], v157 offset:2048
	ds_read_b64_tr_b16 v[180:181], v168
	ds_read_b64_tr_b16 v[182:183], v168 offset:2048
	ds_read_b64_tr_b16 v[184:185], v169
	ds_read_b64_tr_b16 v[186:187], v169 offset:2048
	ds_read_b128 v[188:191], v157 offset:4096
	s_waitcnt lgkmcnt(6)
	v_mfma_f32_16x16x32_bf16 v[18:21], v[160:163], v[172:175], v[18:21]
	v_mfma_f32_16x16x32_bf16 v[22:25], v[164:167], v[172:175], v[22:25]
	s_waitcnt lgkmcnt(3)
	v_mfma_f32_16x16x32_bf16 v[26:29], v[180:183], v[172:175], v[26:29]
	s_waitcnt lgkmcnt(1)
	v_mfma_f32_16x16x32_bf16 v[30:33], v[184:187], v[172:175], v[30:33]
	ds_read_b128 v[172:175], v157 offset:6144
	v_mfma_f32_16x16x32_bf16 v[34:37], v[160:163], v[176:179], v[34:37]
	v_mfma_f32_16x16x32_bf16 v[38:41], v[164:167], v[176:179], v[38:41]
	v_mfma_f32_16x16x32_bf16 v[42:45], v[180:183], v[176:179], v[42:45]
	v_mfma_f32_16x16x32_bf16 v[54:57], v[184:187], v[176:179], v[54:57]
	ds_read_b128 v[176:179], v157 offset:8192
	s_waitcnt lgkmcnt(2)
	v_mfma_f32_16x16x32_bf16 v[66:69], v[160:163], v[188:191], v[66:69]
	v_mfma_f32_16x16x32_bf16 v[78:81], v[164:167], v[188:191], v[78:81]
	v_mfma_f32_16x16x32_bf16 v[90:93], v[180:183], v[188:191], v[90:93]
	v_mfma_f32_16x16x32_bf16 v[94:97], v[184:187], v[188:191], v[94:97]
	ds_read_b128 v[188:191], v157 offset:10240
	s_waitcnt lgkmcnt(2)
	v_mfma_f32_16x16x32_bf16 v[114:117], v[160:163], v[172:175], v[114:117]
	v_mfma_f32_16x16x32_bf16 v[122:125], v[164:167], v[172:175], v[122:125]
	v_mfma_f32_16x16x32_bf16 v[138:141], v[180:183], v[172:175], v[138:141]
	v_mfma_f32_16x16x32_bf16 v[142:145], v[184:187], v[172:175], v[142:145]
	ds_read_b128 v[172:175], v157 offset:12288
	ds_read_b64_tr_b16 v[192:193], v155 offset:16384
	ds_read_b64_tr_b16 v[194:195], v155 offset:18432
	s_waitcnt lgkmcnt(4)
	v_mfma_f32_16x16x32_bf16 v[118:121], v[160:163], v[176:179], v[118:121]
	v_mfma_f32_16x16x32_bf16 v[126:129], v[164:167], v[176:179], v[126:129]
	v_mfma_f32_16x16x32_bf16 v[134:137], v[180:183], v[176:179], v[134:137]
	v_mfma_f32_16x16x32_bf16 v[130:133], v[184:187], v[176:179], v[130:133]
	ds_read_b128 v[176:179], v157 offset:14336
	ds_read_b64_tr_b16 v[196:197], v156 offset:16384
	ds_read_b64_tr_b16 v[198:199], v156 offset:18432
	s_waitcnt lgkmcnt(6)
	v_mfma_f32_16x16x32_bf16 v[98:101], v[160:163], v[188:191], v[98:101]
	v_mfma_f32_16x16x32_bf16 v[102:105], v[164:167], v[188:191], v[102:105]
	v_mfma_f32_16x16x32_bf16 v[110:113], v[180:183], v[188:191], v[110:113]
	v_mfma_f32_16x16x32_bf16 v[106:109], v[184:187], v[188:191], v[106:109]
	v_add_u32_e32 v155, s1, v153
	ds_read_b128 v[188:191], v155
	ds_read_b64_tr_b16 v[216:217], v168 offset:16384
	ds_read_b64_tr_b16 v[218:219], v168 offset:18432
	s_waitcnt lgkmcnt(8)
	v_mfma_f32_16x16x32_bf16 v[70:73], v[160:163], v[172:175], v[70:73]
	v_mfma_f32_16x16x32_bf16 v[82:85], v[164:167], v[172:175], v[82:85]
	v_mfma_f32_16x16x32_bf16 v[86:89], v[180:183], v[172:175], v[86:89]
	v_mfma_f32_16x16x32_bf16 v[74:77], v[184:187], v[172:175], v[74:77]
	s_waitcnt lgkmcnt(5)
	v_mfma_f32_16x16x32_bf16 v[46:49], v[160:163], v[176:179], v[46:49]
	v_mfma_f32_16x16x32_bf16 v[58:61], v[164:167], v[176:179], v[58:61]
	ds_read_b128 v[160:163], v155 offset:2048
	ds_read_b64_tr_b16 v[164:165], v169 offset:16384
	ds_read_b64_tr_b16 v[166:167], v169 offset:18432
	v_mfma_f32_16x16x32_bf16 v[62:65], v[180:183], v[176:179], v[62:65]
	v_mfma_f32_16x16x32_bf16 v[50:53], v[184:187], v[176:179], v[50:53]
	ds_read_b128 v[172:175], v155 offset:4096
	s_add_i32 s0, 0, 0x20000
	s_waitcnt vmcnt(3)
	v_add_u32_e32 v154, s0, v154
	s_waitcnt lgkmcnt(6)
	v_mfma_f32_16x16x32_bf16 v[18:21], v[192:195], v[188:191], v[18:21]
	ds_write_b128 v154, v[14:17]
	v_mfma_f32_16x16x32_bf16 v[22:25], v[196:199], v[188:191], v[22:25]
	s_waitcnt lgkmcnt(5)
	v_mfma_f32_16x16x32_bf16 v[26:29], v[216:219], v[188:191], v[26:29]
	s_waitcnt lgkmcnt(2)
	v_mfma_f32_16x16x32_bf16 v[14:17], v[164:167], v[188:191], v[30:33]
	v_mfma_f32_16x16x32_bf16 v[30:33], v[192:195], v[160:163], v[34:37]
	v_mfma_f32_16x16x32_bf16 v[34:37], v[196:199], v[160:163], v[38:41]
	v_mfma_f32_16x16x32_bf16 v[38:41], v[216:219], v[160:163], v[42:45]
	s_nop 2
	ds_read_b128 v[42:45], v155 offset:6144
	s_waitcnt vmcnt(2)
	ds_write_b128 v154, v[10:13] offset:8192
	v_mfma_f32_16x16x32_bf16 v[10:13], v[164:167], v[160:163], v[54:57]
	s_waitcnt lgkmcnt(3)
	v_mfma_f32_16x16x32_bf16 v[54:57], v[192:195], v[172:175], v[66:69]
	v_mfma_f32_16x16x32_bf16 v[66:69], v[196:199], v[172:175], v[78:81]
	v_mfma_f32_16x16x32_bf16 v[78:81], v[216:219], v[172:175], v[90:93]
	s_nop 2
	ds_read_b128 v[90:93], v155 offset:8192
	s_waitcnt vmcnt(1)
	ds_write_b128 v154, v[6:9] offset:16384
	v_mfma_f32_16x16x32_bf16 v[6:9], v[164:167], v[172:175], v[94:97]
	s_waitcnt lgkmcnt(3)
	v_mfma_f32_16x16x32_bf16 v[94:97], v[192:195], v[42:45], v[114:117]
	v_mfma_f32_16x16x32_bf16 v[114:117], v[196:199], v[42:45], v[122:125]
	v_mfma_f32_16x16x32_bf16 v[122:125], v[216:219], v[42:45], v[138:141]
	s_nop 2
	ds_read_b128 v[138:141], v155 offset:10240
	s_waitcnt vmcnt(0)
	ds_write_b128 v154, v[2:5] offset:24576
	v_mfma_f32_16x16x32_bf16 v[2:5], v[164:167], v[42:45], v[142:145]
	s_waitcnt lgkmcnt(3)
	v_mfma_f32_16x16x32_bf16 v[42:45], v[192:195], v[90:93], v[118:121]
	v_mfma_f32_16x16x32_bf16 v[118:121], v[196:199], v[90:93], v[126:129]
	v_mfma_f32_16x16x32_bf16 v[126:129], v[216:219], v[90:93], v[134:137]
	s_nop 2
	ds_read_b128 v[134:137], v155 offset:12288
	v_mfma_f32_16x16x32_bf16 v[90:93], v[164:167], v[90:93], v[130:133]
	s_nop 2
	ds_read_b128 v[130:133], v155 offset:14336
	s_waitcnt lgkmcnt(3)
	v_mfma_f32_16x16x32_bf16 v[98:101], v[192:195], v[138:141], v[98:101]
	v_mfma_f32_16x16x32_bf16 v[102:105], v[196:199], v[138:141], v[102:105]
	v_mfma_f32_16x16x32_bf16 v[110:113], v[216:219], v[138:141], v[110:113]
	v_mfma_f32_16x16x32_bf16 v[106:109], v[164:167], v[138:141], v[106:109]
	s_waitcnt lgkmcnt(1)
	v_mfma_f32_16x16x32_bf16 v[70:73], v[192:195], v[134:137], v[70:73]
	v_mfma_f32_16x16x32_bf16 v[82:85], v[196:199], v[134:137], v[82:85]
	v_mfma_f32_16x16x32_bf16 v[86:89], v[216:219], v[134:137], v[86:89]
	v_mfma_f32_16x16x32_bf16 v[74:77], v[164:167], v[134:137], v[74:77]
	s_waitcnt lgkmcnt(0)
	v_mfma_f32_16x16x32_bf16 v[46:49], v[192:195], v[130:133], v[46:49]
	v_mfma_f32_16x16x32_bf16 v[58:61], v[196:199], v[130:133], v[58:61]
	v_mfma_f32_16x16x32_bf16 v[62:65], v[216:219], v[130:133], v[62:65]
	v_mfma_f32_16x16x32_bf16 v[50:53], v[164:167], v[130:133], v[50:53]
	s_waitcnt lgkmcnt(0)
	s_barrier
	v_add_u32_e32 v152, s0, v152
	v_add_u32_e32 v169, 0, v150
	v_add_u32_e32 v200, s0, v149
	v_add_u32_e32 v201, s0, v148
	v_add_u32_e32 v168, s0, v151
	ds_read_b64_tr_b16 v[130:131], v152
	ds_read_b64_tr_b16 v[132:133], v152 offset:2048
	ds_read_b64_tr_b16 v[134:135], v168
	ds_read_b64_tr_b16 v[136:137], v168 offset:2048
	ds_read_b128 v[138:141], v169
	ds_read_b128 v[142:145], v169 offset:2048
	ds_read_b64_tr_b16 v[154:155], v200
	ds_read_b64_tr_b16 v[156:157], v200 offset:2048
	ds_read_b64_tr_b16 v[148:149], v201
	ds_read_b64_tr_b16 v[150:151], v201 offset:2048
	ds_read_b128 v[160:163], v169 offset:4096
	s_waitcnt lgkmcnt(6)
	v_mfma_f32_16x16x32_bf16 v[18:21], v[130:133], v[138:141], v[18:21]
	v_mfma_f32_16x16x32_bf16 v[22:25], v[134:137], v[138:141], v[22:25]
	s_waitcnt lgkmcnt(3)
	v_mfma_f32_16x16x32_bf16 v[26:29], v[154:157], v[138:141], v[26:29]
	s_waitcnt lgkmcnt(1)
	v_mfma_f32_16x16x32_bf16 v[14:17], v[148:151], v[138:141], v[14:17]
	ds_read_b128 v[138:141], v169 offset:6144
	v_mfma_f32_16x16x32_bf16 v[10:13], v[148:151], v[142:145], v[10:13]
	v_mfma_f32_16x16x32_bf16 v[30:33], v[130:133], v[142:145], v[30:33]
	v_mfma_f32_16x16x32_bf16 v[34:37], v[134:137], v[142:145], v[34:37]
	v_mfma_f32_16x16x32_bf16 v[38:41], v[154:157], v[142:145], v[38:41]
	ds_read_b128 v[142:145], v169 offset:8192
	s_waitcnt lgkmcnt(2)
	v_mfma_f32_16x16x32_bf16 v[6:9], v[148:151], v[160:163], v[6:9]
	v_mfma_f32_16x16x32_bf16 v[54:57], v[130:133], v[160:163], v[54:57]
	v_mfma_f32_16x16x32_bf16 v[66:69], v[134:137], v[160:163], v[66:69]
	v_mfma_f32_16x16x32_bf16 v[78:81], v[154:157], v[160:163], v[78:81]
	s_waitcnt lgkmcnt(1)
	v_mfma_f32_16x16x32_bf16 v[160:163], v[134:137], v[138:141], v[114:117]
	s_nop 2
	ds_read_b128 v[114:117], v169 offset:10240
	v_mfma_f32_16x16x32_bf16 v[2:5], v[148:151], v[138:141], v[2:5]
	v_mfma_f32_16x16x32_bf16 v[94:97], v[130:133], v[138:141], v[94:97]
	v_mfma_f32_16x16x32_bf16 v[164:167], v[154:157], v[138:141], v[122:125]
	s_waitcnt lgkmcnt(1)
	v_mfma_f32_16x16x32_bf16 v[138:141], v[134:137], v[142:145], v[118:121]
	s_nop 2
	ds_read_b128 v[118:121], v169 offset:12288
	ds_read_b64_tr_b16 v[176:177], v152 offset:16384
	ds_read_b64_tr_b16 v[178:179], v152 offset:18432
	v_mfma_f32_16x16x32_bf16 v[42:45], v[130:133], v[142:145], v[42:45]
	v_mfma_f32_16x16x32_bf16 v[172:175], v[154:157], v[142:145], v[126:129]
	v_mfma_f32_16x16x32_bf16 v[142:145], v[148:151], v[142:145], v[90:93]
	s_nop 2
	ds_read_b128 v[90:93], v169 offset:14336
	ds_read_b64_tr_b16 v[192:193], v168 offset:16384
	ds_read_b64_tr_b16 v[194:195], v168 offset:18432
	s_waitcnt lgkmcnt(6)
	v_mfma_f32_16x16x32_bf16 v[180:183], v[130:133], v[114:117], v[98:101]
	v_mfma_f32_16x16x32_bf16 v[184:187], v[134:137], v[114:117], v[102:105]
	v_mfma_f32_16x16x32_bf16 v[188:191], v[154:157], v[114:117], v[110:113]
	v_mfma_f32_16x16x32_bf16 v[196:199], v[148:151], v[114:117], v[106:109]
	v_add_u32_e32 v168, 0, v153
	s_waitcnt lgkmcnt(5)
	v_mfma_f32_16x16x32_bf16 v[216:219], v[130:133], v[118:121], v[70:73]
	s_nop 2
	ds_read_b128 v[70:73], v168
	ds_read_b64_tr_b16 v[228:229], v200 offset:16384
	ds_read_b64_tr_b16 v[230:231], v200 offset:18432
	v_mfma_f32_16x16x32_bf16 v[220:223], v[134:137], v[118:121], v[82:85]
	v_mfma_f32_16x16x32_bf16 v[224:227], v[154:157], v[118:121], v[86:89]
	v_mfma_f32_16x16x32_bf16 v[232:235], v[148:151], v[118:121], v[74:77]
	s_waitcnt lgkmcnt(5)
	v_mfma_f32_16x16x32_bf16 v[236:239], v[130:133], v[90:93], v[46:49]
	s_nop 2
	ds_read_b128 v[46:49], v168 offset:2048
	ds_read_b64_tr_b16 v[244:245], v201 offset:16384
	ds_read_b64_tr_b16 v[246:247], v201 offset:18432
	v_mfma_f32_16x16x32_bf16 v[240:243], v[134:137], v[90:93], v[58:61]
	v_mfma_f32_16x16x32_bf16 v[152:155], v[154:157], v[90:93], v[62:65]
	v_mfma_f32_16x16x32_bf16 v[148:151], v[148:151], v[90:93], v[50:53]
	s_waitcnt lgkmcnt(5)
	v_mfma_f32_16x16x32_bf16 v[248:251], v[176:179], v[70:73], v[18:21]
	s_nop 2
	ds_read_b128 v[18:21], v168 offset:4096
	v_mfma_f32_16x16x32_bf16 v[202:205], v[192:195], v[70:73], v[22:25]
	s_waitcnt lgkmcnt(4)
	v_mfma_f32_16x16x32_bf16 v[134:137], v[228:231], v[70:73], v[26:29]
	s_waitcnt lgkmcnt(1)
	v_mfma_f32_16x16x32_bf16 v[130:133], v[244:247], v[70:73], v[14:17]
	s_nop 2
	ds_read_b128 v[14:17], v168 offset:6144
	v_mfma_f32_16x16x32_bf16 v[126:129], v[176:179], v[46:49], v[30:33]
	v_mfma_f32_16x16x32_bf16 v[122:125], v[192:195], v[46:49], v[34:37]
	v_mfma_f32_16x16x32_bf16 v[118:121], v[228:231], v[46:49], v[38:41]
	v_mfma_f32_16x16x32_bf16 v[114:117], v[244:247], v[46:49], v[10:13]
	s_nop 2
	ds_read_b128 v[10:13], v168 offset:8192
	s_waitcnt lgkmcnt(2)
	v_mfma_f32_16x16x32_bf16 v[110:113], v[176:179], v[18:21], v[54:57]
	v_mfma_f32_16x16x32_bf16 v[106:109], v[192:195], v[18:21], v[66:69]
	v_mfma_f32_16x16x32_bf16 v[102:105], v[228:231], v[18:21], v[78:81]
	v_mfma_f32_16x16x32_bf16 v[98:101], v[244:247], v[18:21], v[6:9]
	s_nop 2
	ds_read_b128 v[6:9], v168 offset:10240
	s_waitcnt lgkmcnt(2)
	v_mfma_f32_16x16x32_bf16 v[94:97], v[176:179], v[14:17], v[94:97]
	v_mfma_f32_16x16x32_bf16 v[90:93], v[192:195], v[14:17], v[160:163]
	v_mfma_f32_16x16x32_bf16 v[86:89], v[228:231], v[14:17], v[164:167]
	v_mfma_f32_16x16x32_bf16 v[82:85], v[244:247], v[14:17], v[2:5]
	s_nop 2
	ds_read_b128 v[2:5], v168 offset:12288
	s_waitcnt lgkmcnt(2)
	v_mfma_f32_16x16x32_bf16 v[78:81], v[176:179], v[10:13], v[42:45]
	v_mfma_f32_16x16x32_bf16 v[74:77], v[192:195], v[10:13], v[138:141]
	v_mfma_f32_16x16x32_bf16 v[70:73], v[228:231], v[10:13], v[172:175]
	v_mfma_f32_16x16x32_bf16 v[66:69], v[244:247], v[10:13], v[142:145]
	ds_read_b128 v[14:17], v168 offset:14336
	s_waitcnt lgkmcnt(2)
	v_mfma_f32_16x16x32_bf16 v[62:65], v[176:179], v[6:9], v[180:183]
	v_mfma_f32_16x16x32_bf16 v[58:61], v[192:195], v[6:9], v[184:187]
	v_mfma_f32_16x16x32_bf16 v[54:57], v[228:231], v[6:9], v[188:191]
	v_mfma_f32_16x16x32_bf16 v[50:53], v[244:247], v[6:9], v[196:199]
	s_waitcnt lgkmcnt(1)
	v_mfma_f32_16x16x32_bf16 v[46:49], v[176:179], v[2:5], v[216:219]
	v_mfma_f32_16x16x32_bf16 v[42:45], v[192:195], v[2:5], v[220:223]
	v_mfma_f32_16x16x32_bf16 v[38:41], v[228:231], v[2:5], v[224:227]
	v_mfma_f32_16x16x32_bf16 v[34:37], v[244:247], v[2:5], v[232:235]
	s_waitcnt lgkmcnt(0)
	v_mfma_f32_16x16x32_bf16 v[10:13], v[228:231], v[14:17], v[152:155]
	v_mfma_f32_16x16x32_bf16 v[2:5], v[244:247], v[14:17], v[148:151]
	v_mfma_f32_16x16x32_bf16 v[26:29], v[176:179], v[14:17], v[236:239]
	v_mfma_f32_16x16x32_bf16 v[18:21], v[192:195], v[14:17], v[240:243]
	s_lshl_b32 s0, s26, 6
	v_mov_b32_e32 v144, v1
	v_mov_b32_e32 v145, v252
	s_or_b32 s0, s0, s22
	s_waitcnt lgkmcnt(0)
	s_barrier
	s_add_i32 s24, s24, 0
	v_lshl_add_u32 v6, v145, 2, s0
	s_add_i32 s0, s25, s21
	v_add_u32_e32 v138, s0, v144
	v_ashrrev_i32_e32 v139, 31, v138
	v_ashrrev_i32_e32 v7, 31, v6
	v_lshlrev_b64 v[8:9], 11, v[138:139]
	v_lshl_add_u64 v[8:9], s[6:7], 0, v[8:9]
	v_lshlrev_b64 v[140:141], 1, v[6:7]
	v_lshl_add_u64 v[142:143], v[8:9], 0, v[140:141]
	v_lshl_add_u64 v[6:7], v[6:7], 2, s[94:95]
	global_load_dwordx2 v[216:217], v[142:143], off
	global_load_dwordx4 v[30:33], v[6:7], off
	global_load_dwordx4 v[22:25], v[6:7], off offset:64
	global_load_dwordx4 v[14:17], v[6:7], off offset:128
	s_nop 0
	global_load_dwordx4 v[6:9], v[6:7], off offset:192
	s_nop 0
	global_load_dwordx2 v[218:219], v[142:143], off offset:32
	global_load_dwordx2 v[220:221], v[142:143], off offset:64
	global_load_dwordx2 v[200:201], v[142:143], off offset:96
	v_add_u32_e32 v142, 16, v138
	v_ashrrev_i32_e32 v143, 31, v142
	v_lshlrev_b64 v[142:143], 11, v[142:143]
	v_lshl_add_u64 v[142:143], s[6:7], 0, v[142:143]
	v_lshl_add_u64 v[142:143], v[142:143], 0, v[140:141]
	global_load_dwordx2 v[198:199], v[142:143], off
	global_load_dwordx2 v[196:197], v[142:143], off offset:32
	global_load_dwordx2 v[194:195], v[142:143], off offset:64
	global_load_dwordx2 v[192:193], v[142:143], off offset:96
	v_add_u32_e32 v142, 32, v138
	v_ashrrev_i32_e32 v143, 31, v142
	v_lshlrev_b64 v[142:143], 11, v[142:143]
	v_lshl_add_u64 v[142:143], s[6:7], 0, v[142:143]
	v_lshl_add_u64 v[142:143], v[142:143], 0, v[140:141]
	global_load_dwordx2 v[190:191], v[142:143], off
	global_load_dwordx2 v[188:189], v[142:143], off offset:32
	global_load_dwordx2 v[186:187], v[142:143], off offset:64
	global_load_dwordx2 v[184:185], v[142:143], off offset:96
	v_add_u32_e32 v142, 48, v138
	v_ashrrev_i32_e32 v143, 31, v142
	v_lshlrev_b64 v[142:143], 11, v[142:143]
	v_lshl_add_u64 v[142:143], s[6:7], 0, v[142:143]
	v_lshl_add_u64 v[142:143], v[142:143], 0, v[140:141]
	global_load_dwordx2 v[182:183], v[142:143], off
	global_load_dwordx2 v[180:181], v[142:143], off offset:32
	global_load_dwordx2 v[178:179], v[142:143], off offset:64
	global_load_dwordx2 v[176:177], v[142:143], off offset:96
	v_add_u32_e32 v142, 64, v138
	v_ashrrev_i32_e32 v143, 31, v142
	v_lshlrev_b64 v[142:143], 11, v[142:143]
	v_lshl_add_u64 v[142:143], s[6:7], 0, v[142:143]
	v_lshl_add_u64 v[142:143], v[142:143], 0, v[140:141]
	global_load_dwordx2 v[174:175], v[142:143], off
	global_load_dwordx2 v[172:173], v[142:143], off offset:32
	global_load_dwordx2 v[168:169], v[142:143], off offset:64
	global_load_dwordx2 v[166:167], v[142:143], off offset:96
	v_add_u32_e32 v142, 0x50, v138
	v_ashrrev_i32_e32 v143, 31, v142
	v_lshlrev_b64 v[142:143], 11, v[142:143]
	v_lshl_add_u64 v[142:143], s[6:7], 0, v[142:143]
	v_lshl_add_u64 v[142:143], v[142:143], 0, v[140:141]
	global_load_dwordx2 v[164:165], v[142:143], off
	global_load_dwordx2 v[162:163], v[142:143], off offset:32
	global_load_dwordx2 v[160:161], v[142:143], off offset:64
	global_load_dwordx2 v[156:157], v[142:143], off offset:96
	v_add_u32_e32 v215, s25, v144
	v_lshlrev_b32_e32 v222, 3, v145
	v_mul_lo_u32 v215, v215, s18
	v_add3_u32 v215, s24, v222, v215
	v_add_u32_e32 v142, 0x60, v138
	v_add_u32_e32 v138, 0x70, v138
	v_ashrrev_i32_e32 v143, 31, v142
	v_ashrrev_i32_e32 v139, 31, v138
	v_lshlrev_b64 v[142:143], 11, v[142:143]
	v_lshlrev_b64 v[138:139], 11, v[138:139]
	v_lshl_add_u64 v[142:143], s[6:7], 0, v[142:143]
	v_lshl_add_u64 v[138:139], s[6:7], 0, v[138:139]
	v_lshl_add_u64 v[142:143], v[142:143], 0, v[140:141]
	v_lshl_add_u64 v[138:139], v[138:139], 0, v[140:141]
	global_load_dwordx2 v[154:155], v[142:143], off
	global_load_dwordx2 v[152:153], v[142:143], off offset:32
	global_load_dwordx2 v[150:151], v[142:143], off offset:64
	global_load_dwordx2 v[148:149], v[142:143], off offset:96
	global_load_dwordx2 v[144:145], v[138:139], off
	s_nop 0
	global_load_dwordx2 v[142:143], v[138:139], off offset:32
	global_load_dwordx2 v[140:141], v[138:139], off offset:64
	s_nop 0
	global_load_dwordx2 v[138:139], v[138:139], off offset:96
	s_lshl_b32 s2, s22, 1
	s_waitcnt vmcnt(34)
	v_pk_add_f32 v[224:225], v[250:251], v[32:33]
	v_pk_add_f32 v[226:227], v[248:249], v[30:31]
	v_pk_mul_f32 v[224:225], v[224:225], s[14:15] op_sel_hi:[1,0]
	v_pk_mul_f32 v[226:227], v[226:227], s[14:15] op_sel_hi:[1,0]
	v_exp_f32_e32 v224, v224
	v_exp_f32_e32 v226, v226
	v_exp_f32_e32 v227, v227
	v_exp_f32_e32 v225, v225
	s_waitcnt vmcnt(33)
	v_pk_add_f32 v[202:203], v[202:203], v[22:23]
	v_pk_add_f32 v[204:205], v[204:205], v[24:25]
	v_pk_mul_f32 v[202:203], v[202:203], s[14:15] op_sel_hi:[1,0]
	v_pk_mul_f32 v[204:205], v[204:205], s[14:15] op_sel_hi:[1,0]
	v_exp_f32_e32 v202, v202
	v_exp_f32_e32 v203, v203
	v_exp_f32_e32 v204, v204
	v_exp_f32_e32 v205, v205
	v_pk_add_f32 v[226:227], v[226:227], 1.0 op_sel_hi:[1,0]
	v_pk_add_f32 v[224:225], v[224:225], 1.0 op_sel_hi:[1,0]
	s_waitcnt vmcnt(32)
	v_pk_add_f32 v[134:135], v[134:135], v[14:15]
	v_rcp_f32_e32 v226, v226
	v_rcp_f32_e32 v227, v227
	v_rcp_f32_e32 v224, v224
	v_rcp_f32_e32 v225, v225
	v_pk_add_f32 v[136:137], v[136:137], v[16:17]
	v_pk_mul_f32 v[134:135], v[134:135], s[14:15] op_sel_hi:[1,0]
	v_pk_add_f32 v[202:203], v[202:203], 1.0 op_sel_hi:[1,0]
	v_exp_f32_e32 v134, v134
	v_exp_f32_e32 v135, v135
	v_pk_mul_f32 v[136:137], v[136:137], s[14:15] op_sel_hi:[1,0]
	v_rcp_f32_e32 v202, v202
	v_rcp_f32_e32 v203, v203
	v_pk_add_f32 v[204:205], v[204:205], 1.0 op_sel_hi:[1,0]
	v_exp_f32_e32 v136, v136
	v_exp_f32_e32 v137, v137
	s_waitcnt vmcnt(31)
	v_pk_add_f32 v[130:131], v[130:131], v[6:7]
	v_lshlrev_b32_e32 v222, 16, v216
	v_and_b32_e32 v223, 0xffff0000, v216
	v_lshlrev_b32_e32 v216, 16, v217
	v_and_b32_e32 v217, 0xffff0000, v217
	v_rcp_f32_e32 v204, v204
	v_rcp_f32_e32 v205, v205
	v_pk_add_f32 v[132:133], v[132:133], v[8:9]
	v_pk_mul_f32 v[130:131], v[130:131], s[14:15] op_sel_hi:[1,0]
	v_pk_mul_f32 v[222:223], v[226:227], v[222:223]
	v_pk_mul_f32 v[216:217], v[224:225], v[216:217]
	v_exp_f32_e32 v130, v130
	v_exp_f32_e32 v131, v131
	v_pk_mul_f32 v[132:133], v[132:133], s[14:15] op_sel_hi:[1,0]
	v_cvt_pk_bf16_f32 v222, v222, v223
	v_cvt_pk_bf16_f32 v223, v216, v217
	s_waitcnt vmcnt(30)
	v_lshlrev_b32_e32 v216, 16, v218
	v_and_b32_e32 v217, 0xffff0000, v218
	v_pk_add_f32 v[134:135], v[134:135], 1.0 op_sel_hi:[1,0]
	v_exp_f32_e32 v132, v132
	v_exp_f32_e32 v133, v133
	v_pk_mul_f32 v[202:203], v[202:203], v[216:217]
	v_lshlrev_b32_e32 v216, 16, v219
	v_and_b32_e32 v217, 0xffff0000, v219
	v_rcp_f32_e32 v134, v134
	v_rcp_f32_e32 v135, v135
	v_pk_add_f32 v[136:137], v[136:137], 1.0 op_sel_hi:[1,0]
	v_pk_add_f32 v[126:127], v[126:127], v[30:31]
	v_pk_mul_f32 v[204:205], v[204:205], v[216:217]
	v_rcp_f32_e32 v136, v136
	v_rcp_f32_e32 v137, v137
	v_pk_add_f32 v[128:129], v[128:129], v[32:33]
	v_pk_mul_f32 v[126:127], v[126:127], s[14:15] op_sel_hi:[1,0]
	v_cvt_pk_bf16_f32 v202, v202, v203
	v_cvt_pk_bf16_f32 v203, v204, v205
	v_pk_add_f32 v[130:131], v[130:131], 1.0 op_sel_hi:[1,0]
	v_exp_f32_e32 v126, v126
	v_exp_f32_e32 v127, v127
	v_pk_mul_f32 v[128:129], v[128:129], s[14:15] op_sel_hi:[1,0]
	ds_write2_b64 v215, v[222:223], v[202:203] offset1:4
	s_waitcnt vmcnt(29)
	v_lshlrev_b32_e32 v202, 16, v220
	v_and_b32_e32 v203, 0xffff0000, v220
	v_rcp_f32_e32 v130, v130
	v_rcp_f32_e32 v131, v131
	v_pk_add_f32 v[132:133], v[132:133], 1.0 op_sel_hi:[1,0]
	v_exp_f32_e32 v128, v128
	v_exp_f32_e32 v129, v129
	v_pk_add_f32 v[122:123], v[122:123], v[22:23]
	v_pk_mul_f32 v[134:135], v[134:135], v[202:203]
	v_lshlrev_b32_e32 v202, 16, v221
	v_and_b32_e32 v203, 0xffff0000, v221
	v_rcp_f32_e32 v132, v132
	v_rcp_f32_e32 v133, v133
	v_pk_add_f32 v[124:125], v[124:125], v[24:25]
	v_pk_mul_f32 v[122:123], v[122:123], s[14:15] op_sel_hi:[1,0]
	v_pk_mul_f32 v[136:137], v[136:137], v[202:203]
	v_exp_f32_e32 v122, v122
	v_exp_f32_e32 v123, v123
	v_pk_mul_f32 v[124:125], v[124:125], s[14:15] op_sel_hi:[1,0]
	v_cvt_pk_bf16_f32 v134, v134, v135
	v_cvt_pk_bf16_f32 v135, v136, v137
	s_waitcnt vmcnt(28)
	v_lshlrev_b32_e32 v136, 16, v200
	v_and_b32_e32 v137, 0xffff0000, v200
	v_pk_add_f32 v[126:127], v[126:127], 1.0 op_sel_hi:[1,0]
	v_exp_f32_e32 v124, v124
	v_exp_f32_e32 v125, v125
	v_pk_mul_f32 v[130:131], v[130:131], v[136:137]
	v_lshlrev_b32_e32 v136, 16, v201
	v_and_b32_e32 v137, 0xffff0000, v201
	v_rcp_f32_e32 v126, v126
	v_rcp_f32_e32 v127, v127
	v_pk_add_f32 v[128:129], v[128:129], 1.0 op_sel_hi:[1,0]
	v_pk_add_f32 v[118:119], v[118:119], v[14:15]
	v_pk_mul_f32 v[132:133], v[132:133], v[136:137]
	v_rcp_f32_e32 v128, v128
	v_rcp_f32_e32 v129, v129
	v_pk_add_f32 v[120:121], v[120:121], v[16:17]
	v_pk_mul_f32 v[118:119], v[118:119], s[14:15] op_sel_hi:[1,0]
	v_cvt_pk_bf16_f32 v130, v130, v131
	v_cvt_pk_bf16_f32 v131, v132, v133
	v_pk_add_f32 v[122:123], v[122:123], 1.0 op_sel_hi:[1,0]
	v_exp_f32_e32 v118, v118
	v_exp_f32_e32 v119, v119
	v_pk_mul_f32 v[120:121], v[120:121], s[14:15] op_sel_hi:[1,0]
	ds_write2_b64 v215, v[134:135], v[130:131] offset0:8 offset1:12
	s_waitcnt vmcnt(27)
	v_lshlrev_b32_e32 v130, 16, v198
	v_and_b32_e32 v131, 0xffff0000, v198
	v_rcp_f32_e32 v122, v122
	v_rcp_f32_e32 v123, v123
	v_pk_add_f32 v[124:125], v[124:125], 1.0 op_sel_hi:[1,0]
	v_exp_f32_e32 v120, v120
	v_exp_f32_e32 v121, v121
	v_pk_add_f32 v[114:115], v[114:115], v[6:7]
	v_pk_mul_f32 v[126:127], v[126:127], v[130:131]
	v_lshlrev_b32_e32 v130, 16, v199
	v_and_b32_e32 v131, 0xffff0000, v199
	v_rcp_f32_e32 v124, v124
	v_rcp_f32_e32 v125, v125
	v_pk_add_f32 v[116:117], v[116:117], v[8:9]
	v_pk_mul_f32 v[114:115], v[114:115], s[14:15] op_sel_hi:[1,0]
	v_pk_mul_f32 v[128:129], v[128:129], v[130:131]
	v_exp_f32_e32 v114, v114
	v_exp_f32_e32 v115, v115
	v_pk_mul_f32 v[116:117], v[116:117], s[14:15] op_sel_hi:[1,0]
	v_cvt_pk_bf16_f32 v126, v126, v127
	v_cvt_pk_bf16_f32 v127, v128, v129
	s_waitcnt vmcnt(26)
	v_lshlrev_b32_e32 v128, 16, v196
	v_and_b32_e32 v129, 0xffff0000, v196
	v_pk_add_f32 v[118:119], v[118:119], 1.0 op_sel_hi:[1,0]
	v_exp_f32_e32 v116, v116
	v_exp_f32_e32 v117, v117
	v_pk_mul_f32 v[122:123], v[122:123], v[128:129]
	v_lshlrev_b32_e32 v128, 16, v197
	v_and_b32_e32 v129, 0xffff0000, v197
	v_rcp_f32_e32 v118, v118
	v_rcp_f32_e32 v119, v119
	v_pk_add_f32 v[120:121], v[120:121], 1.0 op_sel_hi:[1,0]
	v_pk_add_f32 v[110:111], v[110:111], v[30:31]
	v_pk_mul_f32 v[124:125], v[124:125], v[128:129]
	v_rcp_f32_e32 v120, v120
	v_rcp_f32_e32 v121, v121
	v_pk_add_f32 v[112:113], v[112:113], v[32:33]
	v_pk_mul_f32 v[110:111], v[110:111], s[14:15] op_sel_hi:[1,0]
	v_cvt_pk_bf16_f32 v122, v122, v123
	v_cvt_pk_bf16_f32 v123, v124, v125
	v_add_u32_e32 v124, 0x2000, v215
	v_pk_add_f32 v[114:115], v[114:115], 1.0 op_sel_hi:[1,0]
	v_exp_f32_e32 v110, v110
	v_exp_f32_e32 v111, v111
	v_pk_mul_f32 v[112:113], v[112:113], s[14:15] op_sel_hi:[1,0]
	ds_write2_b64 v124, v[126:127], v[122:123] offset0:32 offset1:36
	s_waitcnt vmcnt(25)
	v_lshlrev_b32_e32 v122, 16, v194
	v_and_b32_e32 v123, 0xffff0000, v194
	v_rcp_f32_e32 v114, v114
	v_rcp_f32_e32 v115, v115
	v_pk_add_f32 v[116:117], v[116:117], 1.0 op_sel_hi:[1,0]
	v_exp_f32_e32 v112, v112
	v_exp_f32_e32 v113, v113
	v_pk_add_f32 v[106:107], v[106:107], v[22:23]
	v_pk_mul_f32 v[118:119], v[118:119], v[122:123]
	v_lshlrev_b32_e32 v122, 16, v195
	v_and_b32_e32 v123, 0xffff0000, v195
	v_rcp_f32_e32 v116, v116
	v_rcp_f32_e32 v117, v117
	v_pk_add_f32 v[108:109], v[108:109], v[24:25]
	v_pk_mul_f32 v[106:107], v[106:107], s[14:15] op_sel_hi:[1,0]
	v_pk_mul_f32 v[120:121], v[120:121], v[122:123]
	v_exp_f32_e32 v106, v106
	v_exp_f32_e32 v107, v107
	v_pk_mul_f32 v[108:109], v[108:109], s[14:15] op_sel_hi:[1,0]
	v_cvt_pk_bf16_f32 v118, v118, v119
	v_cvt_pk_bf16_f32 v119, v120, v121
	s_waitcnt vmcnt(24)
	v_lshlrev_b32_e32 v120, 16, v192
	v_and_b32_e32 v121, 0xffff0000, v192
	v_pk_add_f32 v[110:111], v[110:111], 1.0 op_sel_hi:[1,0]
	v_exp_f32_e32 v108, v108
	v_exp_f32_e32 v109, v109
	v_pk_mul_f32 v[114:115], v[114:115], v[120:121]
	v_lshlrev_b32_e32 v120, 16, v193
	v_and_b32_e32 v121, 0xffff0000, v193
	v_rcp_f32_e32 v110, v110
	v_rcp_f32_e32 v111, v111
	v_pk_add_f32 v[112:113], v[112:113], 1.0 op_sel_hi:[1,0]
	v_pk_add_f32 v[102:103], v[102:103], v[14:15]
	v_pk_mul_f32 v[116:117], v[116:117], v[120:121]
	v_rcp_f32_e32 v112, v112
	v_rcp_f32_e32 v113, v113
	v_pk_add_f32 v[104:105], v[104:105], v[16:17]
	v_pk_mul_f32 v[102:103], v[102:103], s[14:15] op_sel_hi:[1,0]
	v_cvt_pk_bf16_f32 v114, v114, v115
	v_cvt_pk_bf16_f32 v115, v116, v117
	v_pk_add_f32 v[106:107], v[106:107], 1.0 op_sel_hi:[1,0]
	v_exp_f32_e32 v102, v102
	v_exp_f32_e32 v103, v103
	v_pk_mul_f32 v[104:105], v[104:105], s[14:15] op_sel_hi:[1,0]
	ds_write2_b64 v124, v[118:119], v[114:115] offset0:40 offset1:44
	s_waitcnt vmcnt(23)
	v_lshlrev_b32_e32 v114, 16, v190
	v_and_b32_e32 v115, 0xffff0000, v190
	v_rcp_f32_e32 v106, v106
	v_rcp_f32_e32 v107, v107
	v_pk_add_f32 v[108:109], v[108:109], 1.0 op_sel_hi:[1,0]
	v_exp_f32_e32 v104, v104
	v_exp_f32_e32 v105, v105
	v_pk_add_f32 v[98:99], v[98:99], v[6:7]
	v_pk_mul_f32 v[110:111], v[110:111], v[114:115]
	v_lshlrev_b32_e32 v114, 16, v191
	v_and_b32_e32 v115, 0xffff0000, v191
	v_rcp_f32_e32 v108, v108
	v_rcp_f32_e32 v109, v109
	v_pk_add_f32 v[100:101], v[100:101], v[8:9]
	v_pk_mul_f32 v[98:99], v[98:99], s[14:15] op_sel_hi:[1,0]
	v_pk_mul_f32 v[112:113], v[112:113], v[114:115]
	v_exp_f32_e32 v98, v98
	v_exp_f32_e32 v99, v99
	v_pk_mul_f32 v[100:101], v[100:101], s[14:15] op_sel_hi:[1,0]
	v_cvt_pk_bf16_f32 v110, v110, v111
	v_cvt_pk_bf16_f32 v111, v112, v113
	s_waitcnt vmcnt(22)
	v_lshlrev_b32_e32 v112, 16, v188
	v_and_b32_e32 v113, 0xffff0000, v188
	v_pk_add_f32 v[102:103], v[102:103], 1.0 op_sel_hi:[1,0]
	v_exp_f32_e32 v100, v100
	v_exp_f32_e32 v101, v101
	v_pk_mul_f32 v[106:107], v[106:107], v[112:113]
	v_lshlrev_b32_e32 v112, 16, v189
	v_and_b32_e32 v113, 0xffff0000, v189
	v_rcp_f32_e32 v102, v102
	v_rcp_f32_e32 v103, v103
	v_pk_add_f32 v[104:105], v[104:105], 1.0 op_sel_hi:[1,0]
	v_pk_add_f32 v[94:95], v[94:95], v[30:31]
	v_pk_mul_f32 v[108:109], v[108:109], v[112:113]
	v_rcp_f32_e32 v104, v104
	v_rcp_f32_e32 v105, v105
	v_pk_add_f32 v[96:97], v[96:97], v[32:33]
	v_pk_mul_f32 v[94:95], v[94:95], s[14:15] op_sel_hi:[1,0]
	v_cvt_pk_bf16_f32 v106, v106, v107
	v_cvt_pk_bf16_f32 v107, v108, v109
	v_add_u32_e32 v108, 0x4000, v215
	v_pk_add_f32 v[98:99], v[98:99], 1.0 op_sel_hi:[1,0]
	v_exp_f32_e32 v94, v94
	v_exp_f32_e32 v95, v95
	v_pk_mul_f32 v[96:97], v[96:97], s[14:15] op_sel_hi:[1,0]
	ds_write2_b64 v108, v[110:111], v[106:107] offset0:64 offset1:68
	s_waitcnt vmcnt(21)
	v_lshlrev_b32_e32 v106, 16, v186
	v_and_b32_e32 v107, 0xffff0000, v186
	v_rcp_f32_e32 v98, v98
	v_rcp_f32_e32 v99, v99
	v_pk_add_f32 v[100:101], v[100:101], 1.0 op_sel_hi:[1,0]
	v_exp_f32_e32 v96, v96
	v_exp_f32_e32 v97, v97
	v_pk_add_f32 v[90:91], v[90:91], v[22:23]
	v_pk_mul_f32 v[102:103], v[102:103], v[106:107]
	v_lshlrev_b32_e32 v106, 16, v187
	v_and_b32_e32 v107, 0xffff0000, v187
	v_rcp_f32_e32 v100, v100
	v_rcp_f32_e32 v101, v101
	v_pk_add_f32 v[92:93], v[92:93], v[24:25]
	v_pk_mul_f32 v[90:91], v[90:91], s[14:15] op_sel_hi:[1,0]
	v_pk_mul_f32 v[104:105], v[104:105], v[106:107]
	v_exp_f32_e32 v90, v90
	v_exp_f32_e32 v91, v91
	v_pk_mul_f32 v[92:93], v[92:93], s[14:15] op_sel_hi:[1,0]
	v_cvt_pk_bf16_f32 v102, v102, v103
	v_cvt_pk_bf16_f32 v103, v104, v105
	s_waitcnt vmcnt(20)
	v_lshlrev_b32_e32 v104, 16, v184
	v_and_b32_e32 v105, 0xffff0000, v184
	v_pk_add_f32 v[94:95], v[94:95], 1.0 op_sel_hi:[1,0]
	v_exp_f32_e32 v92, v92
	v_exp_f32_e32 v93, v93
	v_pk_mul_f32 v[98:99], v[98:99], v[104:105]
	v_lshlrev_b32_e32 v104, 16, v185
	v_and_b32_e32 v105, 0xffff0000, v185
	v_rcp_f32_e32 v94, v94
	v_rcp_f32_e32 v95, v95
	v_pk_add_f32 v[96:97], v[96:97], 1.0 op_sel_hi:[1,0]
	v_pk_add_f32 v[86:87], v[86:87], v[14:15]
	v_pk_mul_f32 v[100:101], v[100:101], v[104:105]
	v_rcp_f32_e32 v96, v96
	v_rcp_f32_e32 v97, v97
	v_pk_add_f32 v[88:89], v[88:89], v[16:17]
	v_pk_mul_f32 v[86:87], v[86:87], s[14:15] op_sel_hi:[1,0]
	v_cvt_pk_bf16_f32 v98, v98, v99
	v_cvt_pk_bf16_f32 v99, v100, v101
	v_pk_add_f32 v[90:91], v[90:91], 1.0 op_sel_hi:[1,0]
	v_exp_f32_e32 v86, v86
	v_exp_f32_e32 v87, v87
	v_pk_mul_f32 v[88:89], v[88:89], s[14:15] op_sel_hi:[1,0]
	ds_write2_b64 v108, v[102:103], v[98:99] offset0:72 offset1:76
	s_waitcnt vmcnt(19)
	v_lshlrev_b32_e32 v98, 16, v182
	v_and_b32_e32 v99, 0xffff0000, v182
	v_rcp_f32_e32 v90, v90
	v_rcp_f32_e32 v91, v91
	v_pk_add_f32 v[92:93], v[92:93], 1.0 op_sel_hi:[1,0]
	v_exp_f32_e32 v88, v88
	v_exp_f32_e32 v89, v89
	v_pk_add_f32 v[82:83], v[82:83], v[6:7]
	v_pk_mul_f32 v[94:95], v[94:95], v[98:99]
	v_lshlrev_b32_e32 v98, 16, v183
	v_and_b32_e32 v99, 0xffff0000, v183
	v_rcp_f32_e32 v92, v92
	v_rcp_f32_e32 v93, v93
	v_pk_add_f32 v[84:85], v[84:85], v[8:9]
	v_pk_mul_f32 v[82:83], v[82:83], s[14:15] op_sel_hi:[1,0]
	v_pk_mul_f32 v[96:97], v[96:97], v[98:99]
	v_exp_f32_e32 v82, v82
	v_exp_f32_e32 v83, v83
	v_pk_mul_f32 v[84:85], v[84:85], s[14:15] op_sel_hi:[1,0]
	v_cvt_pk_bf16_f32 v94, v94, v95
	v_cvt_pk_bf16_f32 v95, v96, v97
	s_waitcnt vmcnt(18)
	v_lshlrev_b32_e32 v96, 16, v180
	v_and_b32_e32 v97, 0xffff0000, v180
	v_pk_add_f32 v[86:87], v[86:87], 1.0 op_sel_hi:[1,0]
	v_exp_f32_e32 v84, v84
	v_exp_f32_e32 v85, v85
	v_pk_mul_f32 v[90:91], v[90:91], v[96:97]
	v_lshlrev_b32_e32 v96, 16, v181
	v_and_b32_e32 v97, 0xffff0000, v181
	v_rcp_f32_e32 v86, v86
	v_rcp_f32_e32 v87, v87
	v_pk_add_f32 v[88:89], v[88:89], 1.0 op_sel_hi:[1,0]
	v_pk_add_f32 v[78:79], v[78:79], v[30:31]
	v_pk_mul_f32 v[92:93], v[92:93], v[96:97]
	v_rcp_f32_e32 v88, v88
	v_rcp_f32_e32 v89, v89
	v_pk_add_f32 v[80:81], v[80:81], v[32:33]
	v_pk_mul_f32 v[78:79], v[78:79], s[14:15] op_sel_hi:[1,0]
	v_cvt_pk_bf16_f32 v90, v90, v91
	v_cvt_pk_bf16_f32 v91, v92, v93
	v_add_u32_e32 v92, 0x6000, v215
	v_pk_add_f32 v[82:83], v[82:83], 1.0 op_sel_hi:[1,0]
	v_exp_f32_e32 v78, v78
	v_exp_f32_e32 v79, v79
	v_pk_mul_f32 v[80:81], v[80:81], s[14:15] op_sel_hi:[1,0]
	ds_write2_b64 v92, v[94:95], v[90:91] offset0:96 offset1:100
	s_waitcnt vmcnt(17)
	v_lshlrev_b32_e32 v90, 16, v178
	v_and_b32_e32 v91, 0xffff0000, v178
	v_rcp_f32_e32 v82, v82
	v_rcp_f32_e32 v83, v83
	v_pk_add_f32 v[84:85], v[84:85], 1.0 op_sel_hi:[1,0]
	v_exp_f32_e32 v80, v80
	v_exp_f32_e32 v81, v81
	v_pk_add_f32 v[74:75], v[74:75], v[22:23]
	v_pk_mul_f32 v[86:87], v[86:87], v[90:91]
	v_lshlrev_b32_e32 v90, 16, v179
	v_and_b32_e32 v91, 0xffff0000, v179
	v_rcp_f32_e32 v84, v84
	v_rcp_f32_e32 v85, v85
	v_pk_add_f32 v[76:77], v[76:77], v[24:25]
	v_pk_mul_f32 v[74:75], v[74:75], s[14:15] op_sel_hi:[1,0]
	v_pk_mul_f32 v[88:89], v[88:89], v[90:91]
	v_exp_f32_e32 v74, v74
	v_exp_f32_e32 v75, v75
	v_pk_mul_f32 v[76:77], v[76:77], s[14:15] op_sel_hi:[1,0]
	v_cvt_pk_bf16_f32 v86, v86, v87
	v_cvt_pk_bf16_f32 v87, v88, v89
	s_waitcnt vmcnt(16)
	v_lshlrev_b32_e32 v88, 16, v176
	v_and_b32_e32 v89, 0xffff0000, v176
	v_pk_add_f32 v[78:79], v[78:79], 1.0 op_sel_hi:[1,0]
	v_exp_f32_e32 v76, v76
	v_exp_f32_e32 v77, v77
	v_pk_mul_f32 v[82:83], v[82:83], v[88:89]
	v_lshlrev_b32_e32 v88, 16, v177
	v_and_b32_e32 v89, 0xffff0000, v177
	v_rcp_f32_e32 v78, v78
	v_rcp_f32_e32 v79, v79
	v_pk_add_f32 v[80:81], v[80:81], 1.0 op_sel_hi:[1,0]
	v_pk_add_f32 v[70:71], v[70:71], v[14:15]
	v_pk_mul_f32 v[84:85], v[84:85], v[88:89]
	v_rcp_f32_e32 v80, v80
	v_rcp_f32_e32 v81, v81
	v_pk_add_f32 v[72:73], v[72:73], v[16:17]
	v_pk_mul_f32 v[70:71], v[70:71], s[14:15] op_sel_hi:[1,0]
	v_cvt_pk_bf16_f32 v82, v82, v83
	v_cvt_pk_bf16_f32 v83, v84, v85
	v_pk_add_f32 v[74:75], v[74:75], 1.0 op_sel_hi:[1,0]
	v_exp_f32_e32 v70, v70
	v_exp_f32_e32 v71, v71
	v_pk_mul_f32 v[72:73], v[72:73], s[14:15] op_sel_hi:[1,0]
	ds_write2_b64 v92, v[86:87], v[82:83] offset0:104 offset1:108
	s_waitcnt vmcnt(15)
	v_lshlrev_b32_e32 v82, 16, v174
	v_and_b32_e32 v83, 0xffff0000, v174
	v_rcp_f32_e32 v74, v74
	v_rcp_f32_e32 v75, v75
	v_pk_add_f32 v[76:77], v[76:77], 1.0 op_sel_hi:[1,0]
	v_exp_f32_e32 v72, v72
	v_exp_f32_e32 v73, v73
	v_pk_add_f32 v[66:67], v[66:67], v[6:7]
	v_pk_mul_f32 v[78:79], v[78:79], v[82:83]
	v_lshlrev_b32_e32 v82, 16, v175
	v_and_b32_e32 v83, 0xffff0000, v175
	v_rcp_f32_e32 v76, v76
	v_rcp_f32_e32 v77, v77
	v_pk_add_f32 v[68:69], v[68:69], v[8:9]
	v_pk_mul_f32 v[66:67], v[66:67], s[14:15] op_sel_hi:[1,0]
	v_pk_mul_f32 v[80:81], v[80:81], v[82:83]
	v_exp_f32_e32 v66, v66
	v_exp_f32_e32 v67, v67
	v_pk_mul_f32 v[68:69], v[68:69], s[14:15] op_sel_hi:[1,0]
	v_cvt_pk_bf16_f32 v78, v78, v79
	v_cvt_pk_bf16_f32 v79, v80, v81
	s_waitcnt vmcnt(14)
	v_lshlrev_b32_e32 v80, 16, v172
	v_and_b32_e32 v81, 0xffff0000, v172
	v_pk_add_f32 v[70:71], v[70:71], 1.0 op_sel_hi:[1,0]
	v_exp_f32_e32 v68, v68
	v_exp_f32_e32 v69, v69
	v_pk_mul_f32 v[74:75], v[74:75], v[80:81]
	v_lshlrev_b32_e32 v80, 16, v173
	v_and_b32_e32 v81, 0xffff0000, v173
	v_rcp_f32_e32 v70, v70
	v_rcp_f32_e32 v71, v71
	v_pk_add_f32 v[72:73], v[72:73], 1.0 op_sel_hi:[1,0]
	v_pk_add_f32 v[62:63], v[62:63], v[30:31]
	v_pk_mul_f32 v[76:77], v[76:77], v[80:81]
	v_rcp_f32_e32 v72, v72
	v_rcp_f32_e32 v73, v73
	v_pk_add_f32 v[64:65], v[64:65], v[32:33]
	v_pk_mul_f32 v[62:63], v[62:63], s[14:15] op_sel_hi:[1,0]
	v_cvt_pk_bf16_f32 v74, v74, v75
	v_cvt_pk_bf16_f32 v75, v76, v77
	v_add_u32_e32 v76, 0x8000, v215
	v_pk_add_f32 v[66:67], v[66:67], 1.0 op_sel_hi:[1,0]
	v_exp_f32_e32 v62, v62
	v_exp_f32_e32 v63, v63
	v_pk_mul_f32 v[64:65], v[64:65], s[14:15] op_sel_hi:[1,0]
	ds_write2_b64 v76, v[78:79], v[74:75] offset0:128 offset1:132
	s_waitcnt vmcnt(13)
	v_lshlrev_b32_e32 v74, 16, v168
	v_and_b32_e32 v75, 0xffff0000, v168
	v_rcp_f32_e32 v66, v66
	v_rcp_f32_e32 v67, v67
	v_pk_add_f32 v[68:69], v[68:69], 1.0 op_sel_hi:[1,0]
	v_exp_f32_e32 v64, v64
	v_exp_f32_e32 v65, v65
	v_pk_add_f32 v[58:59], v[58:59], v[22:23]
	v_pk_mul_f32 v[70:71], v[70:71], v[74:75]
	v_lshlrev_b32_e32 v74, 16, v169
	v_and_b32_e32 v75, 0xffff0000, v169
	v_rcp_f32_e32 v68, v68
	v_rcp_f32_e32 v69, v69
	v_pk_add_f32 v[60:61], v[60:61], v[24:25]
	v_pk_mul_f32 v[58:59], v[58:59], s[14:15] op_sel_hi:[1,0]
	v_pk_mul_f32 v[72:73], v[72:73], v[74:75]
	v_exp_f32_e32 v58, v58
	v_exp_f32_e32 v59, v59
	v_pk_mul_f32 v[60:61], v[60:61], s[14:15] op_sel_hi:[1,0]
	v_cvt_pk_bf16_f32 v70, v70, v71
	v_cvt_pk_bf16_f32 v71, v72, v73
	s_waitcnt vmcnt(12)
	v_lshlrev_b32_e32 v72, 16, v166
	v_and_b32_e32 v73, 0xffff0000, v166
	v_pk_add_f32 v[62:63], v[62:63], 1.0 op_sel_hi:[1,0]
	v_exp_f32_e32 v60, v60
	v_exp_f32_e32 v61, v61
	v_pk_mul_f32 v[66:67], v[66:67], v[72:73]
	v_lshlrev_b32_e32 v72, 16, v167
	v_and_b32_e32 v73, 0xffff0000, v167
	v_rcp_f32_e32 v62, v62
	v_rcp_f32_e32 v63, v63
	v_pk_add_f32 v[64:65], v[64:65], 1.0 op_sel_hi:[1,0]
	v_pk_add_f32 v[54:55], v[54:55], v[14:15]
	v_pk_mul_f32 v[68:69], v[68:69], v[72:73]
	v_rcp_f32_e32 v64, v64
	v_rcp_f32_e32 v65, v65
	v_pk_add_f32 v[56:57], v[56:57], v[16:17]
	v_pk_mul_f32 v[54:55], v[54:55], s[14:15] op_sel_hi:[1,0]
	v_cvt_pk_bf16_f32 v66, v66, v67
	v_cvt_pk_bf16_f32 v67, v68, v69
	v_pk_add_f32 v[58:59], v[58:59], 1.0 op_sel_hi:[1,0]
	v_exp_f32_e32 v54, v54
	v_exp_f32_e32 v55, v55
	v_pk_mul_f32 v[56:57], v[56:57], s[14:15] op_sel_hi:[1,0]
	ds_write2_b64 v76, v[70:71], v[66:67] offset0:136 offset1:140
	s_waitcnt vmcnt(11)
	v_lshlrev_b32_e32 v66, 16, v164
	v_and_b32_e32 v67, 0xffff0000, v164
	v_rcp_f32_e32 v58, v58
	v_rcp_f32_e32 v59, v59
	v_pk_add_f32 v[60:61], v[60:61], 1.0 op_sel_hi:[1,0]
	v_exp_f32_e32 v56, v56
	v_exp_f32_e32 v57, v57
	v_pk_add_f32 v[50:51], v[50:51], v[6:7]
	v_pk_mul_f32 v[62:63], v[62:63], v[66:67]
	v_lshlrev_b32_e32 v66, 16, v165
	v_and_b32_e32 v67, 0xffff0000, v165
	v_rcp_f32_e32 v60, v60
	v_rcp_f32_e32 v61, v61
	v_pk_add_f32 v[52:53], v[52:53], v[8:9]
	v_pk_mul_f32 v[50:51], v[50:51], s[14:15] op_sel_hi:[1,0]
	v_pk_mul_f32 v[64:65], v[64:65], v[66:67]
	v_exp_f32_e32 v50, v50
	v_exp_f32_e32 v51, v51
	v_pk_mul_f32 v[52:53], v[52:53], s[14:15] op_sel_hi:[1,0]
	v_cvt_pk_bf16_f32 v62, v62, v63
	v_cvt_pk_bf16_f32 v63, v64, v65
	s_waitcnt vmcnt(10)
	v_lshlrev_b32_e32 v64, 16, v162
	v_and_b32_e32 v65, 0xffff0000, v162
	v_pk_add_f32 v[54:55], v[54:55], 1.0 op_sel_hi:[1,0]
	v_exp_f32_e32 v52, v52
	v_exp_f32_e32 v53, v53
	v_pk_mul_f32 v[58:59], v[58:59], v[64:65]
	v_lshlrev_b32_e32 v64, 16, v163
	v_and_b32_e32 v65, 0xffff0000, v163
	v_rcp_f32_e32 v54, v54
	v_rcp_f32_e32 v55, v55
	v_pk_add_f32 v[56:57], v[56:57], 1.0 op_sel_hi:[1,0]
	v_pk_add_f32 v[46:47], v[46:47], v[30:31]
	v_pk_mul_f32 v[60:61], v[60:61], v[64:65]
	v_rcp_f32_e32 v56, v56
	v_rcp_f32_e32 v57, v57
	v_pk_add_f32 v[48:49], v[48:49], v[32:33]
	v_pk_mul_f32 v[46:47], v[46:47], s[14:15] op_sel_hi:[1,0]
	v_cvt_pk_bf16_f32 v58, v58, v59
	v_cvt_pk_bf16_f32 v59, v60, v61
	v_add_u32_e32 v60, 0xa000, v215
	v_pk_add_f32 v[50:51], v[50:51], 1.0 op_sel_hi:[1,0]
	v_exp_f32_e32 v46, v46
	v_exp_f32_e32 v47, v47
	v_pk_mul_f32 v[48:49], v[48:49], s[14:15] op_sel_hi:[1,0]
	ds_write2_b64 v60, v[62:63], v[58:59] offset0:160 offset1:164
	s_waitcnt vmcnt(9)
	v_lshlrev_b32_e32 v58, 16, v160
	v_and_b32_e32 v59, 0xffff0000, v160
	v_rcp_f32_e32 v50, v50
	v_rcp_f32_e32 v51, v51
	v_pk_add_f32 v[52:53], v[52:53], 1.0 op_sel_hi:[1,0]
	v_exp_f32_e32 v48, v48
	v_exp_f32_e32 v49, v49
	v_pk_add_f32 v[42:43], v[42:43], v[22:23]
	v_pk_mul_f32 v[54:55], v[54:55], v[58:59]
	v_lshlrev_b32_e32 v58, 16, v161
	v_and_b32_e32 v59, 0xffff0000, v161
	v_rcp_f32_e32 v52, v52
	v_rcp_f32_e32 v53, v53
	v_pk_add_f32 v[44:45], v[44:45], v[24:25]
	v_pk_mul_f32 v[42:43], v[42:43], s[14:15] op_sel_hi:[1,0]
	v_pk_mul_f32 v[56:57], v[56:57], v[58:59]
	v_exp_f32_e32 v42, v42
	v_exp_f32_e32 v43, v43
	v_pk_mul_f32 v[44:45], v[44:45], s[14:15] op_sel_hi:[1,0]
	v_cvt_pk_bf16_f32 v54, v54, v55
	v_cvt_pk_bf16_f32 v55, v56, v57
	s_waitcnt vmcnt(8)
	v_lshlrev_b32_e32 v56, 16, v156
	v_and_b32_e32 v57, 0xffff0000, v156
	v_pk_add_f32 v[46:47], v[46:47], 1.0 op_sel_hi:[1,0]
	v_exp_f32_e32 v44, v44
	v_exp_f32_e32 v45, v45
	v_pk_mul_f32 v[50:51], v[50:51], v[56:57]
	v_lshlrev_b32_e32 v56, 16, v157
	v_and_b32_e32 v57, 0xffff0000, v157
	v_rcp_f32_e32 v46, v46
	v_rcp_f32_e32 v47, v47
	v_pk_add_f32 v[48:49], v[48:49], 1.0 op_sel_hi:[1,0]
	v_pk_add_f32 v[38:39], v[38:39], v[14:15]
	v_pk_mul_f32 v[52:53], v[52:53], v[56:57]
	v_rcp_f32_e32 v48, v48
	v_rcp_f32_e32 v49, v49
	v_pk_add_f32 v[40:41], v[40:41], v[16:17]
	v_pk_mul_f32 v[38:39], v[38:39], s[14:15] op_sel_hi:[1,0]
	v_cvt_pk_bf16_f32 v50, v50, v51
	v_cvt_pk_bf16_f32 v51, v52, v53
	v_pk_add_f32 v[42:43], v[42:43], 1.0 op_sel_hi:[1,0]
	v_exp_f32_e32 v38, v38
	v_exp_f32_e32 v39, v39
	v_pk_mul_f32 v[40:41], v[40:41], s[14:15] op_sel_hi:[1,0]
	ds_write2_b64 v60, v[54:55], v[50:51] offset0:168 offset1:172
	s_waitcnt vmcnt(7)
	v_lshlrev_b32_e32 v50, 16, v154
	v_and_b32_e32 v51, 0xffff0000, v154
	v_rcp_f32_e32 v42, v42
	v_rcp_f32_e32 v43, v43
	v_pk_add_f32 v[44:45], v[44:45], 1.0 op_sel_hi:[1,0]
	v_exp_f32_e32 v40, v40
	v_exp_f32_e32 v41, v41
	v_pk_add_f32 v[34:35], v[34:35], v[6:7]
	v_pk_mul_f32 v[46:47], v[46:47], v[50:51]
	v_lshlrev_b32_e32 v50, 16, v155
	v_and_b32_e32 v51, 0xffff0000, v155
	v_rcp_f32_e32 v44, v44
	v_rcp_f32_e32 v45, v45
	v_pk_add_f32 v[36:37], v[36:37], v[8:9]
	v_pk_mul_f32 v[34:35], v[34:35], s[14:15] op_sel_hi:[1,0]
	v_pk_mul_f32 v[48:49], v[48:49], v[50:51]
	v_exp_f32_e32 v34, v34
	v_exp_f32_e32 v35, v35
	v_pk_mul_f32 v[36:37], v[36:37], s[14:15] op_sel_hi:[1,0]
	v_cvt_pk_bf16_f32 v46, v46, v47
	v_cvt_pk_bf16_f32 v47, v48, v49
	s_waitcnt vmcnt(6)
	v_lshlrev_b32_e32 v48, 16, v152
	v_and_b32_e32 v49, 0xffff0000, v152
	v_pk_add_f32 v[38:39], v[38:39], 1.0 op_sel_hi:[1,0]
	v_exp_f32_e32 v36, v36
	v_exp_f32_e32 v37, v37
	v_pk_mul_f32 v[42:43], v[42:43], v[48:49]
	v_lshlrev_b32_e32 v48, 16, v153
	v_and_b32_e32 v49, 0xffff0000, v153
	v_rcp_f32_e32 v38, v38
	v_rcp_f32_e32 v39, v39
	v_pk_add_f32 v[40:41], v[40:41], 1.0 op_sel_hi:[1,0]
	v_pk_add_f32 v[28:29], v[28:29], v[32:33]
	v_pk_add_f32 v[26:27], v[26:27], v[30:31]
	v_pk_mul_f32 v[44:45], v[44:45], v[48:49]
	v_rcp_f32_e32 v40, v40
	v_rcp_f32_e32 v41, v41
	v_pk_mul_f32 v[26:27], v[26:27], s[14:15] op_sel_hi:[1,0]
	v_pk_mul_f32 v[28:29], v[28:29], s[14:15] op_sel_hi:[1,0]
	v_cvt_pk_bf16_f32 v42, v42, v43
	v_cvt_pk_bf16_f32 v43, v44, v45
	v_add_u32_e32 v44, 0xc000, v215
	v_pk_add_f32 v[34:35], v[34:35], 1.0 op_sel_hi:[1,0]
	v_exp_f32_e32 v26, v26
	v_exp_f32_e32 v27, v27
	v_exp_f32_e32 v28, v28
	v_exp_f32_e32 v29, v29
	v_pk_add_f32 v[20:21], v[20:21], v[24:25]
	v_pk_add_f32 v[18:19], v[18:19], v[22:23]
	ds_write2_b64 v44, v[46:47], v[42:43] offset0:192 offset1:196
	s_waitcnt vmcnt(5)
	v_lshlrev_b32_e32 v42, 16, v150
	v_and_b32_e32 v43, 0xffff0000, v150
	v_rcp_f32_e32 v34, v34
	v_rcp_f32_e32 v35, v35
	v_pk_add_f32 v[36:37], v[36:37], 1.0 op_sel_hi:[1,0]
	v_pk_mul_f32 v[18:19], v[18:19], s[14:15] op_sel_hi:[1,0]
	v_pk_mul_f32 v[20:21], v[20:21], s[14:15] op_sel_hi:[1,0]
	v_pk_mul_f32 v[38:39], v[38:39], v[42:43]
	v_lshlrev_b32_e32 v42, 16, v151
	v_and_b32_e32 v43, 0xffff0000, v151
	v_rcp_f32_e32 v36, v36
	v_rcp_f32_e32 v37, v37
	v_exp_f32_e32 v18, v18
	v_exp_f32_e32 v19, v19
	v_exp_f32_e32 v20, v20
	v_exp_f32_e32 v21, v21
	v_pk_mul_f32 v[40:41], v[40:41], v[42:43]
	v_pk_add_f32 v[12:13], v[12:13], v[16:17]
	v_pk_add_f32 v[10:11], v[10:11], v[14:15]
	v_cvt_pk_bf16_f32 v38, v38, v39
	v_cvt_pk_bf16_f32 v39, v40, v41
	s_waitcnt vmcnt(4)
	v_lshlrev_b32_e32 v40, 16, v148
	v_and_b32_e32 v41, 0xffff0000, v148
	v_pk_add_f32 v[26:27], v[26:27], 1.0 op_sel_hi:[1,0]
	v_pk_add_f32 v[28:29], v[28:29], 1.0 op_sel_hi:[1,0]
	v_pk_mul_f32 v[10:11], v[10:11], s[14:15] op_sel_hi:[1,0]
	v_pk_mul_f32 v[12:13], v[12:13], s[14:15] op_sel_hi:[1,0]
	v_pk_mul_f32 v[34:35], v[34:35], v[40:41]
	v_lshlrev_b32_e32 v40, 16, v149
	v_and_b32_e32 v41, 0xffff0000, v149
	v_rcp_f32_e32 v26, v26
	v_rcp_f32_e32 v27, v27
	v_rcp_f32_e32 v28, v28
	v_rcp_f32_e32 v29, v29
	v_exp_f32_e32 v10, v10
	v_exp_f32_e32 v11, v11
	v_exp_f32_e32 v12, v12
	v_exp_f32_e32 v13, v13
	v_pk_add_f32 v[4:5], v[4:5], v[8:9]
	v_pk_add_f32 v[2:3], v[2:3], v[6:7]
	v_pk_mul_f32 v[36:37], v[36:37], v[40:41]
	v_pk_add_f32 v[18:19], v[18:19], 1.0 op_sel_hi:[1,0]
	v_pk_add_f32 v[20:21], v[20:21], 1.0 op_sel_hi:[1,0]
	v_pk_mul_f32 v[2:3], v[2:3], s[14:15] op_sel_hi:[1,0]
	v_pk_mul_f32 v[4:5], v[4:5], s[14:15] op_sel_hi:[1,0]
	v_cvt_pk_bf16_f32 v34, v34, v35
	v_cvt_pk_bf16_f32 v35, v36, v37
	v_rcp_f32_e32 v18, v18
	v_rcp_f32_e32 v19, v19
	v_rcp_f32_e32 v20, v20
	v_rcp_f32_e32 v21, v21
	v_exp_f32_e32 v2, v2
	v_exp_f32_e32 v3, v3
	v_exp_f32_e32 v4, v4
	v_exp_f32_e32 v5, v5
	ds_write2_b64 v44, v[38:39], v[34:35] offset0:200 offset1:204
	s_waitcnt vmcnt(3)
	v_lshlrev_b32_e32 v34, 16, v144
	v_and_b32_e32 v35, 0xffff0000, v144
	v_lshlrev_b32_e32 v30, 16, v145
	v_and_b32_e32 v31, 0xffff0000, v145
	v_pk_mul_f32 v[26:27], v[26:27], v[34:35]
	v_pk_mul_f32 v[28:29], v[28:29], v[30:31]
	v_pk_add_f32 v[10:11], v[10:11], 1.0 op_sel_hi:[1,0]
	v_pk_add_f32 v[12:13], v[12:13], 1.0 op_sel_hi:[1,0]
	v_cvt_pk_bf16_f32 v26, v26, v27
	v_cvt_pk_bf16_f32 v27, v28, v29
	s_waitcnt vmcnt(2)
	v_lshlrev_b32_e32 v28, 16, v142
	v_and_b32_e32 v29, 0xffff0000, v142
	v_lshlrev_b32_e32 v22, 16, v143
	v_and_b32_e32 v23, 0xffff0000, v143
	v_rcp_f32_e32 v10, v10
	v_rcp_f32_e32 v11, v11
	v_rcp_f32_e32 v12, v12
	v_rcp_f32_e32 v13, v13
	v_pk_mul_f32 v[18:19], v[18:19], v[28:29]
	v_pk_mul_f32 v[20:21], v[20:21], v[22:23]
	v_pk_add_f32 v[2:3], v[2:3], 1.0 op_sel_hi:[1,0]
	v_pk_add_f32 v[4:5], v[4:5], 1.0 op_sel_hi:[1,0]
	v_cvt_pk_bf16_f32 v18, v18, v19
	v_cvt_pk_bf16_f32 v19, v20, v21
	v_add_u32_e32 v20, 0xe000, v215
	v_rcp_f32_e32 v2, v2
	v_rcp_f32_e32 v3, v3
	v_rcp_f32_e32 v4, v4
	v_rcp_f32_e32 v5, v5
	ds_write2_b64 v20, v[26:27], v[18:19] offset0:224 offset1:228
	s_waitcnt vmcnt(1)
	v_lshlrev_b32_e32 v18, 16, v140
	v_and_b32_e32 v19, 0xffff0000, v140
	v_lshlrev_b32_e32 v14, 16, v141
	v_and_b32_e32 v15, 0xffff0000, v141
	v_pk_mul_f32 v[10:11], v[10:11], v[18:19]
	v_pk_mul_f32 v[12:13], v[12:13], v[14:15]
	v_cvt_pk_bf16_f32 v10, v10, v11
	v_cvt_pk_bf16_f32 v11, v12, v13
	s_waitcnt vmcnt(0)
	v_lshlrev_b32_e32 v12, 16, v138
	v_and_b32_e32 v13, 0xffff0000, v138
	v_lshlrev_b32_e32 v6, 16, v139
	v_and_b32_e32 v7, 0xffff0000, v139
	v_pk_mul_f32 v[2:3], v[2:3], v[12:13]
	v_pk_mul_f32 v[4:5], v[4:5], v[6:7]
	v_cvt_pk_bf16_f32 v2, v2, v3
	v_cvt_pk_bf16_f32 v3, v4, v5
	v_lshl_or_b32 v4, s23, 5, v253
	ds_write2_b64 v20, v[10:11], v[2:3] offset0:232 offset1:236
	v_mul_lo_u32 v2, v4, s18
	s_waitcnt lgkmcnt(0)
	s_barrier
	v_add_u32_e32 v5, v211, v2
	ds_read_b128 v[14:17], v5
	s_waitcnt lgkmcnt(0)
	v_and_b32_e32 v3, 0xffff0000, v14
	v_lshlrev_b32_e32 v2, 16, v14
	v_mul_f32_e32 v3, v3, v3
	v_fmac_f32_e32 v3, v2, v2
	v_lshlrev_b32_e32 v2, 16, v15
	v_fmac_f32_e32 v3, v2, v2
	v_and_b32_e32 v2, 0xffff0000, v15
	v_fmac_f32_e32 v3, v2, v2
	v_lshlrev_b32_e32 v2, 16, v16
	v_fmac_f32_e32 v3, v2, v2
	v_and_b32_e32 v2, 0xffff0000, v16
	v_fmac_f32_e32 v3, v2, v2
	v_lshlrev_b32_e32 v2, 16, v17
	v_fmac_f32_e32 v3, v2, v2
	v_and_b32_e32 v2, 0xffff0000, v17
	v_fmac_f32_e32 v3, v2, v2
	v_and_b32_e32 v2, 64, v214
	v_add_u32_e32 v12, 64, v2
	v_xor_b32_e32 v2, 1, v214
	v_cmp_lt_i32_e64 s[0:1], v2, v12
	s_nop 1
	v_cndmask_b32_e64 v2, v214, v2, s[0:1]
	v_lshlrev_b32_e32 v6, 2, v2
	ds_bpermute_b32 v2, v6, v3
	s_waitcnt lgkmcnt(0)
	v_add_f32_e32 v2, v3, v2
	v_xor_b32_e32 v3, 2, v214
	v_cmp_lt_i32_e64 s[0:1], v3, v12
	s_nop 1
	v_cndmask_b32_e64 v3, v214, v3, s[0:1]
	v_lshlrev_b32_e32 v7, 2, v3
	ds_bpermute_b32 v3, v7, v2
	s_waitcnt lgkmcnt(0)
	v_add_f32_e32 v9, v2, v3
	v_xor_b32_e32 v2, 4, v214
	v_cmp_lt_i32_e64 s[0:1], v2, v12
	s_nop 1
	v_cndmask_b32_e64 v2, v214, v2, s[0:1]
	v_lshlrev_b32_e32 v8, 2, v2
	ds_bpermute_b32 v13, v8, v9
	v_add_u32_e32 v2, s21, v4
	v_ashrrev_i32_e32 v3, 31, v2
	v_lshlrev_b64 v[10:11], 12, v[2:3]
	v_lshl_add_u64 v[10:11], s[8:9], 0, v[10:11]
	s_waitcnt lgkmcnt(0)
	v_add_f32_e32 v13, v9, v13
	v_xor_b32_e32 v9, 8, v214
	v_cmp_lt_i32_e64 s[0:1], v9, v12
	v_lshl_add_u64 v[10:11], v[10:11], 0, s[2:3]
	v_lshl_add_u64 v[18:19], v[10:11], 0, v[146:147]
	v_cndmask_b32_e64 v9, v214, v9, s[0:1]
	v_lshlrev_b32_e32 v9, 2, v9
	ds_bpermute_b32 v20, v9, v13
	v_xor_b32_e32 v10, 16, v214
	v_cmp_lt_i32_e64 s[0:1], v10, v12
	global_store_dwordx4 v[18:19], v[14:17], off sc1
	s_nop 1
	s_waitcnt lgkmcnt(0)
	v_add_f32_e32 v11, v13, v20
	v_cndmask_b32_e64 v10, v214, v10, s[0:1]
	v_lshlrev_b32_e32 v10, 2, v10
	ds_bpermute_b32 v12, v10, v11
	s_and_saveexec_b64 s[0:1], vcc
	s_cbranch_execz .LBB0_1042
	v_lshl_add_u64 v[2:3], v[2:3], 4, s[10:11]
	s_lshl_b32 s22, s20, 2
	s_mov_b32 s23, s3
	s_waitcnt lgkmcnt(0)
	v_add_f32_e32 v11, v11, v12
	v_lshl_add_u64 v[2:3], v[2:3], 0, s[22:23]
	global_store_dword v[2:3], v11, off

.LBB0_1129:
	s_add_i32 s50, s26, 0xffff8000
	s_and_b32 s50, s50, 0x8000
	s_add_i32 s50, s50, 0
	s_add_i32 s49, s8, 0
	s_add_i32 s50, s50, 0x18000
	v_add_u32_e32 v154, s50, v157
	v_add_u32_e32 v218, s49, v161
	v_add_u32_e32 v224, s50, v155
	v_add_u32_e32 v185, s50, v156
	s_branch .Lrot_o1

.Lrot_o1:
	ds_read_b64_tr_b16 v[186:187], v154
	ds_read_b64_tr_b16 v[188:189], v154 offset:2048
	ds_read_b64_tr_b16 v[190:191], v185
	ds_read_b64_tr_b16 v[192:193], v185 offset:2048
	ds_read_b128 v[194:197], v218
	ds_read_b128 v[198:201], v218 offset:2048
	ds_read_b64_tr_b16 v[202:203], v224
	ds_read_b64_tr_b16 v[204:205], v224 offset:2048
	v_add_u32_e32 v226, s50, v153
	ds_read_b64_tr_b16 v[206:207], v226
	ds_read_b64_tr_b16 v[208:209], v226 offset:2048
	ds_read_b128 v[210:213], v218 offset:4096
	s_waitcnt lgkmcnt(6)
	v_mfma_f32_16x16x32_bf16 v[18:21], v[186:189], v[194:197], v[18:21]
	s_add_i32 s50, s48, 0
	v_add_u32_e32 v214, 0xfff40000, v152
	s_add_i32 s51, s50, s44
	v_mfma_f32_16x16x32_bf16 v[22:25], v[190:193], v[194:197], v[22:25]
	s_mov_b32 s52, m0
	s_mov_b32 m0, s51
	s_nop 0
	global_load_lds_dwordx4 v214, s[10:11]
	s_mov_b32 m0, s52
	s_waitcnt lgkmcnt(3)
	v_mfma_f32_16x16x32_bf16 v[26:29], v[202:205], v[194:197], v[26:29]
	s_waitcnt lgkmcnt(1)
	v_mfma_f32_16x16x32_bf16 v[30:33], v[206:209], v[194:197], v[30:33]
	v_mfma_f32_16x16x32_bf16 v[34:37], v[186:189], v[198:201], v[34:37]
	ds_read_b128 v[194:197], v218 offset:6144
	v_add_u32_e32 v214, 0xfff80000, v152
	s_add_i32 s51, s50, s45
	v_mfma_f32_16x16x32_bf16 v[38:41], v[190:193], v[198:201], v[38:41]
	s_mov_b32 s52, m0
	s_mov_b32 m0, s51
	s_nop 0
	global_load_lds_dwordx4 v214, s[10:11]
	s_mov_b32 m0, s52
	v_mfma_f32_16x16x32_bf16 v[42:45], v[202:205], v[198:201], v[42:45]
	v_mfma_f32_16x16x32_bf16 v[46:49], v[206:209], v[198:201], v[46:49]
	s_waitcnt lgkmcnt(1)
	v_mfma_f32_16x16x32_bf16 v[50:53], v[186:189], v[210:213], v[50:53]
	ds_read_b128 v[198:201], v218 offset:8192
	v_add_u32_e32 v214, 0xfffc0000, v152
	s_add_i32 s51, s50, s46
	v_mfma_f32_16x16x32_bf16 v[54:57], v[190:193], v[210:213], v[54:57]
	s_mov_b32 s52, m0
	s_mov_b32 m0, s51
	s_nop 0
	global_load_lds_dwordx4 v214, s[10:11]
	s_mov_b32 m0, s52
	v_mfma_f32_16x16x32_bf16 v[58:61], v[202:205], v[210:213], v[58:61]
	v_mfma_f32_16x16x32_bf16 v[62:65], v[206:209], v[210:213], v[62:65]
	s_waitcnt lgkmcnt(1)
	v_mfma_f32_16x16x32_bf16 v[66:69], v[186:189], v[194:197], v[66:69]
	ds_read_b128 v[210:213], v218 offset:10240
	s_add_i32 s50, s50, s47
	s_mov_b32 s51, m0
	s_mov_b32 m0, s50
	s_nop 0
	global_load_lds_dwordx4 v152, s[10:11]
	s_mov_b32 m0, s51
	v_mfma_f32_16x16x32_bf16 v[70:73], v[190:193], v[194:197], v[70:73]
	v_mfma_f32_16x16x32_bf16 v[74:77], v[202:205], v[194:197], v[74:77]
	v_mfma_f32_16x16x32_bf16 v[78:81], v[206:209], v[194:197], v[78:81]
	ds_read_b128 v[194:197], v218 offset:12288
	ds_read_b64_tr_b16 v[214:215], v154 offset:16384
	ds_read_b64_tr_b16 v[216:217], v154 offset:18432
	s_waitcnt lgkmcnt(4)
	v_mfma_f32_16x16x32_bf16 v[82:85], v[186:189], v[198:201], v[82:85]
	v_mfma_f32_16x16x32_bf16 v[86:89], v[190:193], v[198:201], v[86:89]
	v_mfma_f32_16x16x32_bf16 v[90:93], v[202:205], v[198:201], v[90:93]
	v_mfma_f32_16x16x32_bf16 v[94:97], v[206:209], v[198:201], v[94:97]
	ds_read_b128 v[198:201], v218 offset:14336
	ds_read_b64_tr_b16 v[218:219], v185 offset:16384
	ds_read_b64_tr_b16 v[220:221], v185 offset:18432
	s_waitcnt lgkmcnt(6)
	v_mfma_f32_16x16x32_bf16 v[98:101], v[186:189], v[210:213], v[98:101]
	v_mfma_f32_16x16x32_bf16 v[102:105], v[190:193], v[210:213], v[102:105]
	v_mfma_f32_16x16x32_bf16 v[106:109], v[202:205], v[210:213], v[106:109]
	v_mfma_f32_16x16x32_bf16 v[110:113], v[206:209], v[210:213], v[110:113]
	v_add_u32_e32 v154, s49, v162
	ds_read_b128 v[210:213], v154
	ds_read_b64_tr_b16 v[222:223], v224 offset:16384
	ds_read_b64_tr_b16 v[224:225], v224 offset:18432
	s_waitcnt lgkmcnt(8)
	v_mfma_f32_16x16x32_bf16 v[114:117], v[186:189], v[194:197], v[114:117]
	v_mfma_f32_16x16x32_bf16 v[118:121], v[190:193], v[194:197], v[118:121]
	v_mfma_f32_16x16x32_bf16 v[122:125], v[202:205], v[194:197], v[122:125]
	v_mfma_f32_16x16x32_bf16 v[126:129], v[206:209], v[194:197], v[126:129]
	s_waitcnt lgkmcnt(5)
	v_mfma_f32_16x16x32_bf16 v[130:133], v[186:189], v[198:201], v[130:133]
	ds_read_b128 v[186:189], v154 offset:2048
	s_and_b32 s49, s26, 0x8000
	v_mfma_f32_16x16x32_bf16 v[134:137], v[190:193], v[198:201], v[134:137]
	ds_read_b64_tr_b16 v[190:191], v226 offset:16384
	ds_read_b64_tr_b16 v[192:193], v226 offset:18432
	v_mfma_f32_16x16x32_bf16 v[138:141], v[202:205], v[198:201], v[138:141]
	v_mfma_f32_16x16x32_bf16 v[142:145], v[206:209], v[198:201], v[142:145]
	s_waitcnt lgkmcnt(5)
	v_mfma_f32_16x16x32_bf16 v[18:21], v[214:217], v[210:213], v[18:21]
	ds_read_b128 v[194:197], v154 offset:4096
	v_add_u32_e32 v185, s49, v163
	s_add_u32 s49, s6, s4
	v_mfma_f32_16x16x32_bf16 v[22:25], v[218:221], v[210:213], v[22:25]
	s_addc_u32 s52, s7, s5
	s_waitcnt vmcnt(7)
	s_add_u32 s50, s49, 0x80000
	s_waitcnt lgkmcnt(4)
	v_mfma_f32_16x16x32_bf16 v[26:29], v[222:225], v[210:213], v[26:29]
	ds_write_b128 v185, v[14:17]
	s_addc_u32 s51, s52, 0
	global_load_dwordx4 v[14:17], v173, s[50:51]
	s_waitcnt lgkmcnt(2)
	v_mfma_f32_16x16x32_bf16 v[30:33], v[190:193], v[210:213], v[30:33]
	v_mfma_f32_16x16x32_bf16 v[34:37], v[214:217], v[186:189], v[34:37]
	ds_read_b128 v[198:201], v154 offset:6144
	s_waitcnt vmcnt(7)
	s_add_u32 s50, s49, 0x90000
	v_mfma_f32_16x16x32_bf16 v[38:41], v[218:221], v[186:189], v[38:41]
	ds_write_b128 v185, v[10:13] offset:8192
	s_addc_u32 s51, s52, 0
	global_load_dwordx4 v[10:13], v173, s[50:51]
	v_mfma_f32_16x16x32_bf16 v[42:45], v[222:225], v[186:189], v[42:45]
	v_mfma_f32_16x16x32_bf16 v[46:49], v[190:193], v[186:189], v[46:49]
	s_waitcnt lgkmcnt(3)
	v_mfma_f32_16x16x32_bf16 v[50:53], v[214:217], v[194:197], v[50:53]
	ds_read_b128 v[186:189], v154 offset:8192
	s_waitcnt vmcnt(7)
	s_add_u32 s50, s49, 0xa0000
	v_mfma_f32_16x16x32_bf16 v[54:57], v[218:221], v[194:197], v[54:57]
	ds_write_b128 v185, v[6:9] offset:16384
	s_addc_u32 s51, s52, 0
	global_load_dwordx4 v[6:9], v173, s[50:51]
	v_mfma_f32_16x16x32_bf16 v[58:61], v[222:225], v[194:197], v[58:61]
	v_mfma_f32_16x16x32_bf16 v[62:65], v[190:193], v[194:197], v[62:65]
	s_waitcnt lgkmcnt(3)
	v_mfma_f32_16x16x32_bf16 v[66:69], v[214:217], v[198:201], v[66:69]
	ds_read_b128 v[194:197], v154 offset:10240
	s_waitcnt vmcnt(7)
	s_add_u32 s50, s49, 0xb0000
	v_mfma_f32_16x16x32_bf16 v[70:73], v[218:221], v[198:201], v[70:73]
	ds_write_b128 v185, v[2:5] offset:24576
	s_addc_u32 s51, s52, 0
	global_load_dwordx4 v[2:5], v173, s[50:51]
	v_mfma_f32_16x16x32_bf16 v[74:77], v[222:225], v[198:201], v[74:77]
	v_mfma_f32_16x16x32_bf16 v[78:81], v[190:193], v[198:201], v[78:81]
	s_waitcnt lgkmcnt(3)
	v_mfma_f32_16x16x32_bf16 v[82:85], v[214:217], v[186:189], v[82:85]
	ds_read_b128 v[198:201], v154 offset:12288
	v_mfma_f32_16x16x32_bf16 v[86:89], v[218:221], v[186:189], v[86:89]
	v_mfma_f32_16x16x32_bf16 v[90:93], v[222:225], v[186:189], v[90:93]
	v_mfma_f32_16x16x32_bf16 v[94:97], v[190:193], v[186:189], v[94:97]
	s_waitcnt lgkmcnt(2)
	v_mfma_f32_16x16x32_bf16 v[98:101], v[214:217], v[194:197], v[98:101]
	ds_read_b128 v[186:189], v154 offset:14336
	v_mfma_f32_16x16x32_bf16 v[102:105], v[218:221], v[194:197], v[102:105]
	v_mfma_f32_16x16x32_bf16 v[106:109], v[222:225], v[194:197], v[106:109]
	v_mfma_f32_16x16x32_bf16 v[110:113], v[190:193], v[194:197], v[110:113]
	s_waitcnt lgkmcnt(1)
	v_mfma_f32_16x16x32_bf16 v[114:117], v[214:217], v[198:201], v[114:117]
	v_mfma_f32_16x16x32_bf16 v[118:121], v[218:221], v[198:201], v[118:121]
	v_mfma_f32_16x16x32_bf16 v[122:125], v[222:225], v[198:201], v[122:125]
	v_mfma_f32_16x16x32_bf16 v[126:129], v[190:193], v[198:201], v[126:129]
	s_waitcnt lgkmcnt(0)
	v_mfma_f32_16x16x32_bf16 v[130:133], v[214:217], v[186:189], v[130:133]
	v_mfma_f32_16x16x32_bf16 v[134:137], v[218:221], v[186:189], v[134:137]
	v_mfma_f32_16x16x32_bf16 v[138:141], v[222:225], v[186:189], v[138:141]
	v_mfma_f32_16x16x32_bf16 v[142:145], v[190:193], v[186:189], v[142:145]
	s_add_i32 s49, s8, 0x8000
	s_cmp_lg_u32 s8, 0x10000
	s_cselect_b32 s8, s49, 0
	s_add_i32 s49, s48, 0x8000
	s_cmp_lg_u32 s48, 0x10000
	s_cselect_b32 s48, s49, 0
	s_add_u32 s4, s4, 0x40000
	s_addc_u32 s5, s5, 0
	s_add_i32 s26, s26, 0x8000
	v_add_u32_e32 v152, 0x80, v152
	s_add_i32 s50, s26, 0xffff8000
	s_and_b32 s50, s50, 0x8000
	s_add_i32 s50, s50, 0
	s_add_i32 s49, s8, 0
	s_add_i32 s50, s50, 0x18000
	v_add_u32_e32 v154, s50, v157
	v_add_u32_e32 v218, s49, v161
	v_add_u32_e32 v224, s50, v155
	v_add_u32_e32 v185, s50, v156
	s_waitcnt lgkmcnt(0)
	s_cmp_eq_u32 s4, 0x400000
	s_cbranch_scc0 .Lrot_o1_head
	s_barrier
	v_or_b32_e32 v152, v181, v1
	v_lshlrev_b32_e32 v185, 2, v152
	ds_bpermute_b32 v152, v185, v165
	ds_bpermute_b32 v154, v185, v165 offset:64
	ds_bpermute_b32 v186, v185, v165 offset:128
	ds_bpermute_b32 v188, v185, v184 offset:192
	ds_bpermute_b32 v190, v185, v165 offset:192
	ds_bpermute_b32 v192, v185, v184
	ds_bpermute_b32 v194, v185, v184 offset:64
	ds_bpermute_b32 v184, v185, v184 offset:128
	s_mov_b32 s8, 0
	s_waitcnt lgkmcnt(4)
	v_pk_mul_f32 v[144:145], v[144:145], v[188:189] op_sel_hi:[1,0]
	v_pk_mul_f32 v[142:143], v[142:143], v[188:189] op_sel_hi:[1,0]
	v_pk_mul_f32 v[140:141], v[140:141], v[188:189] op_sel_hi:[1,0]
	v_pk_mul_f32 v[138:139], v[138:139], v[188:189] op_sel_hi:[1,0]
	v_pk_mul_f32 v[136:137], v[136:137], v[188:189] op_sel_hi:[1,0]
	v_pk_mul_f32 v[134:135], v[134:135], v[188:189] op_sel_hi:[1,0]
	v_pk_mul_f32 v[132:133], v[132:133], v[188:189] op_sel_hi:[1,0]
	v_pk_mul_f32 v[130:131], v[130:131], v[188:189] op_sel_hi:[1,0]
	s_waitcnt lgkmcnt(0)
	v_pk_mul_f32 v[128:129], v[128:129], v[184:185] op_sel_hi:[1,0]
	v_pk_mul_f32 v[126:127], v[126:127], v[184:185] op_sel_hi:[1,0]
	v_pk_mul_f32 v[124:125], v[124:125], v[184:185] op_sel_hi:[1,0]
	v_pk_mul_f32 v[122:123], v[122:123], v[184:185] op_sel_hi:[1,0]
	v_pk_mul_f32 v[120:121], v[120:121], v[184:185] op_sel_hi:[1,0]
	v_pk_mul_f32 v[118:119], v[118:119], v[184:185] op_sel_hi:[1,0]
	v_pk_mul_f32 v[116:117], v[116:117], v[184:185] op_sel_hi:[1,0]
	v_pk_mul_f32 v[114:115], v[114:115], v[184:185] op_sel_hi:[1,0]
	v_pk_mul_f32 v[112:113], v[112:113], v[194:195] op_sel_hi:[1,0]
	v_pk_mul_f32 v[110:111], v[110:111], v[194:195] op_sel_hi:[1,0]
	v_pk_mul_f32 v[108:109], v[108:109], v[194:195] op_sel_hi:[1,0]
	v_pk_mul_f32 v[106:107], v[106:107], v[194:195] op_sel_hi:[1,0]
	v_pk_mul_f32 v[104:105], v[104:105], v[194:195] op_sel_hi:[1,0]
	v_pk_mul_f32 v[102:103], v[102:103], v[194:195] op_sel_hi:[1,0]
	v_pk_mul_f32 v[100:101], v[100:101], v[194:195] op_sel_hi:[1,0]
	v_pk_mul_f32 v[98:99], v[98:99], v[194:195] op_sel_hi:[1,0]
	v_pk_mul_f32 v[96:97], v[96:97], v[192:193] op_sel_hi:[1,0]
	v_pk_mul_f32 v[94:95], v[94:95], v[192:193] op_sel_hi:[1,0]
	v_pk_mul_f32 v[92:93], v[92:93], v[192:193] op_sel_hi:[1,0]
	v_pk_mul_f32 v[90:91], v[90:91], v[192:193] op_sel_hi:[1,0]
	v_pk_mul_f32 v[88:89], v[88:89], v[192:193] op_sel_hi:[1,0]
	v_pk_mul_f32 v[86:87], v[86:87], v[192:193] op_sel_hi:[1,0]
	v_pk_mul_f32 v[84:85], v[84:85], v[192:193] op_sel_hi:[1,0]
	v_pk_mul_f32 v[82:83], v[82:83], v[192:193] op_sel_hi:[1,0]
	v_pk_mul_f32 v[80:81], v[80:81], v[190:191] op_sel_hi:[1,0]
	v_pk_mul_f32 v[78:79], v[78:79], v[190:191] op_sel_hi:[1,0]
	v_pk_mul_f32 v[76:77], v[76:77], v[190:191] op_sel_hi:[1,0]
	v_pk_mul_f32 v[74:75], v[74:75], v[190:191] op_sel_hi:[1,0]
	v_pk_mul_f32 v[72:73], v[72:73], v[190:191] op_sel_hi:[1,0]
	v_pk_mul_f32 v[70:71], v[70:71], v[190:191] op_sel_hi:[1,0]
	v_pk_mul_f32 v[68:69], v[68:69], v[190:191] op_sel_hi:[1,0]
	v_pk_mul_f32 v[66:67], v[66:67], v[190:191] op_sel_hi:[1,0]
	v_pk_mul_f32 v[64:65], v[64:65], v[186:187] op_sel_hi:[1,0]
	v_pk_mul_f32 v[62:63], v[62:63], v[186:187] op_sel_hi:[1,0]
	v_pk_mul_f32 v[60:61], v[60:61], v[186:187] op_sel_hi:[1,0]
	v_pk_mul_f32 v[58:59], v[58:59], v[186:187] op_sel_hi:[1,0]
	v_pk_mul_f32 v[56:57], v[56:57], v[186:187] op_sel_hi:[1,0]
	v_pk_mul_f32 v[54:55], v[54:55], v[186:187] op_sel_hi:[1,0]
	v_pk_mul_f32 v[52:53], v[52:53], v[186:187] op_sel_hi:[1,0]
	v_pk_mul_f32 v[50:51], v[50:51], v[186:187] op_sel_hi:[1,0]
	v_pk_mul_f32 v[48:49], v[48:49], v[154:155] op_sel_hi:[1,0]
	v_pk_mul_f32 v[46:47], v[46:47], v[154:155] op_sel_hi:[1,0]
	v_pk_mul_f32 v[44:45], v[44:45], v[154:155] op_sel_hi:[1,0]
	v_pk_mul_f32 v[42:43], v[42:43], v[154:155] op_sel_hi:[1,0]
	v_pk_mul_f32 v[40:41], v[40:41], v[154:155] op_sel_hi:[1,0]
	v_pk_mul_f32 v[38:39], v[38:39], v[154:155] op_sel_hi:[1,0]
	v_pk_mul_f32 v[36:37], v[36:37], v[154:155] op_sel_hi:[1,0]
	v_pk_mul_f32 v[34:35], v[34:35], v[154:155] op_sel_hi:[1,0]
	v_pk_mul_f32 v[32:33], v[32:33], v[152:153] op_sel_hi:[1,0]
	v_pk_mul_f32 v[30:31], v[30:31], v[152:153] op_sel_hi:[1,0]
	v_pk_mul_f32 v[28:29], v[28:29], v[152:153] op_sel_hi:[1,0]
	v_pk_mul_f32 v[26:27], v[26:27], v[152:153] op_sel_hi:[1,0]
	v_pk_mul_f32 v[24:25], v[24:25], v[152:153] op_sel_hi:[1,0]
	v_pk_mul_f32 v[22:23], v[22:23], v[152:153] op_sel_hi:[1,0]
	v_pk_mul_f32 v[20:21], v[20:21], v[152:153] op_sel_hi:[1,0]
	v_pk_mul_f32 v[18:19], v[18:19], v[152:153] op_sel_hi:[1,0]
	v_add_u32_e32 v152, v178, v164
	s_mov_b32 s26, 0x8000
	s_mov_b64 s[4:5], 0
	s_mov_b32 s48, 0x88000
.LBB0_1131:
	s_add_i32 s50, s48, 0xffff8000
	s_and_b32 s50, s50, 0x8000
	s_add_i32 s50, s50, 0
	s_add_i32 s49, s26, 0
	s_add_i32 s50, s50, 0x18000
	v_add_u32_e32 v154, s50, v157
	v_add_u32_e32 v165, s49, v161
	v_add_u32_e32 v222, s50, v155
	v_add_u32_e32 v164, s50, v156
	s_branch .Lrot_o2

.Lrot_o2:
	ds_read_b64_tr_b16 v[184:185], v154
	ds_read_b64_tr_b16 v[186:187], v154 offset:2048
	ds_read_b64_tr_b16 v[188:189], v164
	ds_read_b64_tr_b16 v[190:191], v164 offset:2048
	ds_read_b128 v[192:195], v165
	ds_read_b128 v[196:199], v165 offset:2048
	ds_read_b64_tr_b16 v[200:201], v222
	ds_read_b64_tr_b16 v[202:203], v222 offset:2048
	v_add_u32_e32 v224, s50, v153
	ds_read_b64_tr_b16 v[204:205], v224
	ds_read_b64_tr_b16 v[206:207], v224 offset:2048
	ds_read_b128 v[208:211], v165 offset:4096
	s_waitcnt lgkmcnt(6)
	v_mfma_f32_16x16x32_bf16 v[18:21], v[184:187], v[192:195], v[18:21]
	s_add_i32 s50, s8, 0
	v_add_u32_e32 v212, 0xfff40000, v152
	s_add_i32 s51, s50, s44
	v_mfma_f32_16x16x32_bf16 v[22:25], v[188:191], v[192:195], v[22:25]
	s_mov_b32 s52, m0
	s_mov_b32 m0, s51
	s_nop 0
	global_load_lds_dwordx4 v212, s[10:11]
	s_mov_b32 m0, s52
	s_waitcnt lgkmcnt(3)
	v_mfma_f32_16x16x32_bf16 v[26:29], v[200:203], v[192:195], v[26:29]
	s_waitcnt lgkmcnt(1)
	v_mfma_f32_16x16x32_bf16 v[30:33], v[204:207], v[192:195], v[30:33]
	v_mfma_f32_16x16x32_bf16 v[34:37], v[184:187], v[196:199], v[34:37]
	ds_read_b128 v[192:195], v165 offset:6144
	v_add_u32_e32 v212, 0xfff80000, v152
	s_add_i32 s51, s50, s45
	v_mfma_f32_16x16x32_bf16 v[38:41], v[188:191], v[196:199], v[38:41]
	s_mov_b32 s52, m0
	s_mov_b32 m0, s51
	s_nop 0
	global_load_lds_dwordx4 v212, s[10:11]
	s_mov_b32 m0, s52
	v_mfma_f32_16x16x32_bf16 v[42:45], v[200:203], v[196:199], v[42:45]
	v_mfma_f32_16x16x32_bf16 v[46:49], v[204:207], v[196:199], v[46:49]
	s_waitcnt lgkmcnt(1)
	v_mfma_f32_16x16x32_bf16 v[50:53], v[184:187], v[208:211], v[50:53]
	ds_read_b128 v[196:199], v165 offset:8192
	v_add_u32_e32 v212, 0xfffc0000, v152
	s_add_i32 s51, s50, s46
	v_mfma_f32_16x16x32_bf16 v[54:57], v[188:191], v[208:211], v[54:57]
	s_mov_b32 s52, m0
	s_mov_b32 m0, s51
	s_nop 0
	global_load_lds_dwordx4 v212, s[10:11]
	s_mov_b32 m0, s52
	v_mfma_f32_16x16x32_bf16 v[58:61], v[200:203], v[208:211], v[58:61]
	v_mfma_f32_16x16x32_bf16 v[62:65], v[204:207], v[208:211], v[62:65]
	s_waitcnt lgkmcnt(1)
	v_mfma_f32_16x16x32_bf16 v[66:69], v[184:187], v[192:195], v[66:69]
	ds_read_b128 v[208:211], v165 offset:10240
	s_add_i32 s50, s50, s47
	s_mov_b32 s51, m0
	s_mov_b32 m0, s50
	s_nop 0
	global_load_lds_dwordx4 v152, s[10:11]
	s_mov_b32 m0, s51
	v_mfma_f32_16x16x32_bf16 v[70:73], v[188:191], v[192:195], v[70:73]
	v_mfma_f32_16x16x32_bf16 v[74:77], v[200:203], v[192:195], v[74:77]
	v_mfma_f32_16x16x32_bf16 v[78:81], v[204:207], v[192:195], v[78:81]
	ds_read_b128 v[192:195], v165 offset:12288
	ds_read_b64_tr_b16 v[212:213], v154 offset:16384
	ds_read_b64_tr_b16 v[214:215], v154 offset:18432
	s_waitcnt lgkmcnt(4)
	v_mfma_f32_16x16x32_bf16 v[82:85], v[184:187], v[196:199], v[82:85]
	v_mfma_f32_16x16x32_bf16 v[86:89], v[188:191], v[196:199], v[86:89]
	v_mfma_f32_16x16x32_bf16 v[90:93], v[200:203], v[196:199], v[90:93]
	v_mfma_f32_16x16x32_bf16 v[94:97], v[204:207], v[196:199], v[94:97]
	ds_read_b128 v[196:199], v165 offset:14336
	ds_read_b64_tr_b16 v[216:217], v164 offset:16384
	ds_read_b64_tr_b16 v[218:219], v164 offset:18432
	s_waitcnt lgkmcnt(6)
	v_mfma_f32_16x16x32_bf16 v[98:101], v[184:187], v[208:211], v[98:101]
	v_mfma_f32_16x16x32_bf16 v[102:105], v[188:191], v[208:211], v[102:105]
	v_mfma_f32_16x16x32_bf16 v[106:109], v[200:203], v[208:211], v[106:109]
	v_mfma_f32_16x16x32_bf16 v[110:113], v[204:207], v[208:211], v[110:113]
	v_add_u32_e32 v154, s49, v162
	ds_read_b128 v[208:211], v154
	ds_read_b64_tr_b16 v[220:221], v222 offset:16384
	ds_read_b64_tr_b16 v[222:223], v222 offset:18432
	s_waitcnt lgkmcnt(8)
	v_mfma_f32_16x16x32_bf16 v[114:117], v[184:187], v[192:195], v[114:117]
	v_mfma_f32_16x16x32_bf16 v[118:121], v[188:191], v[192:195], v[118:121]
	v_mfma_f32_16x16x32_bf16 v[122:125], v[200:203], v[192:195], v[122:125]
	v_mfma_f32_16x16x32_bf16 v[126:129], v[204:207], v[192:195], v[126:129]
	s_waitcnt lgkmcnt(5)
	v_mfma_f32_16x16x32_bf16 v[130:133], v[184:187], v[196:199], v[130:133]
	ds_read_b128 v[184:187], v154 offset:2048
	s_and_b32 s49, s48, 0x8000
	v_mfma_f32_16x16x32_bf16 v[134:137], v[188:191], v[196:199], v[134:137]
	ds_read_b64_tr_b16 v[188:189], v224 offset:16384
	ds_read_b64_tr_b16 v[190:191], v224 offset:18432
	v_mfma_f32_16x16x32_bf16 v[138:141], v[200:203], v[196:199], v[138:141]
	v_mfma_f32_16x16x32_bf16 v[142:145], v[204:207], v[196:199], v[142:145]
	s_waitcnt lgkmcnt(5)
	v_mfma_f32_16x16x32_bf16 v[18:21], v[212:215], v[208:211], v[18:21]
	ds_read_b128 v[192:195], v154 offset:4096
	v_add_u32_e32 v164, s49, v163
	s_add_u32 s49, s6, s4
	v_mfma_f32_16x16x32_bf16 v[22:25], v[216:219], v[208:211], v[22:25]
	s_addc_u32 s52, s7, s5
	s_waitcnt vmcnt(7)
	s_add_u32 s50, s49, 0x480000
	s_waitcnt lgkmcnt(4)
	v_mfma_f32_16x16x32_bf16 v[26:29], v[220:223], v[208:211], v[26:29]
	ds_write_b128 v164, v[14:17]
	s_addc_u32 s51, s52, 0
	global_load_dwordx4 v[14:17], v173, s[50:51]
	s_waitcnt lgkmcnt(2)
	v_mfma_f32_16x16x32_bf16 v[30:33], v[188:191], v[208:211], v[30:33]
	v_mfma_f32_16x16x32_bf16 v[34:37], v[212:215], v[184:187], v[34:37]
	ds_read_b128 v[196:199], v154 offset:6144
	s_waitcnt vmcnt(7)
	s_add_u32 s50, s49, 0x490000
	v_mfma_f32_16x16x32_bf16 v[38:41], v[216:219], v[184:187], v[38:41]
	ds_write_b128 v164, v[10:13] offset:8192
	s_addc_u32 s51, s52, 0
	global_load_dwordx4 v[10:13], v173, s[50:51]
	v_mfma_f32_16x16x32_bf16 v[42:45], v[220:223], v[184:187], v[42:45]
	v_mfma_f32_16x16x32_bf16 v[46:49], v[188:191], v[184:187], v[46:49]
	s_waitcnt lgkmcnt(3)
	v_mfma_f32_16x16x32_bf16 v[50:53], v[212:215], v[192:195], v[50:53]
	ds_read_b128 v[184:187], v154 offset:8192
	s_waitcnt vmcnt(7)
	s_add_u32 s50, s49, 0x4a0000
	v_mfma_f32_16x16x32_bf16 v[54:57], v[216:219], v[192:195], v[54:57]
	ds_write_b128 v164, v[6:9] offset:16384
	s_addc_u32 s51, s52, 0
	global_load_dwordx4 v[6:9], v173, s[50:51]
	v_mfma_f32_16x16x32_bf16 v[58:61], v[220:223], v[192:195], v[58:61]
	v_mfma_f32_16x16x32_bf16 v[62:65], v[188:191], v[192:195], v[62:65]
	s_waitcnt lgkmcnt(3)
	v_mfma_f32_16x16x32_bf16 v[66:69], v[212:215], v[196:199], v[66:69]
	ds_read_b128 v[192:195], v154 offset:10240
	s_waitcnt vmcnt(7)
	s_add_u32 s50, s49, 0x4b0000
	v_mfma_f32_16x16x32_bf16 v[70:73], v[216:219], v[196:199], v[70:73]
	ds_write_b128 v164, v[2:5] offset:24576
	s_addc_u32 s51, s52, 0
	global_load_dwordx4 v[2:5], v173, s[50:51]
	v_mfma_f32_16x16x32_bf16 v[74:77], v[220:223], v[196:199], v[74:77]
	v_mfma_f32_16x16x32_bf16 v[78:81], v[188:191], v[196:199], v[78:81]
	s_waitcnt lgkmcnt(3)
	v_mfma_f32_16x16x32_bf16 v[82:85], v[212:215], v[184:187], v[82:85]
	ds_read_b128 v[196:199], v154 offset:12288
	v_mfma_f32_16x16x32_bf16 v[86:89], v[216:219], v[184:187], v[86:89]
	v_mfma_f32_16x16x32_bf16 v[90:93], v[220:223], v[184:187], v[90:93]
	v_mfma_f32_16x16x32_bf16 v[94:97], v[188:191], v[184:187], v[94:97]
	s_waitcnt lgkmcnt(2)
	v_mfma_f32_16x16x32_bf16 v[98:101], v[212:215], v[192:195], v[98:101]
	ds_read_b128 v[184:187], v154 offset:14336
	v_mfma_f32_16x16x32_bf16 v[102:105], v[216:219], v[192:195], v[102:105]
	v_mfma_f32_16x16x32_bf16 v[106:109], v[220:223], v[192:195], v[106:109]
	v_mfma_f32_16x16x32_bf16 v[110:113], v[188:191], v[192:195], v[110:113]
	s_waitcnt lgkmcnt(1)
	v_mfma_f32_16x16x32_bf16 v[114:117], v[212:215], v[196:199], v[114:117]
	v_mfma_f32_16x16x32_bf16 v[118:121], v[216:219], v[196:199], v[118:121]
	v_mfma_f32_16x16x32_bf16 v[122:125], v[220:223], v[196:199], v[122:125]
	v_mfma_f32_16x16x32_bf16 v[126:129], v[188:191], v[196:199], v[126:129]
	s_waitcnt lgkmcnt(0)
	v_mfma_f32_16x16x32_bf16 v[130:133], v[212:215], v[184:187], v[130:133]
	v_mfma_f32_16x16x32_bf16 v[134:137], v[216:219], v[184:187], v[134:137]
	v_mfma_f32_16x16x32_bf16 v[138:141], v[220:223], v[184:187], v[138:141]
	v_mfma_f32_16x16x32_bf16 v[142:145], v[188:191], v[184:187], v[142:145]
	s_add_i32 s49, s26, 0x8000
	s_cmp_lg_u32 s26, 0x10000
	s_cselect_b32 s26, s49, 0
	s_add_i32 s49, s8, 0x8000
	s_cmp_lg_u32 s8, 0x10000
	s_cselect_b32 s8, s49, 0
	s_add_u32 s4, s4, 0x40000
	s_addc_u32 s5, s5, 0
	s_add_i32 s48, s48, 0x8000
	v_add_u32_e32 v152, 0x80, v152
	s_add_i32 s50, s48, 0xffff8000
	s_and_b32 s50, s50, 0x8000
	s_add_i32 s50, s50, 0
	s_add_i32 s49, s26, 0
	s_add_i32 s50, s50, 0x18000
	v_add_u32_e32 v154, s50, v157
	v_add_u32_e32 v165, s49, v161
	v_add_u32_e32 v222, s50, v155
	v_add_u32_e32 v164, s50, v156
	s_waitcnt lgkmcnt(0)
	s_cmp_lg_u32 s4, 0x380000
	s_cbranch_scc1 .Lrot_o2_head
	s_barrier
	s_add_i32 s4, 0, 0x18000
	v_add_u32_e32 v152, s4, v157
	v_add_u32_e32 v220, 0, v161
	v_add_u32_e32 v161, s4, v155
	v_add_u32_e32 v221, s4, v153
	ds_read_b64_tr_b16 v[184:185], v152
	ds_read_b64_tr_b16 v[186:187], v152 offset:2048
	v_add_u32_e32 v154, s4, v156
	ds_read_b128 v[188:191], v220
	ds_read_b64_tr_b16 v[192:193], v154
	ds_read_b64_tr_b16 v[194:195], v154 offset:2048
	ds_read_b128 v[196:199], v220 offset:2048
	ds_read_b64_tr_b16 v[200:201], v161
	ds_read_b64_tr_b16 v[202:203], v161 offset:2048
	ds_read_b64_tr_b16 v[204:205], v221
	ds_read_b64_tr_b16 v[206:207], v221 offset:2048
	ds_read_b128 v[208:211], v220 offset:4096
	s_waitcnt lgkmcnt(8)
	v_mfma_f32_16x16x32_bf16 v[18:21], v[184:187], v[188:191], v[18:21]
	s_waitcnt lgkmcnt(6)
	v_mfma_f32_16x16x32_bf16 v[22:25], v[192:195], v[188:191], v[22:25]
	s_waitcnt lgkmcnt(3)
	v_mfma_f32_16x16x32_bf16 v[26:29], v[200:203], v[188:191], v[26:29]
	s_waitcnt lgkmcnt(1)
	v_mfma_f32_16x16x32_bf16 v[30:33], v[204:207], v[188:191], v[30:33]
	ds_read_b128 v[188:191], v220 offset:6144
	v_mfma_f32_16x16x32_bf16 v[34:37], v[184:187], v[196:199], v[34:37]
	v_mfma_f32_16x16x32_bf16 v[38:41], v[192:195], v[196:199], v[38:41]
	v_mfma_f32_16x16x32_bf16 v[42:45], v[200:203], v[196:199], v[42:45]
	v_mfma_f32_16x16x32_bf16 v[46:49], v[204:207], v[196:199], v[46:49]
	ds_read_b128 v[196:199], v220 offset:8192
	s_waitcnt lgkmcnt(2)
	v_mfma_f32_16x16x32_bf16 v[50:53], v[184:187], v[208:211], v[50:53]
	v_mfma_f32_16x16x32_bf16 v[54:57], v[192:195], v[208:211], v[54:57]
	v_mfma_f32_16x16x32_bf16 v[58:61], v[200:203], v[208:211], v[58:61]
	v_mfma_f32_16x16x32_bf16 v[62:65], v[204:207], v[208:211], v[62:65]
	ds_read_b128 v[208:211], v220 offset:10240
	s_waitcnt lgkmcnt(2)
	v_mfma_f32_16x16x32_bf16 v[66:69], v[184:187], v[188:191], v[66:69]
	v_mfma_f32_16x16x32_bf16 v[70:73], v[192:195], v[188:191], v[70:73]
	v_mfma_f32_16x16x32_bf16 v[74:77], v[200:203], v[188:191], v[74:77]
	v_mfma_f32_16x16x32_bf16 v[78:81], v[204:207], v[188:191], v[78:81]
	ds_read_b128 v[188:191], v220 offset:12288
	ds_read_b64_tr_b16 v[212:213], v152 offset:16384
	ds_read_b64_tr_b16 v[214:215], v152 offset:18432
	s_waitcnt lgkmcnt(4)
	v_mfma_f32_16x16x32_bf16 v[82:85], v[184:187], v[196:199], v[82:85]
	v_mfma_f32_16x16x32_bf16 v[86:89], v[192:195], v[196:199], v[86:89]
	v_mfma_f32_16x16x32_bf16 v[90:93], v[200:203], v[196:199], v[90:93]
	v_mfma_f32_16x16x32_bf16 v[94:97], v[204:207], v[196:199], v[94:97]
	ds_read_b128 v[196:199], v220 offset:14336
	ds_read_b64_tr_b16 v[216:217], v154 offset:16384
	ds_read_b64_tr_b16 v[218:219], v154 offset:18432
	s_waitcnt lgkmcnt(6)
	v_mfma_f32_16x16x32_bf16 v[98:101], v[184:187], v[208:211], v[98:101]
	v_mfma_f32_16x16x32_bf16 v[102:105], v[192:195], v[208:211], v[102:105]
	v_mfma_f32_16x16x32_bf16 v[106:109], v[200:203], v[208:211], v[106:109]
	v_mfma_f32_16x16x32_bf16 v[110:113], v[204:207], v[208:211], v[110:113]
	v_add_u32_e32 v236, 0, v162
	ds_read_b128 v[162:165], v236
	ds_read_b64_tr_b16 v[208:209], v161 offset:16384
	ds_read_b64_tr_b16 v[210:211], v161 offset:18432
	s_waitcnt lgkmcnt(8)
	v_mfma_f32_16x16x32_bf16 v[114:117], v[184:187], v[188:191], v[114:117]
	v_mfma_f32_16x16x32_bf16 v[118:121], v[192:195], v[188:191], v[118:121]
	v_mfma_f32_16x16x32_bf16 v[122:125], v[200:203], v[188:191], v[122:125]
	v_mfma_f32_16x16x32_bf16 v[126:129], v[204:207], v[188:191], v[126:129]
	s_waitcnt lgkmcnt(5)
	v_mfma_f32_16x16x32_bf16 v[130:133], v[184:187], v[196:199], v[130:133]
	ds_read_b128 v[184:187], v236 offset:2048
	ds_read_b64_tr_b16 v[188:189], v221 offset:16384
	ds_read_b64_tr_b16 v[190:191], v221 offset:18432
	v_mfma_f32_16x16x32_bf16 v[134:137], v[192:195], v[196:199], v[134:137]
	v_mfma_f32_16x16x32_bf16 v[138:141], v[200:203], v[196:199], v[138:141]
	v_mfma_f32_16x16x32_bf16 v[142:145], v[204:207], v[196:199], v[142:145]
	ds_read_b128 v[192:195], v236 offset:4096
	s_waitcnt vmcnt(3)
	v_add_u32_e32 v152, s34, v160
	s_waitcnt lgkmcnt(6)
	v_mfma_f32_16x16x32_bf16 v[18:21], v[212:215], v[162:165], v[18:21]
	ds_write_b128 v152, v[14:17]
	v_mfma_f32_16x16x32_bf16 v[22:25], v[216:219], v[162:165], v[22:25]
	s_waitcnt lgkmcnt(5)
	v_mfma_f32_16x16x32_bf16 v[26:29], v[208:211], v[162:165], v[26:29]
	s_waitcnt lgkmcnt(2)
	v_mfma_f32_16x16x32_bf16 v[14:17], v[188:191], v[162:165], v[30:33]
	v_mfma_f32_16x16x32_bf16 v[30:33], v[212:215], v[184:187], v[34:37]
	v_mfma_f32_16x16x32_bf16 v[34:37], v[216:219], v[184:187], v[38:41]
	v_mfma_f32_16x16x32_bf16 v[38:41], v[208:211], v[184:187], v[42:45]
	s_nop 2
	ds_read_b128 v[42:45], v236 offset:6144
	s_waitcnt vmcnt(2)
	ds_write_b128 v152, v[10:13] offset:8192
	v_mfma_f32_16x16x32_bf16 v[10:13], v[188:191], v[184:187], v[46:49]
	s_waitcnt lgkmcnt(3)
	v_mfma_f32_16x16x32_bf16 v[46:49], v[212:215], v[192:195], v[50:53]
	v_mfma_f32_16x16x32_bf16 v[50:53], v[216:219], v[192:195], v[54:57]
	v_mfma_f32_16x16x32_bf16 v[54:57], v[208:211], v[192:195], v[58:61]
	s_nop 2
	ds_read_b128 v[58:61], v236 offset:8192
	s_waitcnt vmcnt(1)
	ds_write_b128 v152, v[6:9] offset:16384
	v_mfma_f32_16x16x32_bf16 v[6:9], v[188:191], v[192:195], v[62:65]
	s_waitcnt lgkmcnt(3)
	v_mfma_f32_16x16x32_bf16 v[62:65], v[212:215], v[42:45], v[66:69]
	v_mfma_f32_16x16x32_bf16 v[66:69], v[216:219], v[42:45], v[70:73]
	v_mfma_f32_16x16x32_bf16 v[70:73], v[208:211], v[42:45], v[74:77]
	s_nop 2
	ds_read_b128 v[74:77], v236 offset:10240
	s_waitcnt vmcnt(0)
	ds_write_b128 v152, v[2:5] offset:24576
	v_mfma_f32_16x16x32_bf16 v[2:5], v[188:191], v[42:45], v[78:81]
	s_waitcnt lgkmcnt(3)
	v_mfma_f32_16x16x32_bf16 v[78:81], v[216:219], v[58:61], v[86:89]
	s_nop 2
	ds_read_b128 v[86:89], v236 offset:12288
	v_mfma_f32_16x16x32_bf16 v[42:45], v[212:215], v[58:61], v[82:85]
	v_mfma_f32_16x16x32_bf16 v[82:85], v[208:211], v[58:61], v[90:93]
	v_mfma_f32_16x16x32_bf16 v[58:61], v[188:191], v[58:61], v[94:97]
	s_waitcnt lgkmcnt(2)
	v_mfma_f32_16x16x32_bf16 v[94:97], v[216:219], v[74:77], v[102:105]
	s_nop 2
	ds_read_b128 v[102:105], v236 offset:14336
	v_mfma_f32_16x16x32_bf16 v[90:93], v[212:215], v[74:77], v[98:101]
	v_mfma_f32_16x16x32_bf16 v[98:101], v[208:211], v[74:77], v[106:109]
	v_mfma_f32_16x16x32_bf16 v[74:77], v[188:191], v[74:77], v[110:113]
	s_waitcnt lgkmcnt(1)
	v_mfma_f32_16x16x32_bf16 v[106:109], v[212:215], v[86:89], v[114:117]
	v_mfma_f32_16x16x32_bf16 v[110:113], v[216:219], v[86:89], v[118:121]
	v_mfma_f32_16x16x32_bf16 v[114:117], v[208:211], v[86:89], v[122:125]
	v_mfma_f32_16x16x32_bf16 v[86:89], v[188:191], v[86:89], v[126:129]
	s_waitcnt lgkmcnt(0)
	v_mfma_f32_16x16x32_bf16 v[118:121], v[212:215], v[102:105], v[130:133]
	v_mfma_f32_16x16x32_bf16 v[122:125], v[216:219], v[102:105], v[134:137]
	v_mfma_f32_16x16x32_bf16 v[126:129], v[208:211], v[102:105], v[138:141]
	v_mfma_f32_16x16x32_bf16 v[102:105], v[188:191], v[102:105], v[142:145]
	s_waitcnt lgkmcnt(0)
	s_barrier
	v_add_u32_e32 v164, s34, v157
	v_add_u32_e32 v165, s34, v156
	v_add_u32_e32 v198, s34, v155
	ds_read_b64_tr_b16 v[130:131], v164
	ds_read_b64_tr_b16 v[132:133], v164 offset:2048
	ds_read_b64_tr_b16 v[134:135], v165
	ds_read_b64_tr_b16 v[136:137], v165 offset:2048
	ds_read_b128 v[138:141], v220 offset:32768
	ds_read_b64_tr_b16 v[142:143], v198
	ds_read_b128 v[154:157], v220 offset:34816
	ds_read_b128 v[160:163], v220 offset:36864
	ds_read_b64_tr_b16 v[144:145], v198 offset:2048
	v_add_u32_e32 v200, s34, v153
	ds_read_b64_tr_b16 v[184:185], v200
	ds_read_b64_tr_b16 v[186:187], v200 offset:2048
	s_waitcnt lgkmcnt(6)
	v_mfma_f32_16x16x32_bf16 v[18:21], v[130:133], v[138:141], v[18:21]
	v_mfma_f32_16x16x32_bf16 v[22:25], v[134:137], v[138:141], v[22:25]
	s_waitcnt lgkmcnt(2)
	v_mfma_f32_16x16x32_bf16 v[26:29], v[142:145], v[138:141], v[26:29]
	s_waitcnt lgkmcnt(0)
	v_mfma_f32_16x16x32_bf16 v[14:17], v[184:187], v[138:141], v[14:17]
	ds_read_b128 v[138:141], v220 offset:38912
	v_mfma_f32_16x16x32_bf16 v[30:33], v[130:133], v[154:157], v[30:33]
	v_mfma_f32_16x16x32_bf16 v[34:37], v[134:137], v[154:157], v[34:37]
	v_mfma_f32_16x16x32_bf16 v[38:41], v[142:145], v[154:157], v[38:41]
	v_mfma_f32_16x16x32_bf16 v[10:13], v[184:187], v[154:157], v[10:13]
	ds_read_b128 v[152:155], v220 offset:40960
	v_mfma_f32_16x16x32_bf16 v[46:49], v[130:133], v[160:163], v[46:49]
	v_mfma_f32_16x16x32_bf16 v[50:53], v[134:137], v[160:163], v[50:53]
	v_mfma_f32_16x16x32_bf16 v[54:57], v[142:145], v[160:163], v[54:57]
	v_mfma_f32_16x16x32_bf16 v[6:9], v[184:187], v[160:163], v[6:9]
	ds_read_b128 v[160:163], v220 offset:43008
	s_waitcnt lgkmcnt(2)
	v_mfma_f32_16x16x32_bf16 v[62:65], v[130:133], v[138:141], v[62:65]
	v_mfma_f32_16x16x32_bf16 v[66:69], v[134:137], v[138:141], v[66:69]
	v_mfma_f32_16x16x32_bf16 v[70:73], v[142:145], v[138:141], v[70:73]
	v_mfma_f32_16x16x32_bf16 v[2:5], v[184:187], v[138:141], v[2:5]
	s_waitcnt lgkmcnt(1)
	v_mfma_f32_16x16x32_bf16 v[138:141], v[134:137], v[152:155], v[78:81]
	s_nop 2
	ds_read_b128 v[78:81], v220 offset:45056
	ds_read_b64_tr_b16 v[188:189], v164 offset:16384
	ds_read_b64_tr_b16 v[190:191], v164 offset:18432
	v_mfma_f32_16x16x32_bf16 v[42:45], v[130:133], v[152:155], v[42:45]
	v_mfma_f32_16x16x32_bf16 v[82:85], v[142:145], v[152:155], v[82:85]
	v_mfma_f32_16x16x32_bf16 v[152:155], v[184:187], v[152:155], v[58:61]
	s_nop 2
	ds_read_b128 v[58:61], v220 offset:47104
	ds_read_b64_tr_b16 v[192:193], v165 offset:16384
	ds_read_b64_tr_b16 v[194:195], v165 offset:18432
	s_waitcnt lgkmcnt(6)
	v_mfma_f32_16x16x32_bf16 v[90:93], v[130:133], v[160:163], v[90:93]
	v_mfma_f32_16x16x32_bf16 v[94:97], v[134:137], v[160:163], v[94:97]
	v_mfma_f32_16x16x32_bf16 v[98:101], v[142:145], v[160:163], v[98:101]
	v_mfma_f32_16x16x32_bf16 v[160:163], v[184:187], v[160:163], v[74:77]
	s_nop 2
	ds_read_b128 v[74:77], v236 offset:32768
	ds_read_b64_tr_b16 v[196:197], v198 offset:16384
	ds_read_b64_tr_b16 v[198:199], v198 offset:18432
	s_waitcnt lgkmcnt(8)
	v_mfma_f32_16x16x32_bf16 v[106:109], v[130:133], v[78:81], v[106:109]
	v_mfma_f32_16x16x32_bf16 v[110:113], v[134:137], v[78:81], v[110:113]
	v_mfma_f32_16x16x32_bf16 v[114:117], v[142:145], v[78:81], v[114:117]
	v_mfma_f32_16x16x32_bf16 v[86:89], v[184:187], v[78:81], v[86:89]
	s_waitcnt lgkmcnt(5)
	v_mfma_f32_16x16x32_bf16 v[118:121], v[130:133], v[58:61], v[118:121]
	ds_read_b128 v[78:81], v236 offset:34816
	ds_read_b64_tr_b16 v[130:131], v200 offset:16384
	ds_read_b64_tr_b16 v[132:133], v200 offset:18432
	v_mfma_f32_16x16x32_bf16 v[122:125], v[134:137], v[58:61], v[122:125]
	v_mfma_f32_16x16x32_bf16 v[126:129], v[142:145], v[58:61], v[126:129]
	v_mfma_f32_16x16x32_bf16 v[102:105], v[184:187], v[58:61], v[102:105]
	s_waitcnt lgkmcnt(5)
	v_mfma_f32_16x16x32_bf16 v[134:137], v[188:191], v[74:77], v[18:21]
	s_nop 2
	ds_read_b128 v[18:21], v236 offset:36864
	v_mfma_f32_16x16x32_bf16 v[142:145], v[192:195], v[74:77], v[22:25]
	s_waitcnt lgkmcnt(4)
	v_mfma_f32_16x16x32_bf16 v[184:187], v[196:199], v[74:77], v[26:29]
	s_waitcnt lgkmcnt(1)
	v_mfma_f32_16x16x32_bf16 v[14:17], v[130:133], v[74:77], v[14:17]
	ds_read_b128 v[22:25], v236 offset:38912
	v_mfma_f32_16x16x32_bf16 v[200:203], v[188:191], v[78:81], v[30:33]
	v_mfma_f32_16x16x32_bf16 v[204:207], v[192:195], v[78:81], v[34:37]
	v_mfma_f32_16x16x32_bf16 v[208:211], v[196:199], v[78:81], v[38:41]
	v_mfma_f32_16x16x32_bf16 v[10:13], v[130:133], v[78:81], v[10:13]
	ds_read_b128 v[26:29], v236 offset:40960
	s_waitcnt lgkmcnt(2)
	v_mfma_f32_16x16x32_bf16 v[212:215], v[188:191], v[18:21], v[46:49]
	v_mfma_f32_16x16x32_bf16 v[216:219], v[192:195], v[18:21], v[50:53]
	v_mfma_f32_16x16x32_bf16 v[220:223], v[196:199], v[18:21], v[54:57]
	v_mfma_f32_16x16x32_bf16 v[6:9], v[130:133], v[18:21], v[6:9]
	ds_read_b128 v[18:21], v236 offset:43008
	s_waitcnt lgkmcnt(2)
	v_mfma_f32_16x16x32_bf16 v[224:227], v[188:191], v[22:25], v[62:65]
	v_mfma_f32_16x16x32_bf16 v[228:231], v[192:195], v[22:25], v[66:69]
	v_mfma_f32_16x16x32_bf16 v[232:235], v[196:199], v[22:25], v[70:73]
	v_mfma_f32_16x16x32_bf16 v[2:5], v[130:133], v[22:25], v[2:5]
	ds_read_b128 v[22:25], v236 offset:45056
	s_waitcnt lgkmcnt(2)
	v_mfma_f32_16x16x32_bf16 v[78:81], v[188:191], v[26:29], v[42:45]
	v_mfma_f32_16x16x32_bf16 v[74:77], v[192:195], v[26:29], v[138:141]
	v_mfma_f32_16x16x32_bf16 v[58:61], v[196:199], v[26:29], v[82:85]
	v_mfma_f32_16x16x32_bf16 v[62:65], v[130:133], v[26:29], v[152:155]
	s_nop 1
	ds_read_b128 v[82:85], v236 offset:47104
	s_waitcnt lgkmcnt(2)
	v_mfma_f32_16x16x32_bf16 v[70:73], v[188:191], v[18:21], v[90:93]
	v_mfma_f32_16x16x32_bf16 v[66:69], v[192:195], v[18:21], v[94:97]
	v_mfma_f32_16x16x32_bf16 v[50:53], v[196:199], v[18:21], v[98:101]
	v_mfma_f32_16x16x32_bf16 v[54:57], v[130:133], v[18:21], v[160:163]
	s_waitcnt lgkmcnt(1)
	v_mfma_f32_16x16x32_bf16 v[46:49], v[188:191], v[22:25], v[106:109]
	v_mfma_f32_16x16x32_bf16 v[42:45], v[192:195], v[22:25], v[110:113]
	v_mfma_f32_16x16x32_bf16 v[38:41], v[196:199], v[22:25], v[114:117]
	v_mfma_f32_16x16x32_bf16 v[30:33], v[130:133], v[22:25], v[86:89]
	s_waitcnt lgkmcnt(0)
	v_mfma_f32_16x16x32_bf16 v[34:37], v[188:191], v[82:85], v[118:121]
	v_mfma_f32_16x16x32_bf16 v[26:29], v[192:195], v[82:85], v[122:125]
	v_mfma_f32_16x16x32_bf16 v[22:25], v[196:199], v[82:85], v[126:129]
	v_mfma_f32_16x16x32_bf16 v[18:21], v[130:133], v[82:85], v[102:105]
	v_mov_b32_e32 v236, v1
	v_mov_b32_e32 v237, v166
	s_waitcnt lgkmcnt(0)
	s_barrier
	s_lshl_b32 s4, s42, 6
	v_and_or_b32 v82, v236, 63, v181
	v_lshlrev_b32_e32 v122, 2, v82
	ds_bpermute_b32 v82, v122, v183
	v_xor_b32_e32 v239, 0x80, v122
	s_or_b32 s4, s4, s24
	v_lshlrev_b32_e32 v240, 3, v237
	s_waitcnt lgkmcnt(0)
	v_pk_mul_f32 v[162:163], v[136:137], v[82:83] op_sel_hi:[1,0]
	v_pk_mul_f32 v[164:165], v[134:135], v[82:83] op_sel_hi:[1,0]
	v_pk_mul_f32 v[152:153], v[144:145], v[82:83] op_sel_hi:[1,0]
	v_pk_mul_f32 v[154:155], v[142:143], v[82:83] op_sel_hi:[1,0]
	v_add_u32_e32 v83, 16, v236
	v_and_or_b32 v83, v83, 63, v181
	v_lshlrev_b32_e32 v238, 2, v83
	ds_bpermute_b32 v84, v238, v183
	v_pk_mul_f32 v[138:139], v[14:15], v[82:83] op_sel_hi:[1,0]
	ds_bpermute_b32 v14, v239, v183
	v_add_u32_e32 v144, s43, v236
	v_ashrrev_i32_e32 v145, 31, v144
	s_waitcnt lgkmcnt(1)
	v_pk_mul_f32 v[116:117], v[10:11], v[84:85] op_sel_hi:[1,0]
	v_add_u32_e32 v10, 48, v236
	v_and_or_b32 v10, v10, 63, v181
	s_waitcnt lgkmcnt(0)
	v_pk_mul_f32 v[112:113], v[212:213], v[14:15] op_sel_hi:[1,0]
	v_lshlrev_b32_e32 v213, 2, v10
	ds_bpermute_b32 v10, v213, v183
	v_pk_mul_f32 v[98:99], v[8:9], v[14:15] op_sel_hi:[1,0]
	v_lshlrev_b64 v[8:9], 13, v[144:145]
	v_pk_mul_f32 v[118:119], v[208:209], v[84:85] op_sel_hi:[1,0]
	v_pk_mul_f32 v[100:101], v[6:7], v[14:15] op_sel_hi:[1,0]
	s_waitcnt lgkmcnt(0)
	v_pk_mul_f32 v[86:87], v[2:3], v[10:11] op_sel_hi:[1,0]
	v_lshl_add_u32 v2, v237, 2, s4
	s_mul_i32 s4, s41, 0x3000
	s_ashr_i32 s5, s4, 31
	s_lshl_b64 s[4:5], s[4:5], 2
	s_add_u32 s4, s70, s4
	s_addc_u32 s5, s71, s5
	s_add_u32 s4, s4, 0xc000
	v_ashrrev_i32_e32 v3, 31, v2
	ds_bpermute_b32 v208, v122, v182
	s_addc_u32 s5, s5, 0
	v_lshlrev_b64 v[122:123], 2, v[2:3]
	v_add_u32_e32 v6, 16, v2
	v_lshl_add_u64 v[8:9], s[12:13], 0, v[8:9]
	v_pk_mul_f32 v[128:129], v[202:203], v[84:85] op_sel_hi:[1,0]
	v_pk_mul_f32 v[130:131], v[200:201], v[84:85] op_sel_hi:[1,0]
	v_pk_mul_f32 v[124:125], v[206:207], v[84:85] op_sel_hi:[1,0]
	v_pk_mul_f32 v[126:127], v[204:205], v[84:85] op_sel_hi:[1,0]
	v_pk_mul_f32 v[120:121], v[210:211], v[84:85] op_sel_hi:[1,0]
	v_pk_mul_f32 v[114:115], v[12:13], v[84:85] op_sel_hi:[1,0]
	v_pk_mul_f32 v[84:85], v[4:5], v[10:11] op_sel_hi:[1,0]
	v_lshl_add_u64 v[4:5], s[4:5], 0, v[122:123]
	v_ashrrev_i32_e32 v7, 31, v6
	v_lshl_add_u64 v[132:133], v[8:9], 0, v[122:123]
	v_pk_mul_f32 v[156:157], v[186:187], v[82:83] op_sel_hi:[1,0]
	v_pk_mul_f32 v[160:161], v[184:185], v[82:83] op_sel_hi:[1,0]
	v_pk_mul_f32 v[136:137], v[16:17], v[82:83] op_sel_hi:[1,0]
	v_pk_mul_f32 v[110:111], v[214:215], v[14:15] op_sel_hi:[1,0]
	v_pk_mul_f32 v[106:107], v[218:219], v[14:15] op_sel_hi:[1,0]
	v_pk_mul_f32 v[108:109], v[216:217], v[14:15] op_sel_hi:[1,0]
	v_pk_mul_f32 v[102:103], v[222:223], v[14:15] op_sel_hi:[1,0]
	v_pk_mul_f32 v[104:105], v[220:221], v[14:15] op_sel_hi:[1,0]
	v_pk_mul_f32 v[94:95], v[226:227], v[10:11] op_sel_hi:[1,0]
	v_pk_mul_f32 v[96:97], v[224:225], v[10:11] op_sel_hi:[1,0]
	v_pk_mul_f32 v[90:91], v[230:231], v[10:11] op_sel_hi:[1,0]
	v_pk_mul_f32 v[92:93], v[228:229], v[10:11] op_sel_hi:[1,0]
	v_pk_mul_f32 v[88:89], v[234:235], v[10:11] op_sel_hi:[1,0]
	v_pk_mul_f32 v[82:83], v[232:233], v[10:11] op_sel_hi:[1,0]
	v_lshl_add_u64 v[6:7], v[6:7], 2, s[4:5]
	global_load_dwordx4 v[184:187], v[132:133], off nt
	global_load_dwordx4 v[14:17], v[4:5], off
	global_load_dwordx4 v[10:13], v[6:7], off
	v_add_u32_e32 v4, 32, v2
	v_add_u32_e32 v2, 48, v2
	v_ashrrev_i32_e32 v5, 31, v4
	v_ashrrev_i32_e32 v3, 31, v2
	v_lshl_add_u64 v[4:5], v[4:5], 2, s[4:5]
	v_lshl_add_u64 v[2:3], v[2:3], 2, s[4:5]
	global_load_dwordx4 v[188:191], v[132:133], off offset:64 nt
	global_load_dwordx4 v[192:195], v[132:133], off offset:128 nt
	global_load_dwordx4 v[6:9], v[4:5], off
	s_nop 0
	global_load_dwordx4 v[2:5], v[2:3], off
	s_nop 0
	global_load_dwordx4 v[196:199], v[132:133], off offset:192 nt
	v_add_u32_e32 v132, 16, v144
	ds_bpermute_b32 v212, v238, v182
	ds_bpermute_b32 v216, v239, v182
	v_ashrrev_i32_e32 v133, 31, v132
	v_lshlrev_b64 v[132:133], 13, v[132:133]
	v_lshl_add_u64 v[132:133], s[12:13], 0, v[132:133]
	v_lshl_add_u64 v[210:211], v[132:133], 0, v[122:123]
	global_load_dwordx4 v[200:203], v[210:211], off nt
	global_load_dwordx4 v[204:207], v[210:211], off offset:64 nt
	s_waitcnt lgkmcnt(2)
	v_pk_mul_f32 v[142:143], v[78:79], v[208:209] op_sel_hi:[1,0]
	v_pk_mul_f32 v[78:79], v[60:61], v[208:209] op_sel_hi:[1,0]
	s_waitcnt lgkmcnt(1)
	v_pk_mul_f32 v[60:61], v[50:51], v[212:213] op_sel_hi:[1,0]
	s_waitcnt lgkmcnt(0)
	v_pk_mul_f32 v[50:51], v[48:49], v[216:217] op_sel_hi:[1,0]
	v_pk_mul_f32 v[48:49], v[42:43], v[216:217] op_sel_hi:[1,0]
	v_add_u32_e32 v42, 32, v144
	ds_bpermute_b32 v182, v213, v182
	v_ashrrev_i32_e32 v43, 31, v42
	v_pk_mul_f32 v[132:133], v[76:77], v[208:209] op_sel_hi:[1,0]
	v_pk_mul_f32 v[134:135], v[74:75], v[208:209] op_sel_hi:[1,0]
	v_pk_mul_f32 v[74:75], v[64:65], v[208:209] op_sel_hi:[1,0]
	v_pk_mul_f32 v[76:77], v[62:63], v[208:209] op_sel_hi:[1,0]
	v_pk_mul_f32 v[62:63], v[68:69], v[212:213] op_sel_hi:[1,0]
	v_pk_mul_f32 v[64:65], v[66:67], v[212:213] op_sel_hi:[1,0]
	global_load_dwordx4 v[66:69], v[210:211], off offset:128 nt
	v_lshlrev_b64 v[42:43], 13, v[42:43]
	v_lshl_add_u64 v[42:43], s[12:13], 0, v[42:43]
	v_lshl_add_u64 v[220:221], v[42:43], 0, v[122:123]
	v_pk_mul_f32 v[140:141], v[80:81], v[208:209] op_sel_hi:[1,0]
	v_pk_mul_f32 v[80:81], v[58:59], v[208:209] op_sel_hi:[1,0]
	v_pk_mul_f32 v[72:73], v[72:73], v[212:213] op_sel_hi:[1,0]
	v_pk_mul_f32 v[70:71], v[70:71], v[212:213] op_sel_hi:[1,0]
	v_pk_mul_f32 v[58:59], v[52:53], v[212:213] op_sel_hi:[1,0]
	v_pk_mul_f32 v[56:57], v[56:57], v[212:213] op_sel_hi:[1,0]
	v_pk_mul_f32 v[54:55], v[54:55], v[212:213] op_sel_hi:[1,0]
	global_load_dwordx4 v[212:215], v[220:221], off nt
	v_pk_mul_f32 v[52:53], v[46:47], v[216:217] op_sel_hi:[1,0]
	global_load_dwordx4 v[208:211], v[210:211], off offset:192 nt
	v_pk_mul_f32 v[46:47], v[44:45], v[216:217] op_sel_hi:[1,0]
	v_pk_mul_f32 v[42:43], v[32:33], v[216:217] op_sel_hi:[1,0]
	v_pk_mul_f32 v[44:45], v[30:31], v[216:217] op_sel_hi:[1,0]
	s_waitcnt lgkmcnt(0)
	v_pk_mul_f32 v[30:31], v[36:37], v[182:183] op_sel_hi:[1,0]
	v_pk_mul_f32 v[32:33], v[34:35], v[182:183] op_sel_hi:[1,0]
	global_load_dwordx4 v[34:37], v[220:221], off offset:64 nt
	v_pk_mul_f32 v[40:41], v[40:41], v[216:217] op_sel_hi:[1,0]
	v_pk_mul_f32 v[38:39], v[38:39], v[216:217] op_sel_hi:[1,0]
	global_load_dwordx4 v[216:219], v[220:221], off offset:128 nt
	s_nop 0
	global_load_dwordx4 v[220:223], v[220:221], off offset:192 nt
	v_pk_mul_f32 v[28:29], v[28:29], v[182:183] op_sel_hi:[1,0]
	v_pk_mul_f32 v[26:27], v[26:27], v[182:183] op_sel_hi:[1,0]
	v_pk_mul_f32 v[24:25], v[24:25], v[182:183] op_sel_hi:[1,0]
	v_pk_mul_f32 v[22:23], v[22:23], v[182:183] op_sel_hi:[1,0]
	v_pk_mul_f32 v[20:21], v[20:21], v[182:183] op_sel_hi:[1,0]
	v_pk_mul_f32 v[18:19], v[18:19], v[182:183] op_sel_hi:[1,0]
	v_add_u32_e32 v182, 48, v144
	v_ashrrev_i32_e32 v183, 31, v182
	v_lshlrev_b64 v[182:183], 13, v[182:183]
	v_lshl_add_u64 v[182:183], s[12:13], 0, v[182:183]
	v_lshl_add_u64 v[182:183], v[182:183], 0, v[122:123]
	v_add_u32_e32 v145, s39, v236
	global_load_dwordx4 v[224:227], v[182:183], off nt
	global_load_dwordx4 v[228:231], v[182:183], off offset:64 nt
	global_load_dwordx4 v[232:235], v[182:183], off offset:128 nt
	global_load_dwordx4 v[236:239], v[182:183], off offset:192 nt
	s_add_i32 s40, s40, 0
	v_mul_lo_u32 v145, v145, s35
	v_add3_u32 v240, s40, v240, v145
	v_add_u32_e32 v145, 0x2000, v240
	s_andn2_b64 vcc, exec, s[76:77]
	s_waitcnt vmcnt(18)
	v_pk_fma_f32 v[162:163], v[162:163], v[16:17], v[186:187]
	v_pk_fma_f32 v[164:165], v[164:165], v[14:15], v[184:185]
	s_waitcnt vmcnt(16)
	v_pk_fma_f32 v[152:153], v[152:153], v[12:13], v[190:191]
	v_pk_fma_f32 v[154:155], v[154:155], v[10:11], v[188:189]
	v_cvt_pk_bf16_f32 v164, v164, v165
	v_cvt_pk_bf16_f32 v165, v162, v163
	v_cvt_pk_bf16_f32 v154, v154, v155
	v_cvt_pk_bf16_f32 v155, v152, v153
	ds_write2_b64 v240, v[164:165], v[154:155] offset1:4
	s_waitcnt vmcnt(14)
	v_pk_fma_f32 v[152:153], v[156:157], v[8:9], v[194:195]
	v_pk_fma_f32 v[154:155], v[160:161], v[6:7], v[192:193]
	s_waitcnt vmcnt(12)
	v_pk_fma_f32 v[136:137], v[136:137], v[4:5], v[198:199]
	v_pk_fma_f32 v[138:139], v[138:139], v[2:3], v[196:197]
	s_waitcnt vmcnt(11)
	v_pk_fma_f32 v[128:129], v[128:129], v[16:17], v[202:203]
	v_pk_fma_f32 v[130:131], v[130:131], v[14:15], v[200:201]
	s_waitcnt vmcnt(10)
	v_pk_fma_f32 v[124:125], v[124:125], v[12:13], v[206:207]
	v_cvt_pk_bf16_f32 v130, v130, v131
	v_cvt_pk_bf16_f32 v131, v128, v129
	v_cvt_pk_bf16_f32 v129, v124, v125
	v_add_u32_e32 v124, 64, v144
	v_ashrrev_i32_e32 v125, 31, v124
	v_lshlrev_b64 v[124:125], 13, v[124:125]
	v_pk_fma_f32 v[126:127], v[126:127], v[10:11], v[204:205]
	v_lshl_add_u64 v[124:125], s[12:13], 0, v[124:125]
	v_cvt_pk_bf16_f32 v154, v154, v155
	v_cvt_pk_bf16_f32 v155, v152, v153
	v_cvt_pk_bf16_f32 v138, v138, v139
	v_cvt_pk_bf16_f32 v139, v136, v137
	v_cvt_pk_bf16_f32 v128, v126, v127
	s_waitcnt vmcnt(9)
	v_pk_fma_f32 v[66:67], v[118:119], v[6:7], v[66:67]
	v_add_u32_e32 v118, 0x50, v144
	v_ashrrev_i32_e32 v119, 31, v118
	v_lshlrev_b64 v[118:119], 13, v[118:119]
	v_lshl_add_u64 v[136:137], v[124:125], 0, v[122:123]
	v_pk_fma_f32 v[68:69], v[120:121], v[8:9], v[68:69]
	v_lshl_add_u64 v[118:119], s[12:13], 0, v[118:119]
	ds_write2_b64 v240, v[154:155], v[138:139] offset0:8 offset1:12
	global_load_dwordx4 v[124:127], v[136:137], off nt
	ds_write2_b64 v145, v[130:131], v[128:129] offset0:32 offset1:36
	global_load_dwordx4 v[128:131], v[136:137], off offset:64 nt
	v_cvt_pk_bf16_f32 v138, v66, v67
	v_cvt_pk_bf16_f32 v139, v68, v69
	s_waitcnt vmcnt(9)
	v_pk_fma_f32 v[114:115], v[114:115], v[4:5], v[210:211]
	v_pk_fma_f32 v[116:117], v[116:117], v[2:3], v[208:209]
	global_load_dwordx4 v[66:69], v[136:137], off offset:128 nt
	v_cvt_pk_bf16_f32 v152, v116, v117
	v_cvt_pk_bf16_f32 v153, v114, v115
	global_load_dwordx4 v[114:117], v[136:137], off offset:192 nt
	v_lshl_add_u64 v[136:137], v[118:119], 0, v[122:123]
	s_waitcnt vmcnt(10)
	v_pk_fma_f32 v[106:107], v[106:107], v[12:13], v[36:37]
	v_pk_fma_f32 v[34:35], v[108:109], v[10:11], v[34:35]
	global_load_dwordx4 v[118:121], v[136:137], off nt
	ds_write2_b64 v145, v[138:139], v[152:153] offset0:40 offset1:44
	v_pk_fma_f32 v[138:139], v[110:111], v[16:17], v[214:215]
	v_pk_fma_f32 v[152:153], v[112:113], v[14:15], v[212:213]
	global_load_dwordx4 v[110:113], v[136:137], off offset:64 nt
	v_cvt_pk_bf16_f32 v154, v34, v35
	global_load_dwordx4 v[34:37], v[136:137], off offset:128 nt
	v_cvt_pk_bf16_f32 v155, v106, v107
	global_load_dwordx4 v[106:109], v[136:137], off offset:192 nt
	v_add_u32_e32 v136, 0x60, v144
	v_cvt_pk_bf16_f32 v152, v152, v153
	v_cvt_pk_bf16_f32 v153, v138, v139
	v_add_u32_e32 v145, 0x4000, v240
	v_ashrrev_i32_e32 v137, 31, v136
	v_lshlrev_b64 v[136:137], 13, v[136:137]
	ds_write2_b64 v145, v[152:153], v[154:155] offset0:64 offset1:68
	s_waitcnt vmcnt(13)
	v_pk_fma_f32 v[152:153], v[102:103], v[8:9], v[218:219]
	v_pk_fma_f32 v[154:155], v[104:105], v[6:7], v[216:217]
	v_lshl_add_u64 v[136:137], s[12:13], 0, v[136:137]
	v_cvt_pk_bf16_f32 v154, v154, v155
	v_cvt_pk_bf16_f32 v155, v152, v153
	s_waitcnt vmcnt(12)
	v_pk_fma_f32 v[152:153], v[98:99], v[4:5], v[222:223]
	v_pk_fma_f32 v[98:99], v[100:101], v[2:3], v[220:221]
	v_lshl_add_u64 v[156:157], v[136:137], 0, v[122:123]
	v_cvt_pk_bf16_f32 v160, v98, v99
	v_cvt_pk_bf16_f32 v161, v152, v153
	v_add_u32_e32 v144, 0x70, v144
	global_load_dwordx4 v[136:139], v[156:157], off nt
	global_load_dwordx4 v[102:105], v[156:157], off offset:64 nt
	ds_write2_b64 v145, v[154:155], v[160:161] offset0:72 offset1:76
	v_ashrrev_i32_e32 v145, 31, v144
	v_lshlrev_b64 v[144:145], 13, v[144:145]
	v_lshl_add_u64 v[144:145], s[12:13], 0, v[144:145]
	global_load_dwordx4 v[98:101], v[156:157], off offset:128 nt
	global_load_dwordx4 v[152:155], v[156:157], off offset:192 nt
	v_lshl_add_u64 v[122:123], v[144:145], 0, v[122:123]
	s_waitcnt vmcnt(15)
	v_pk_fma_f32 v[144:145], v[94:95], v[16:17], v[226:227]
	v_pk_fma_f32 v[94:95], v[96:97], v[14:15], v[224:225]
	s_waitcnt vmcnt(14)
	v_pk_fma_f32 v[90:91], v[90:91], v[12:13], v[230:231]
	v_pk_fma_f32 v[92:93], v[92:93], v[10:11], v[228:229]
	global_load_dwordx4 v[160:163], v[122:123], off nt
	v_cvt_pk_bf16_f32 v156, v94, v95
	global_load_dwordx4 v[94:97], v[122:123], off offset:64 nt
	v_cvt_pk_bf16_f32 v157, v144, v145
	v_cvt_pk_bf16_f32 v144, v92, v93
	v_cvt_pk_bf16_f32 v145, v90, v91
	global_load_dwordx4 v[90:93], v[122:123], off offset:128 nt
	global_load_dwordx4 v[182:185], v[122:123], off offset:192 nt
	s_waitcnt vmcnt(17)
	v_pk_fma_f32 v[88:89], v[88:89], v[8:9], v[234:235]
	v_pk_fma_f32 v[82:83], v[82:83], v[6:7], v[232:233]
	s_waitcnt vmcnt(16)
	v_pk_fma_f32 v[84:85], v[84:85], v[4:5], v[238:239]
	v_pk_fma_f32 v[86:87], v[86:87], v[2:3], v[236:237]
	v_add_u32_e32 v164, 0x6000, v240
	v_cvt_pk_bf16_f32 v82, v82, v83
	v_cvt_pk_bf16_f32 v83, v88, v89
	v_cvt_pk_bf16_f32 v86, v86, v87
	v_cvt_pk_bf16_f32 v87, v84, v85
	ds_write2_b64 v164, v[82:83], v[86:87] offset0:104 offset1:108
	ds_write2_b64 v164, v[156:157], v[144:145] offset0:96 offset1:100
	s_waitcnt vmcnt(15)
	v_pk_fma_f32 v[82:83], v[140:141], v[16:17], v[126:127]
	v_pk_fma_f32 v[84:85], v[142:143], v[14:15], v[124:125]
	s_waitcnt vmcnt(14)
	v_pk_fma_f32 v[86:87], v[134:135], v[10:11], v[128:129]
	v_cvt_pk_bf16_f32 v84, v84, v85
	v_cvt_pk_bf16_f32 v85, v82, v83
	v_pk_fma_f32 v[82:83], v[132:133], v[12:13], v[130:131]
	v_cvt_pk_bf16_f32 v86, v86, v87
	s_waitcnt vmcnt(13)
	v_pk_fma_f32 v[68:69], v[78:79], v[8:9], v[68:69]
	v_pk_fma_f32 v[66:67], v[80:81], v[6:7], v[66:67]
	v_cvt_pk_bf16_f32 v87, v82, v83
	v_cvt_pk_bf16_f32 v66, v66, v67
	v_cvt_pk_bf16_f32 v67, v68, v69
	s_waitcnt vmcnt(12)
	v_pk_fma_f32 v[68:69], v[74:75], v[4:5], v[116:117]
	v_pk_fma_f32 v[74:75], v[76:77], v[2:3], v[114:115]
	v_add_u32_e32 v82, 0x8000, v240
	v_cvt_pk_bf16_f32 v74, v74, v75
	v_cvt_pk_bf16_f32 v75, v68, v69
	ds_write2_b64 v82, v[66:67], v[74:75] offset0:136 offset1:140
	s_waitcnt vmcnt(10)
	v_pk_fma_f32 v[62:63], v[62:63], v[12:13], v[112:113]
	v_pk_fma_f32 v[64:65], v[64:65], v[10:11], v[110:111]
	s_waitcnt vmcnt(9)
	v_pk_fma_f32 v[36:37], v[58:59], v[8:9], v[36:37]
	v_pk_fma_f32 v[34:35], v[60:61], v[6:7], v[34:35]
	s_waitcnt vmcnt(8)
	v_pk_fma_f32 v[54:55], v[54:55], v[2:3], v[106:107]
	v_cvt_pk_bf16_f32 v34, v34, v35
	v_cvt_pk_bf16_f32 v35, v36, v37
	v_pk_fma_f32 v[36:37], v[56:57], v[4:5], v[108:109]
	v_cvt_pk_bf16_f32 v64, v64, v65
	v_cvt_pk_bf16_f32 v65, v62, v63
	v_add_u32_e32 v62, 0xa000, v240
	v_cvt_pk_bf16_f32 v54, v54, v55
	v_cvt_pk_bf16_f32 v55, v36, v37
	ds_write2_b64 v62, v[34:35], v[54:55] offset0:168 offset1:172
	v_pk_fma_f32 v[66:67], v[16:17], v[72:73], v[120:121]
	v_pk_fma_f32 v[68:69], v[14:15], v[70:71], v[118:119]
	ds_write2_b64 v82, v[84:85], v[86:87] offset0:128 offset1:132
	v_cvt_pk_bf16_f32 v68, v68, v69
	v_cvt_pk_bf16_f32 v69, v66, v67
	ds_write2_b64 v62, v[68:69], v[64:65] offset0:160 offset1:164
	s_waitcnt vmcnt(7)
	v_pk_fma_f32 v[34:35], v[16:17], v[50:51], v[138:139]
	v_pk_fma_f32 v[36:37], v[14:15], v[52:53], v[136:137]
	s_waitcnt vmcnt(3)
	v_pk_fma_f32 v[16:17], v[16:17], v[30:31], v[162:163]
	v_cvt_pk_bf16_f32 v36, v36, v37
	v_cvt_pk_bf16_f32 v37, v34, v35
	v_pk_fma_f32 v[34:35], v[12:13], v[46:47], v[104:105]
	v_pk_fma_f32 v[46:47], v[10:11], v[48:49], v[102:103]
	v_add_u32_e32 v48, 0xc000, v240
	v_cvt_pk_bf16_f32 v46, v46, v47
	v_cvt_pk_bf16_f32 v47, v34, v35
	ds_write2_b64 v48, v[36:37], v[46:47] offset0:192 offset1:196
	v_pk_fma_f32 v[34:35], v[40:41], v[8:9], v[100:101]
	v_pk_fma_f32 v[36:37], v[38:39], v[6:7], v[98:99]
	v_pk_fma_f32 v[38:39], v[44:45], v[2:3], v[152:153]
	v_cvt_pk_bf16_f32 v36, v36, v37
	v_cvt_pk_bf16_f32 v37, v34, v35
	v_pk_fma_f32 v[34:35], v[42:43], v[4:5], v[154:155]
	s_waitcnt vmcnt(2)
	v_pk_fma_f32 v[12:13], v[12:13], v[28:29], v[96:97]
	v_pk_fma_f32 v[10:11], v[10:11], v[26:27], v[94:95]
	s_waitcnt vmcnt(1)
	v_pk_fma_f32 v[8:9], v[8:9], v[24:25], v[92:93]
	v_pk_fma_f32 v[6:7], v[6:7], v[22:23], v[90:91]
	s_waitcnt vmcnt(0)
	v_pk_fma_f32 v[4:5], v[20:21], v[4:5], v[184:185]
	v_pk_fma_f32 v[2:3], v[18:19], v[2:3], v[182:183]
	v_cvt_pk_bf16_f32 v10, v10, v11
	v_cvt_pk_bf16_f32 v11, v12, v13
	v_add_u32_e32 v12, 0xe000, v240
	v_cvt_pk_bf16_f32 v6, v6, v7
	v_cvt_pk_bf16_f32 v7, v8, v9
	v_cvt_pk_bf16_f32 v2, v2, v3
	v_cvt_pk_bf16_f32 v3, v4, v5
	v_lshl_or_b32 v8, s38, 5, v167
	v_pk_fma_f32 v[14:15], v[14:15], v[32:33], v[160:161]
	ds_write2_b64 v12, v[6:7], v[2:3] offset0:232 offset1:236
	v_mad_u64_u32 v[6:7], s[4:5], v8, s35, v[148:149]
	v_add_u32_e32 v8, s25, v8
	v_cvt_pk_bf16_f32 v14, v14, v15
	v_cvt_pk_bf16_f32 v15, v16, v17
	v_ashrrev_i32_e32 v9, 31, v8
	ds_write2_b64 v12, v[14:15], v[10:11] offset0:224 offset1:228
	v_lshlrev_b64 v[10:11], 12, v[8:9]
	v_cvt_pk_bf16_f32 v38, v38, v39
	v_cvt_pk_bf16_f32 v39, v34, v35
	v_lshl_add_u64 v[10:11], s[18:19], 0, v[10:11]
	ds_write2_b64 v48, v[36:37], v[38:39] offset0:200 offset1:204
	v_lshl_add_u64 v[10:11], v[10:11], 0, s[22:23]
	s_waitcnt lgkmcnt(0)
	s_barrier
	v_lshl_add_u64 v[10:11], v[10:11], 0, v[146:147]
	ds_read_b128 v[2:5], v6
	s_waitcnt lgkmcnt(0)
	global_store_dwordx4 v[10:11], v[2:5], off sc1
	s_nop 1
	v_add_u32_e32 v10, 2, v8
	v_ashrrev_i32_e32 v11, 31, v10
	v_lshlrev_b64 v[10:11], 12, v[10:11]
	v_lshl_add_u64 v[10:11], s[18:19], 0, v[10:11]
	v_lshl_add_u64 v[10:11], v[10:11], 0, s[22:23]
	v_lshl_add_u64 v[10:11], v[10:11], 0, v[146:147]
	ds_read_b128 v[2:5], v6 offset:1056
	s_waitcnt lgkmcnt(0)
	global_store_dwordx4 v[10:11], v[2:5], off sc1
	s_nop 1
	v_add_u32_e32 v10, 4, v8
	v_ashrrev_i32_e32 v11, 31, v10
	v_lshlrev_b64 v[10:11], 12, v[10:11]
	v_lshl_add_u64 v[10:11], s[18:19], 0, v[10:11]
	v_lshl_add_u64 v[10:11], v[10:11], 0, s[22:23]
	v_lshl_add_u64 v[10:11], v[10:11], 0, v[146:147]
	ds_read_b128 v[2:5], v6 offset:2112
	s_waitcnt lgkmcnt(0)
	global_store_dwordx4 v[10:11], v[2:5], off sc1
	s_nop 1
	v_add_u32_e32 v10, 6, v8
	v_ashrrev_i32_e32 v11, 31, v10
	v_lshlrev_b64 v[10:11], 12, v[10:11]
	v_lshl_add_u64 v[10:11], s[18:19], 0, v[10:11]
	v_lshl_add_u64 v[10:11], v[10:11], 0, s[22:23]
	v_lshl_add_u64 v[10:11], v[10:11], 0, v[146:147]
	ds_read_b128 v[2:5], v6 offset:3168
	s_waitcnt lgkmcnt(0)
	global_store_dwordx4 v[10:11], v[2:5], off sc1
	s_nop 1
	v_add_u32_e32 v10, 8, v8
	v_ashrrev_i32_e32 v11, 31, v10
	v_lshlrev_b64 v[10:11], 12, v[10:11]
	v_lshl_add_u64 v[10:11], s[18:19], 0, v[10:11]
	v_lshl_add_u64 v[10:11], v[10:11], 0, s[22:23]
	v_lshl_add_u64 v[10:11], v[10:11], 0, v[146:147]
	ds_read_b128 v[2:5], v6 offset:4224
	s_waitcnt lgkmcnt(0)
	global_store_dwordx4 v[10:11], v[2:5], off sc1
	s_nop 1
	v_add_u32_e32 v10, 10, v8
	v_ashrrev_i32_e32 v11, 31, v10
	v_lshlrev_b64 v[10:11], 12, v[10:11]
	v_lshl_add_u64 v[10:11], s[18:19], 0, v[10:11]
	v_lshl_add_u64 v[10:11], v[10:11], 0, s[22:23]
	v_lshl_add_u64 v[10:11], v[10:11], 0, v[146:147]
	ds_read_b128 v[2:5], v6 offset:5280
	s_waitcnt lgkmcnt(0)
	global_store_dwordx4 v[10:11], v[2:5], off sc1
	s_nop 1
	v_add_u32_e32 v10, 12, v8
	v_ashrrev_i32_e32 v11, 31, v10
	v_lshlrev_b64 v[10:11], 12, v[10:11]
	v_lshl_add_u64 v[10:11], s[18:19], 0, v[10:11]
	v_lshl_add_u64 v[10:11], v[10:11], 0, s[22:23]
	v_lshl_add_u64 v[10:11], v[10:11], 0, v[146:147]
	ds_read_b128 v[2:5], v6 offset:6336
	s_waitcnt lgkmcnt(0)
	global_store_dwordx4 v[10:11], v[2:5], off sc1
	s_nop 1
	v_add_u32_e32 v10, 14, v8
	v_ashrrev_i32_e32 v11, 31, v10
	v_lshlrev_b64 v[10:11], 12, v[10:11]
	v_lshl_add_u64 v[10:11], s[18:19], 0, v[10:11]
	v_lshl_add_u64 v[10:11], v[10:11], 0, s[22:23]
	v_lshl_add_u64 v[10:11], v[10:11], 0, v[146:147]
	ds_read_b128 v[2:5], v6 offset:7392
	s_waitcnt lgkmcnt(0)
	global_store_dwordx4 v[10:11], v[2:5], off sc1
	s_nop 1
	v_add_u32_e32 v10, 16, v8
	v_ashrrev_i32_e32 v11, 31, v10
	v_lshlrev_b64 v[10:11], 12, v[10:11]
	v_lshl_add_u64 v[10:11], s[18:19], 0, v[10:11]
	v_lshl_add_u64 v[10:11], v[10:11], 0, s[22:23]
	v_lshl_add_u64 v[10:11], v[10:11], 0, v[146:147]
	ds_read_b128 v[2:5], v6 offset:8448
	s_waitcnt lgkmcnt(0)
	global_store_dwordx4 v[10:11], v[2:5], off sc1
	s_nop 1
	v_add_u32_e32 v10, 18, v8
	v_ashrrev_i32_e32 v11, 31, v10
	v_lshlrev_b64 v[10:11], 12, v[10:11]
	v_lshl_add_u64 v[10:11], s[18:19], 0, v[10:11]
	v_lshl_add_u64 v[10:11], v[10:11], 0, s[22:23]
	v_lshl_add_u64 v[10:11], v[10:11], 0, v[146:147]
	ds_read_b128 v[2:5], v6 offset:9504
	s_waitcnt lgkmcnt(0)
	global_store_dwordx4 v[10:11], v[2:5], off sc1
	s_nop 1
	v_add_u32_e32 v10, 20, v8
	v_ashrrev_i32_e32 v11, 31, v10
	v_lshlrev_b64 v[10:11], 12, v[10:11]
	v_lshl_add_u64 v[10:11], s[18:19], 0, v[10:11]
	v_lshl_add_u64 v[10:11], v[10:11], 0, s[22:23]
	v_lshl_add_u64 v[10:11], v[10:11], 0, v[146:147]
	ds_read_b128 v[2:5], v6 offset:10560
	s_waitcnt lgkmcnt(0)
	global_store_dwordx4 v[10:11], v[2:5], off sc1
	s_nop 1
	v_add_u32_e32 v10, 22, v8
	v_ashrrev_i32_e32 v11, 31, v10
	v_lshlrev_b64 v[10:11], 12, v[10:11]
	v_lshl_add_u64 v[10:11], s[18:19], 0, v[10:11]
	v_lshl_add_u64 v[10:11], v[10:11], 0, s[22:23]
	v_lshl_add_u64 v[10:11], v[10:11], 0, v[146:147]
	ds_read_b128 v[2:5], v6 offset:11616
	s_waitcnt lgkmcnt(0)
	global_store_dwordx4 v[10:11], v[2:5], off sc1
	s_nop 1
	v_add_u32_e32 v10, 24, v8
	v_ashrrev_i32_e32 v11, 31, v10
	v_lshlrev_b64 v[10:11], 12, v[10:11]
	v_lshl_add_u64 v[10:11], s[18:19], 0, v[10:11]
	v_lshl_add_u64 v[10:11], v[10:11], 0, s[22:23]
	v_lshl_add_u64 v[10:11], v[10:11], 0, v[146:147]
	ds_read_b128 v[2:5], v6 offset:12672
	s_waitcnt lgkmcnt(0)
	global_store_dwordx4 v[10:11], v[2:5], off sc1
	s_nop 1
	v_add_u32_e32 v10, 26, v8
	v_ashrrev_i32_e32 v11, 31, v10
	v_lshlrev_b64 v[10:11], 12, v[10:11]
	v_lshl_add_u64 v[10:11], s[18:19], 0, v[10:11]
	v_lshl_add_u64 v[10:11], v[10:11], 0, s[22:23]
	v_lshl_add_u64 v[10:11], v[10:11], 0, v[146:147]
	ds_read_b128 v[2:5], v6 offset:13728
	s_waitcnt lgkmcnt(0)
	global_store_dwordx4 v[10:11], v[2:5], off sc1
	s_nop 1
	v_add_u32_e32 v10, 28, v8
	v_ashrrev_i32_e32 v11, 31, v10
	v_lshlrev_b64 v[10:11], 12, v[10:11]
	v_lshl_add_u64 v[10:11], s[18:19], 0, v[10:11]
	v_lshl_add_u64 v[10:11], v[10:11], 0, s[22:23]
	ds_read_b128 v[2:5], v6 offset:14784
	v_lshl_add_u64 v[10:11], v[10:11], 0, v[146:147]
	s_waitcnt lgkmcnt(0)
	global_store_dwordx4 v[10:11], v[2:5], off sc1
	s_nop 1
	ds_read_b128 v[2:5], v6 offset:15840
	v_add_u32_e32 v6, 30, v8
	v_ashrrev_i32_e32 v7, 31, v6
	v_lshlrev_b64 v[6:7], 12, v[6:7]
	v_lshl_add_u64 v[6:7], s[18:19], 0, v[6:7]
	v_lshl_add_u64 v[6:7], v[6:7], 0, s[22:23]
	v_lshl_add_u64 v[6:7], v[6:7], 0, v[146:147]
	s_waitcnt lgkmcnt(0)
	global_store_dwordx4 v[6:7], v[2:5], off sc1
	s_nop 1
	s_waitcnt lgkmcnt(0)
	s_barrier
	s_cbranch_vccnz .LBB0_1127
	s_waitcnt vmcnt(0)
	s_barrier
	s_and_saveexec_b64 s[4:5], s[0:1]
	s_cbranch_execz .LBB0_1126
	s_mov_b64 s[6:7], exec
	v_mbcnt_lo_u32_b32 v2, s6, 0
	v_mbcnt_hi_u32_b32 v2, s7, v2
	v_cmp_eq_u32_e32 vcc, 0, v2
	s_and_b64 s[22:23], exec, vcc
	s_mov_b64 exec, s[22:23]
	s_cbranch_execz .LBB0_1126
	s_lshl_b32 s22, s37, 4
	s_ashr_i32 s23, s22, 31
	s_lshl_b64 s[22:23], s[22:23], 2
	s_add_u32 s22, s29, s22
	s_addc_u32 s23, s30, s23
	s_bcnt1_i32_b64 s6, s[6:7]
	v_mov_b32_e32 v2, s6
	global_atomic_add v147, v2, s[22:23]
	s_branch .LBB0_1126

.LBB0_1433:
	s_add_i32 s88, s39, 0xffff8000
	s_and_b32 s88, s88, 0x8000
	s_add_i32 s88, s88, 0
	s_add_i32 s87, s86, 0
	s_add_i32 s88, s88, 0x18000
	v_add_u32_e32 v246, s88, v212
	v_add_u32_e32 v247, s87, v215
	v_add_u32_e32 v252, s88, v181
	v_add_u32_e32 v254, s88, v172
	v_add_u32_e32 v250, s88, v183
	s_branch .Lrot_m1

.Lrot_m1:
	ds_read_b64_tr_b16 v[222:223], v246
	ds_read_b64_tr_b16 v[224:225], v246 offset:2048
	ds_read_b64_tr_b16 v[226:227], v250
	ds_read_b64_tr_b16 v[228:229], v250 offset:2048
	ds_read_b128 v[162:165], v247
	ds_read_b128 v[166:169], v247 offset:2048
	ds_read_b64_tr_b16 v[230:231], v252
	ds_read_b64_tr_b16 v[232:233], v252 offset:2048
	ds_read_b64_tr_b16 v[234:235], v254
	ds_read_b64_tr_b16 v[236:237], v254 offset:2048
	s_waitcnt lgkmcnt(5)
	v_mfma_f32_16x16x32_bf16 v[62:65], v[222:225], v[162:165], v[62:65]
	ds_read_b128 v[238:241], v247 offset:4096
	s_and_b32 s88, s39, 0x8000
	s_add_i32 s89, s38, s85
	v_mfma_f32_16x16x32_bf16 v[58:61], v[226:229], v[162:165], v[58:61]
	s_mov_b32 s90, m0
	s_mov_b32 m0, s89
	s_nop 0
	global_load_lds_dwordx4 v221, s[18:19]
	s_mov_b32 m0, s90
	s_waitcnt lgkmcnt(3)
	v_mfma_f32_16x16x32_bf16 v[54:57], v[230:233], v[162:165], v[54:57]
	s_waitcnt lgkmcnt(1)
	v_mfma_f32_16x16x32_bf16 v[42:45], v[234:237], v[162:165], v[42:45]
	v_mfma_f32_16x16x32_bf16 v[50:53], v[222:225], v[166:169], v[50:53]
	ds_read_b128 v[162:165], v247 offset:6144
	s_add_i32 s90, s89, 0x2000
	s_mov_b32 s91, m0
	s_mov_b32 m0, s90
	s_nop 0
	global_load_lds_dwordx4 v220, s[18:19]
	s_mov_b32 m0, s91
	v_mfma_f32_16x16x32_bf16 v[46:49], v[226:229], v[166:169], v[46:49]
	v_mfma_f32_16x16x32_bf16 v[38:41], v[230:233], v[166:169], v[38:41]
	v_mfma_f32_16x16x32_bf16 v[34:37], v[234:237], v[166:169], v[34:37]
	s_waitcnt lgkmcnt(1)
	v_mfma_f32_16x16x32_bf16 v[66:69], v[222:225], v[238:241], v[66:69]
	ds_read_b128 v[166:169], v247 offset:8192
	s_add_i32 s90, s89, 0x4000
	s_mov_b32 s91, m0
	s_mov_b32 m0, s90
	s_nop 0
	global_load_lds_dwordx4 v219, s[18:19]
	s_mov_b32 m0, s91
	v_mfma_f32_16x16x32_bf16 v[70:73], v[226:229], v[238:241], v[70:73]
	v_mfma_f32_16x16x32_bf16 v[74:77], v[230:233], v[238:241], v[74:77]
	v_mfma_f32_16x16x32_bf16 v[78:81], v[234:237], v[238:241], v[78:81]
	s_waitcnt lgkmcnt(1)
	v_mfma_f32_16x16x32_bf16 v[82:85], v[222:225], v[162:165], v[82:85]
	ds_read_b128 v[238:241], v247 offset:10240
	s_addk_i32 s89, 0x6000
	s_mov_b32 s90, m0
	s_mov_b32 m0, s89
	s_nop 0
	global_load_lds_dwordx4 v218, s[18:19]
	s_mov_b32 m0, s90
	v_mfma_f32_16x16x32_bf16 v[86:89], v[226:229], v[162:165], v[86:89]
	v_mfma_f32_16x16x32_bf16 v[90:93], v[230:233], v[162:165], v[90:93]
	v_mfma_f32_16x16x32_bf16 v[94:97], v[234:237], v[162:165], v[94:97]
	ds_read_b128 v[242:245], v247 offset:12288
	ds_read_b64_tr_b16 v[162:163], v246 offset:16384
	ds_read_b64_tr_b16 v[164:165], v246 offset:18432
	s_waitcnt lgkmcnt(4)
	v_mfma_f32_16x16x32_bf16 v[98:101], v[222:225], v[166:169], v[98:101]
	v_mfma_f32_16x16x32_bf16 v[102:105], v[226:229], v[166:169], v[102:105]
	v_mfma_f32_16x16x32_bf16 v[106:109], v[230:233], v[166:169], v[106:109]
	v_mfma_f32_16x16x32_bf16 v[110:113], v[234:237], v[166:169], v[110:113]
	ds_read_b128 v[246:249], v247 offset:14336
	ds_read_b64_tr_b16 v[166:167], v250 offset:16384
	ds_read_b64_tr_b16 v[168:169], v250 offset:18432
	s_waitcnt lgkmcnt(6)
	v_mfma_f32_16x16x32_bf16 v[114:117], v[222:225], v[238:241], v[114:117]
	v_mfma_f32_16x16x32_bf16 v[118:121], v[226:229], v[238:241], v[118:121]
	v_mfma_f32_16x16x32_bf16 v[122:125], v[230:233], v[238:241], v[122:125]
	v_mfma_f32_16x16x32_bf16 v[126:129], v[234:237], v[238:241], v[126:129]
	v_add_u32_e32 v200, s87, v216
	ds_read_b128 v[238:241], v200
	ds_read_b64_tr_b16 v[250:251], v252 offset:16384
	ds_read_b64_tr_b16 v[252:253], v252 offset:18432
	s_waitcnt lgkmcnt(8)
	v_mfma_f32_16x16x32_bf16 v[130:133], v[222:225], v[242:245], v[130:133]
	v_mfma_f32_16x16x32_bf16 v[134:137], v[226:229], v[242:245], v[134:137]
	v_mfma_f32_16x16x32_bf16 v[138:141], v[230:233], v[242:245], v[138:141]
	v_mfma_f32_16x16x32_bf16 v[142:145], v[234:237], v[242:245], v[142:145]
	s_waitcnt lgkmcnt(5)
	v_mfma_f32_16x16x32_bf16 v[146:149], v[222:225], v[246:249], v[146:149]
	v_mfma_f32_16x16x32_bf16 v[150:153], v[226:229], v[246:249], v[150:153]
	ds_read_b128 v[222:225], v200 offset:2048
	ds_read_b64_tr_b16 v[226:227], v254 offset:16384
	ds_read_b64_tr_b16 v[228:229], v254 offset:18432
	v_mfma_f32_16x16x32_bf16 v[154:157], v[230:233], v[246:249], v[154:157]
	v_mfma_f32_16x16x32_bf16 v[158:161], v[234:237], v[246:249], v[158:161]
	ds_read_b128 v[230:233], v200 offset:4096
	s_waitcnt lgkmcnt(6)
	v_mfma_f32_16x16x32_bf16 v[62:65], v[162:165], v[238:241], v[62:65]
	s_add_u32 s87, s83, s2
	s_waitcnt vmcnt(11)
	s_addc_u32 s90, s84, s3
	v_mfma_f32_16x16x32_bf16 v[58:61], v[166:169], v[238:241], v[58:61]
	v_cvt_pk_bf16_f32 v30, v30, v31
	v_cvt_pk_bf16_f32 v31, v32, v33
	v_add_u32_e32 v242, s88, v217
	s_waitcnt lgkmcnt(4)
	v_mfma_f32_16x16x32_bf16 v[54:57], v[250:253], v[238:241], v[54:57]
	s_add_u32 s88, s87, 0x160000
	ds_write_b64 v242, v[30:31]
	s_addc_u32 s89, s90, 0
	s_waitcnt lgkmcnt(2)
	v_mfma_f32_16x16x32_bf16 v[42:45], v[226:229], v[238:241], v[42:45]
	global_load_dwordx4 v[30:33], v199, s[88:89] nt
	v_mfma_f32_16x16x32_bf16 v[50:53], v[162:165], v[222:225], v[50:53]
	ds_read_b128 v[234:237], v200 offset:6144
	s_waitcnt vmcnt(11)
	s_add_u32 s88, s87, 0x18c000
	v_mfma_f32_16x16x32_bf16 v[46:49], v[166:169], v[222:225], v[46:49]
	v_cvt_pk_bf16_f32 v26, v26, v27
	v_cvt_pk_bf16_f32 v27, v28, v29
	ds_write_b64 v242, v[26:27] offset:8192
	v_mfma_f32_16x16x32_bf16 v[38:41], v[250:253], v[222:225], v[38:41]
	s_addc_u32 s89, s90, 0
	global_load_dwordx4 v[26:29], v199, s[88:89] nt
	v_mfma_f32_16x16x32_bf16 v[34:37], v[226:229], v[222:225], v[34:37]
	s_waitcnt lgkmcnt(3)
	v_mfma_f32_16x16x32_bf16 v[66:69], v[162:165], v[230:233], v[66:69]
	ds_read_b128 v[222:225], v200 offset:8192
	s_waitcnt vmcnt(11)
	s_add_u32 s88, s87, 0x1b8000
	v_mfma_f32_16x16x32_bf16 v[70:73], v[166:169], v[230:233], v[70:73]
	v_cvt_pk_bf16_f32 v22, v22, v23
	v_cvt_pk_bf16_f32 v23, v24, v25
	ds_write_b64 v242, v[22:23] offset:16384
	v_mfma_f32_16x16x32_bf16 v[74:77], v[250:253], v[230:233], v[74:77]
	s_addc_u32 s89, s90, 0
	global_load_dwordx4 v[22:25], v199, s[88:89] nt
	v_mfma_f32_16x16x32_bf16 v[78:81], v[226:229], v[230:233], v[78:81]
	s_waitcnt lgkmcnt(3)
	v_mfma_f32_16x16x32_bf16 v[82:85], v[162:165], v[234:237], v[82:85]
	ds_read_b128 v[230:233], v200 offset:10240
	s_waitcnt vmcnt(11)
	s_add_u32 s88, s87, 0x1e4000
	v_mfma_f32_16x16x32_bf16 v[86:89], v[166:169], v[234:237], v[86:89]
	v_cvt_pk_bf16_f32 v18, v18, v19
	v_cvt_pk_bf16_f32 v19, v20, v21
	ds_write_b64 v242, v[18:19] offset:24576
	v_mfma_f32_16x16x32_bf16 v[90:93], v[250:253], v[234:237], v[90:93]
	s_addc_u32 s89, s90, 0
	global_load_dwordx4 v[18:21], v199, s[88:89] nt
	v_mfma_f32_16x16x32_bf16 v[94:97], v[226:229], v[234:237], v[94:97]
	ds_read_b128 v[234:237], v200 offset:12288
	s_waitcnt lgkmcnt(4)
	v_mfma_f32_16x16x32_bf16 v[98:101], v[162:165], v[222:225], v[98:101]
	s_add_u32 s87, s40, s2
	s_waitcnt vmcnt(11)
	s_addc_u32 s90, s41, s3
	v_mfma_f32_16x16x32_bf16 v[102:105], v[166:169], v[222:225], v[102:105]
	v_cvt_pk_bf16_f32 v14, v14, v15
	v_cvt_pk_bf16_f32 v15, v16, v17
	s_add_u32 s88, s87, 0x160000
	v_mfma_f32_16x16x32_bf16 v[106:109], v[250:253], v[222:225], v[106:109]
	ds_write_b64 v242, v[14:15] offset:256
	s_addc_u32 s89, s90, 0
	global_load_dwordx4 v[14:17], v199, s[88:89] nt
	v_mfma_f32_16x16x32_bf16 v[110:113], v[226:229], v[222:225], v[110:113]
	s_waitcnt lgkmcnt(3)
	v_mfma_f32_16x16x32_bf16 v[114:117], v[162:165], v[230:233], v[114:117]
	ds_read_b128 v[222:225], v200 offset:14336
	s_waitcnt vmcnt(11)
	s_add_u32 s88, s87, 0x18c000
	v_mfma_f32_16x16x32_bf16 v[118:121], v[166:169], v[230:233], v[118:121]
	v_cvt_pk_bf16_f32 v10, v10, v11
	v_cvt_pk_bf16_f32 v11, v12, v13
	ds_write_b64 v242, v[10:11] offset:8448
	v_mfma_f32_16x16x32_bf16 v[122:125], v[250:253], v[230:233], v[122:125]
	s_addc_u32 s89, s90, 0
	global_load_dwordx4 v[10:13], v199, s[88:89] nt
	v_mfma_f32_16x16x32_bf16 v[126:129], v[226:229], v[230:233], v[126:129]
	s_waitcnt lgkmcnt(3)
	v_mfma_f32_16x16x32_bf16 v[130:133], v[162:165], v[234:237], v[130:133]
	s_waitcnt vmcnt(11)
	s_add_u32 s88, s87, 0x1b8000
	v_cvt_pk_bf16_f32 v6, v6, v7
	v_mfma_f32_16x16x32_bf16 v[134:137], v[166:169], v[234:237], v[134:137]
	v_cvt_pk_bf16_f32 v7, v8, v9
	ds_write_b64 v242, v[6:7] offset:16640
	s_addc_u32 s89, s90, 0
	v_mfma_f32_16x16x32_bf16 v[138:141], v[250:253], v[234:237], v[138:141]
	global_load_dwordx4 v[6:9], v199, s[88:89] nt
	v_mfma_f32_16x16x32_bf16 v[142:145], v[226:229], v[234:237], v[142:145]
	s_waitcnt lgkmcnt(2)
	v_mfma_f32_16x16x32_bf16 v[146:149], v[162:165], v[222:225], v[146:149]
	s_waitcnt vmcnt(11)
	s_add_u32 s88, s87, 0x1e4000
	v_cvt_pk_bf16_f32 v2, v2, v3
	v_mfma_f32_16x16x32_bf16 v[150:153], v[166:169], v[222:225], v[150:153]
	v_cvt_pk_bf16_f32 v3, v4, v5
	ds_write_b64 v242, v[2:3] offset:24832
	s_addc_u32 s89, s90, 0
	v_mfma_f32_16x16x32_bf16 v[154:157], v[250:253], v[222:225], v[154:157]
	global_load_dwordx4 v[2:5], v199, s[88:89] nt
	v_mfma_f32_16x16x32_bf16 v[158:161], v[226:229], v[222:225], v[158:161]
	s_add_i32 s87, s86, 0x8000
	s_cmp_lg_u32 s86, 0x10000
	s_cselect_b32 s86, s87, 0
	s_add_i32 s87, s85, 0x8000
	s_cmp_lg_u32 s85, 0x10000
	s_cselect_b32 s85, s87, 0
	s_add_u32 s2, s2, 0xb0000
	s_addc_u32 s3, s3, 0
	s_add_i32 s39, s39, 0x8000
	v_add_u32_e32 v218, 0x80, v218
	v_add_u32_e32 v219, 0x80, v219
	v_add_u32_e32 v220, 0x80, v220
	v_add_u32_e32 v221, 0x80, v221
	s_add_i32 s88, s39, 0xffff8000
	s_and_b32 s88, s88, 0x8000
	s_add_i32 s88, s88, 0
	s_add_i32 s87, s86, 0
	s_add_i32 s88, s88, 0x18000
	v_add_u32_e32 v246, s88, v212
	v_add_u32_e32 v247, s87, v215
	v_add_u32_e32 v252, s88, v181
	v_add_u32_e32 v254, s88, v172
	v_add_u32_e32 v250, s88, v183
	s_waitcnt lgkmcnt(0)
	s_cmp_lg_u32 s2, 0x14a0000
	s_cbranch_scc1 .Lrot_m1_head
	s_barrier
	v_add_u32_e32 v200, s52, v212
	v_add_u32_e32 v250, 0, v215
	v_add_u32_e32 v215, s52, v181
	v_add_u32_e32 v251, s52, v172
	v_add_u32_e32 v217, s52, v183
	ds_read_b64_tr_b16 v[162:163], v200
	ds_read_b64_tr_b16 v[164:165], v200 offset:2048
	ds_read_b64_tr_b16 v[166:167], v217
	ds_read_b64_tr_b16 v[168:169], v217 offset:2048
	ds_read_b128 v[218:221], v250
	ds_read_b128 v[222:225], v250 offset:2048
	ds_read_b64_tr_b16 v[226:227], v215
	ds_read_b64_tr_b16 v[228:229], v215 offset:2048
	ds_read_b64_tr_b16 v[230:231], v251
	ds_read_b64_tr_b16 v[232:233], v251 offset:2048
	s_waitcnt lgkmcnt(5)
	v_mfma_f32_16x16x32_bf16 v[62:65], v[162:165], v[218:221], v[62:65]
	ds_read_b128 v[234:237], v250 offset:4096
	v_mfma_f32_16x16x32_bf16 v[58:61], v[166:169], v[218:221], v[58:61]
	s_waitcnt lgkmcnt(3)
	v_mfma_f32_16x16x32_bf16 v[54:57], v[226:229], v[218:221], v[54:57]
	s_waitcnt lgkmcnt(1)
	v_mfma_f32_16x16x32_bf16 v[42:45], v[230:233], v[218:221], v[42:45]
	v_mfma_f32_16x16x32_bf16 v[50:53], v[162:165], v[222:225], v[50:53]
	ds_read_b128 v[218:221], v250 offset:6144
	v_mfma_f32_16x16x32_bf16 v[46:49], v[166:169], v[222:225], v[46:49]
	v_mfma_f32_16x16x32_bf16 v[38:41], v[226:229], v[222:225], v[38:41]
	v_mfma_f32_16x16x32_bf16 v[34:37], v[230:233], v[222:225], v[34:37]
	s_waitcnt lgkmcnt(1)
	v_mfma_f32_16x16x32_bf16 v[66:69], v[162:165], v[234:237], v[66:69]
	ds_read_b128 v[222:225], v250 offset:8192
	v_mfma_f32_16x16x32_bf16 v[70:73], v[166:169], v[234:237], v[70:73]
	v_mfma_f32_16x16x32_bf16 v[74:77], v[226:229], v[234:237], v[74:77]
	v_mfma_f32_16x16x32_bf16 v[78:81], v[230:233], v[234:237], v[78:81]
	s_waitcnt lgkmcnt(1)
	v_mfma_f32_16x16x32_bf16 v[82:85], v[162:165], v[218:221], v[82:85]
	ds_read_b128 v[234:237], v250 offset:10240
	v_mfma_f32_16x16x32_bf16 v[86:89], v[166:169], v[218:221], v[86:89]
	v_mfma_f32_16x16x32_bf16 v[90:93], v[226:229], v[218:221], v[90:93]
	v_mfma_f32_16x16x32_bf16 v[94:97], v[230:233], v[218:221], v[94:97]
	ds_read_b128 v[218:221], v250 offset:12288
	ds_read_b64_tr_b16 v[238:239], v200 offset:16384
	ds_read_b64_tr_b16 v[240:241], v200 offset:18432
	s_waitcnt lgkmcnt(4)
	v_mfma_f32_16x16x32_bf16 v[98:101], v[162:165], v[222:225], v[98:101]
	v_mfma_f32_16x16x32_bf16 v[102:105], v[166:169], v[222:225], v[102:105]
	v_mfma_f32_16x16x32_bf16 v[106:109], v[226:229], v[222:225], v[106:109]
	v_mfma_f32_16x16x32_bf16 v[110:113], v[230:233], v[222:225], v[110:113]
	ds_read_b128 v[222:225], v250 offset:14336
	ds_read_b64_tr_b16 v[242:243], v217 offset:16384
	ds_read_b64_tr_b16 v[244:245], v217 offset:18432
	s_waitcnt lgkmcnt(6)
	v_mfma_f32_16x16x32_bf16 v[114:117], v[162:165], v[234:237], v[114:117]
	v_mfma_f32_16x16x32_bf16 v[118:121], v[166:169], v[234:237], v[118:121]
	v_mfma_f32_16x16x32_bf16 v[122:125], v[226:229], v[234:237], v[122:125]
	v_mfma_f32_16x16x32_bf16 v[126:129], v[230:233], v[234:237], v[126:129]
	v_add_u32_e32 v200, 0, v216
	ds_read_b128 v[234:237], v200
	ds_read_b64_tr_b16 v[246:247], v215 offset:16384
	ds_read_b64_tr_b16 v[248:249], v215 offset:18432
	s_waitcnt lgkmcnt(8)
	v_mfma_f32_16x16x32_bf16 v[130:133], v[162:165], v[218:221], v[130:133]
	v_mfma_f32_16x16x32_bf16 v[134:137], v[166:169], v[218:221], v[134:137]
	v_mfma_f32_16x16x32_bf16 v[138:141], v[226:229], v[218:221], v[138:141]
	v_mfma_f32_16x16x32_bf16 v[142:145], v[230:233], v[218:221], v[142:145]
	s_waitcnt lgkmcnt(5)
	v_mfma_f32_16x16x32_bf16 v[146:149], v[162:165], v[222:225], v[146:149]
	v_mfma_f32_16x16x32_bf16 v[150:153], v[166:169], v[222:225], v[150:153]
	ds_read_b128 v[162:165], v200 offset:2048
	ds_read_b64_tr_b16 v[166:167], v251 offset:16384
	ds_read_b64_tr_b16 v[168:169], v251 offset:18432
	v_mfma_f32_16x16x32_bf16 v[154:157], v[226:229], v[222:225], v[154:157]
	v_mfma_f32_16x16x32_bf16 v[158:161], v[230:233], v[222:225], v[158:161]
	ds_read_b128 v[216:219], v200 offset:4096
	s_waitcnt vmcnt(7)
	v_add_u32_e32 v214, s56, v214
	v_cvt_pk_bf16_f32 v30, v30, v31
	v_cvt_pk_bf16_f32 v31, v32, v33
	s_waitcnt lgkmcnt(6)
	v_mfma_f32_16x16x32_bf16 v[62:65], v[238:241], v[234:237], v[62:65]
	ds_write_b64 v214, v[30:31]
	v_mfma_f32_16x16x32_bf16 v[58:61], v[242:245], v[234:237], v[58:61]
	s_waitcnt lgkmcnt(5)
	v_mfma_f32_16x16x32_bf16 v[54:57], v[246:249], v[234:237], v[54:57]
	s_waitcnt lgkmcnt(2)
	v_mfma_f32_16x16x32_bf16 v[30:33], v[166:169], v[234:237], v[42:45]
	v_mfma_f32_16x16x32_bf16 v[42:45], v[238:241], v[162:165], v[50:53]
	s_nop 2
	ds_read_b128 v[50:53], v200 offset:6144
	s_waitcnt vmcnt(6)
	v_mfma_f32_16x16x32_bf16 v[46:49], v[242:245], v[162:165], v[46:49]
	v_cvt_pk_bf16_f32 v26, v26, v27
	v_cvt_pk_bf16_f32 v27, v28, v29
	ds_write_b64 v214, v[26:27] offset:8192
	v_mfma_f32_16x16x32_bf16 v[38:41], v[246:249], v[162:165], v[38:41]
	v_mfma_f32_16x16x32_bf16 v[26:29], v[166:169], v[162:165], v[34:37]
	s_waitcnt lgkmcnt(3)
	v_mfma_f32_16x16x32_bf16 v[34:37], v[238:241], v[216:219], v[66:69]
	v_mfma_f32_16x16x32_bf16 v[66:69], v[242:245], v[216:219], v[70:73]
	s_nop 2
	ds_read_b128 v[70:73], v200 offset:8192
	s_waitcnt vmcnt(5)
	v_mfma_f32_16x16x32_bf16 v[74:77], v[246:249], v[216:219], v[74:77]
	v_cvt_pk_bf16_f32 v22, v22, v23
	v_cvt_pk_bf16_f32 v23, v24, v25
	ds_write_b64 v214, v[22:23] offset:16384
	v_mfma_f32_16x16x32_bf16 v[22:25], v[166:169], v[216:219], v[78:81]
	s_waitcnt lgkmcnt(3)
	v_mfma_f32_16x16x32_bf16 v[78:81], v[238:241], v[50:53], v[82:85]
	v_mfma_f32_16x16x32_bf16 v[82:85], v[242:245], v[50:53], v[86:89]
	s_nop 2
	ds_read_b128 v[86:89], v200 offset:10240
	s_waitcnt vmcnt(4)
	v_mfma_f32_16x16x32_bf16 v[90:93], v[246:249], v[50:53], v[90:93]
	v_cvt_pk_bf16_f32 v18, v18, v19
	v_cvt_pk_bf16_f32 v19, v20, v21
	ds_write_b64 v214, v[18:19] offset:24576
	v_mfma_f32_16x16x32_bf16 v[18:21], v[166:169], v[50:53], v[94:97]
	s_waitcnt lgkmcnt(3)
	v_mfma_f32_16x16x32_bf16 v[50:53], v[238:241], v[70:73], v[98:101]
	v_add_u32_e32 v162, s56, v213
	s_nop 1
	ds_read_b128 v[98:101], v200 offset:12288
	s_waitcnt vmcnt(3)
	v_mfma_f32_16x16x32_bf16 v[94:97], v[242:245], v[70:73], v[102:105]
	v_cvt_pk_bf16_f32 v14, v14, v15
	v_cvt_pk_bf16_f32 v15, v16, v17
	ds_write_b64 v162, v[14:15]
	v_mfma_f32_16x16x32_bf16 v[102:105], v[246:249], v[70:73], v[106:109]
	v_mfma_f32_16x16x32_bf16 v[14:17], v[166:169], v[70:73], v[110:113]
	s_nop 2
	ds_read_b128 v[110:113], v200 offset:14336
	s_waitcnt vmcnt(2)
	s_waitcnt lgkmcnt(4)
	v_mfma_f32_16x16x32_bf16 v[70:73], v[238:241], v[86:89], v[114:117]
	v_cvt_pk_bf16_f32 v10, v10, v11
	v_cvt_pk_bf16_f32 v11, v12, v13
	ds_write_b64 v162, v[10:11] offset:8192
	v_mfma_f32_16x16x32_bf16 v[106:109], v[242:245], v[86:89], v[118:121]
	v_mfma_f32_16x16x32_bf16 v[114:117], v[246:249], v[86:89], v[122:125]
	v_mfma_f32_16x16x32_bf16 v[10:13], v[166:169], v[86:89], v[126:129]
	s_waitcnt vmcnt(1)
	s_waitcnt lgkmcnt(3)
	v_mfma_f32_16x16x32_bf16 v[86:89], v[238:241], v[98:101], v[130:133]
	v_cvt_pk_bf16_f32 v6, v6, v7
	v_cvt_pk_bf16_f32 v7, v8, v9
	ds_write_b64 v162, v[6:7] offset:16384
	v_mfma_f32_16x16x32_bf16 v[118:121], v[242:245], v[98:101], v[134:137]
	v_mfma_f32_16x16x32_bf16 v[122:125], v[246:249], v[98:101], v[138:141]
	v_mfma_f32_16x16x32_bf16 v[6:9], v[166:169], v[98:101], v[142:145]
	s_waitcnt vmcnt(0)
	s_waitcnt lgkmcnt(2)
	v_mfma_f32_16x16x32_bf16 v[98:101], v[238:241], v[110:113], v[146:149]
	v_cvt_pk_bf16_f32 v2, v2, v3
	v_cvt_pk_bf16_f32 v3, v4, v5
	ds_write_b64 v162, v[2:3] offset:24576
	v_mfma_f32_16x16x32_bf16 v[126:129], v[242:245], v[110:113], v[150:153]
	v_mfma_f32_16x16x32_bf16 v[130:133], v[246:249], v[110:113], v[154:157]
	v_mfma_f32_16x16x32_bf16 v[2:5], v[166:169], v[110:113], v[158:161]
	s_waitcnt lgkmcnt(0)
	s_barrier
	v_add_u32_e32 v168, s56, v212
	v_add_u32_e32 v183, s56, v183
	v_add_u32_e32 v181, s56, v181
	ds_read_b64_tr_b16 v[110:111], v168
	ds_read_b64_tr_b16 v[112:113], v168 offset:2048
	ds_read_b64_tr_b16 v[134:135], v183
	ds_read_b64_tr_b16 v[136:137], v183 offset:2048
	ds_read_b128 v[138:141], v250 offset:32768
	ds_read_b64_tr_b16 v[142:143], v181
	ds_read_b128 v[146:149], v250 offset:34816
	ds_read_b128 v[150:153], v250 offset:36864
	ds_read_b64_tr_b16 v[144:145], v181 offset:2048
	v_add_u32_e32 v172, s56, v172
	ds_read_b64_tr_b16 v[154:155], v172
	ds_read_b64_tr_b16 v[156:157], v172 offset:2048
	s_waitcnt lgkmcnt(6)
	v_mfma_f32_16x16x32_bf16 v[62:65], v[110:113], v[138:141], v[62:65]
	v_mfma_f32_16x16x32_bf16 v[58:61], v[134:137], v[138:141], v[58:61]
	s_waitcnt lgkmcnt(2)
	v_mfma_f32_16x16x32_bf16 v[54:57], v[142:145], v[138:141], v[54:57]
	s_waitcnt lgkmcnt(0)
	v_mfma_f32_16x16x32_bf16 v[30:33], v[154:157], v[138:141], v[30:33]
	v_mfma_f32_16x16x32_bf16 v[42:45], v[110:113], v[146:149], v[42:45]
	ds_read_b128 v[138:141], v250 offset:38912
	v_mfma_f32_16x16x32_bf16 v[46:49], v[134:137], v[146:149], v[46:49]
	v_mfma_f32_16x16x32_bf16 v[38:41], v[142:145], v[146:149], v[38:41]
	v_mfma_f32_16x16x32_bf16 v[26:29], v[154:157], v[146:149], v[26:29]
	v_mfma_f32_16x16x32_bf16 v[34:37], v[110:113], v[150:153], v[34:37]
	ds_read_b128 v[146:149], v250 offset:40960
	v_mfma_f32_16x16x32_bf16 v[66:69], v[134:137], v[150:153], v[66:69]
	v_mfma_f32_16x16x32_bf16 v[74:77], v[142:145], v[150:153], v[74:77]
	v_mfma_f32_16x16x32_bf16 v[22:25], v[154:157], v[150:153], v[22:25]
	s_waitcnt lgkmcnt(1)
	v_mfma_f32_16x16x32_bf16 v[150:153], v[134:137], v[138:141], v[82:85]
	s_nop 2
	ds_read_b128 v[82:85], v250 offset:43008
	v_mfma_f32_16x16x32_bf16 v[78:81], v[110:113], v[138:141], v[78:81]
	v_mfma_f32_16x16x32_bf16 v[18:21], v[154:157], v[138:141], v[18:21]
	v_mfma_f32_16x16x32_bf16 v[158:161], v[142:145], v[138:141], v[90:93]
	s_nop 2
	ds_read_b128 v[90:93], v250 offset:45056
	ds_read_b64_tr_b16 v[166:167], v168 offset:16384
	ds_read_b64_tr_b16 v[168:169], v168 offset:18432
	s_waitcnt lgkmcnt(4)
	v_mfma_f32_16x16x32_bf16 v[50:53], v[110:113], v[146:149], v[50:53]
	v_mfma_f32_16x16x32_bf16 v[14:17], v[154:157], v[146:149], v[14:17]
	v_mfma_f32_16x16x32_bf16 v[138:141], v[134:137], v[146:149], v[94:97]
	v_mfma_f32_16x16x32_bf16 v[162:165], v[142:145], v[146:149], v[102:105]
	s_waitcnt lgkmcnt(3)
	v_mfma_f32_16x16x32_bf16 v[146:149], v[110:113], v[82:85], v[70:73]
	s_nop 2
	ds_read_b128 v[70:73], v250 offset:47104
	ds_read_b64_tr_b16 v[220:221], v183 offset:16384
	ds_read_b64_tr_b16 v[222:223], v183 offset:18432
	v_mfma_f32_16x16x32_bf16 v[10:13], v[154:157], v[82:85], v[10:13]
	v_mfma_f32_16x16x32_bf16 v[212:215], v[134:137], v[82:85], v[106:109]
	v_mfma_f32_16x16x32_bf16 v[216:219], v[142:145], v[82:85], v[114:117]
	ds_read_b128 v[82:85], v200 offset:32768
	ds_read_b64_tr_b16 v[236:237], v181 offset:16384
	ds_read_b64_tr_b16 v[238:239], v181 offset:18432
	s_waitcnt lgkmcnt(8)
	v_mfma_f32_16x16x32_bf16 v[6:9], v[154:157], v[90:93], v[6:9]
	v_mfma_f32_16x16x32_bf16 v[224:227], v[110:113], v[90:93], v[86:89]
	v_mfma_f32_16x16x32_bf16 v[228:231], v[134:137], v[90:93], v[118:121]
	v_mfma_f32_16x16x32_bf16 v[232:235], v[142:145], v[90:93], v[122:125]
	s_waitcnt lgkmcnt(5)
	v_mfma_f32_16x16x32_bf16 v[130:133], v[142:145], v[70:73], v[130:133]
	ds_read_b128 v[86:89], v200 offset:34816
	ds_read_b64_tr_b16 v[142:143], v172 offset:16384
	ds_read_b64_tr_b16 v[144:145], v172 offset:18432
	v_mfma_f32_16x16x32_bf16 v[240:243], v[110:113], v[70:73], v[98:101]
	v_mfma_f32_16x16x32_bf16 v[134:137], v[134:137], v[70:73], v[126:129]
	v_mfma_f32_16x16x32_bf16 v[154:157], v[154:157], v[70:73], v[2:5]
	s_nop 2
	ds_read_b128 v[2:5], v200 offset:36864
	s_waitcnt lgkmcnt(6)
	v_mfma_f32_16x16x32_bf16 v[122:125], v[166:169], v[82:85], v[62:65]
	v_mfma_f32_16x16x32_bf16 v[114:117], v[220:223], v[82:85], v[58:61]
	s_waitcnt lgkmcnt(4)
	v_mfma_f32_16x16x32_bf16 v[126:129], v[236:239], v[82:85], v[54:57]
	s_waitcnt lgkmcnt(1)
	v_mfma_f32_16x16x32_bf16 v[118:121], v[142:145], v[82:85], v[30:33]
	s_nop 2
	ds_read_b128 v[30:33], v200 offset:38912
	v_mfma_f32_16x16x32_bf16 v[106:109], v[166:169], v[86:89], v[42:45]
	v_mfma_f32_16x16x32_bf16 v[98:101], v[220:223], v[86:89], v[46:49]
	v_mfma_f32_16x16x32_bf16 v[110:113], v[236:239], v[86:89], v[38:41]
	v_mfma_f32_16x16x32_bf16 v[102:105], v[142:145], v[86:89], v[26:29]
	s_nop 2
	ds_read_b128 v[26:29], v200 offset:40960
	s_waitcnt lgkmcnt(2)
	v_mfma_f32_16x16x32_bf16 v[90:93], v[166:169], v[2:5], v[34:37]
	v_mfma_f32_16x16x32_bf16 v[82:85], v[220:223], v[2:5], v[66:69]
	v_mfma_f32_16x16x32_bf16 v[94:97], v[236:239], v[2:5], v[74:77]
	v_mfma_f32_16x16x32_bf16 v[86:89], v[142:145], v[2:5], v[22:25]
	ds_read_b128 v[2:5], v200 offset:43008
	s_waitcnt lgkmcnt(2)
	v_mfma_f32_16x16x32_bf16 v[74:77], v[166:169], v[30:33], v[78:81]
	v_mfma_f32_16x16x32_bf16 v[66:69], v[220:223], v[30:33], v[150:153]
	v_mfma_f32_16x16x32_bf16 v[78:81], v[236:239], v[30:33], v[158:161]
	v_mfma_f32_16x16x32_bf16 v[70:73], v[142:145], v[30:33], v[18:21]
	ds_read_b128 v[22:25], v200 offset:45056
	s_waitcnt lgkmcnt(2)
	v_mfma_f32_16x16x32_bf16 v[58:61], v[166:169], v[26:29], v[50:53]
	v_mfma_f32_16x16x32_bf16 v[50:53], v[220:223], v[26:29], v[138:141]
	v_mfma_f32_16x16x32_bf16 v[62:65], v[236:239], v[26:29], v[162:165]
	v_mfma_f32_16x16x32_bf16 v[54:57], v[142:145], v[26:29], v[14:17]
	s_waitcnt lgkmcnt(1)
	v_mfma_f32_16x16x32_bf16 v[42:45], v[166:169], v[2:5], v[146:149]
	ds_read_b128 v[138:141], v200 offset:47104
	v_mfma_f32_16x16x32_bf16 v[34:37], v[220:223], v[2:5], v[212:215]
	v_mfma_f32_16x16x32_bf16 v[46:49], v[236:239], v[2:5], v[216:219]
	v_mfma_f32_16x16x32_bf16 v[38:41], v[142:145], v[2:5], v[10:13]
	s_waitcnt lgkmcnt(1)
	v_mfma_f32_16x16x32_bf16 v[26:29], v[166:169], v[22:25], v[224:227]
	v_mfma_f32_16x16x32_bf16 v[18:21], v[220:223], v[22:25], v[228:231]
	v_mfma_f32_16x16x32_bf16 v[30:33], v[236:239], v[22:25], v[232:235]
	v_mfma_f32_16x16x32_bf16 v[22:25], v[142:145], v[22:25], v[6:9]
	s_waitcnt lgkmcnt(0)
	v_mfma_f32_16x16x32_bf16 v[10:13], v[166:169], v[138:141], v[240:243]
	v_mfma_f32_16x16x32_bf16 v[2:5], v[220:223], v[138:141], v[134:137]
	v_mfma_f32_16x16x32_bf16 v[14:17], v[236:239], v[138:141], v[130:133]
	v_mfma_f32_16x16x32_bf16 v[6:9], v[142:145], v[138:141], v[154:157]
	s_waitcnt lgkmcnt(0)
	s_barrier
	s_nop 0
	v_mov_b32_e32 v130, 0
	s_and_b64 vcc, exec, s[6:7]
	v_mov_b32_e32 v131, 0
	v_mov_b32_e32 v132, 0
	s_cbranch_vccnz .LBB0_1436
	global_load_dword v130, v[184:185], off
	global_load_dword v131, v[186:187], off
	global_load_dword v132, v[188:189], off

.LBB0_1446:
	s_add_i32 s87, s37, 0xffff8000
	s_and_b32 s87, s87, 0x8000
	s_add_i32 s87, s87, 0
	s_add_i32 s86, s85, 0
	s_add_i32 s87, s87, 0x18000
	v_add_u32_e32 v240, s87, v185
	v_add_u32_e32 v241, s86, v183
	v_add_u32_e32 v246, s87, v181
	v_add_u32_e32 v248, s87, v172
	v_add_u32_e32 v244, s87, v184
	s_branch .Lrot_mo

.Lrot_mo:
	ds_read_b64_tr_b16 v[216:217], v240
	ds_read_b64_tr_b16 v[218:219], v240 offset:2048
	ds_read_b64_tr_b16 v[220:221], v244
	ds_read_b64_tr_b16 v[222:223], v244 offset:2048
	ds_read_b128 v[162:165], v241
	ds_read_b128 v[166:169], v241 offset:2048
	ds_read_b64_tr_b16 v[224:225], v246
	ds_read_b64_tr_b16 v[226:227], v246 offset:2048
	ds_read_b64_tr_b16 v[228:229], v248
	ds_read_b64_tr_b16 v[230:231], v248 offset:2048
	s_waitcnt lgkmcnt(5)
	v_mfma_f32_16x16x32_bf16 v[62:65], v[216:219], v[162:165], v[62:65]
	ds_read_b128 v[232:235], v241 offset:4096
	s_and_b32 s87, s37, 0x8000
	s_add_i32 s88, s36, s84
	v_mfma_f32_16x16x32_bf16 v[58:61], v[220:223], v[162:165], v[58:61]
	s_mov_b32 s89, m0
	s_mov_b32 m0, s88
	s_nop 0
	global_load_lds_dwordx4 v215, s[18:19]
	s_mov_b32 m0, s89
	s_waitcnt lgkmcnt(3)
	v_mfma_f32_16x16x32_bf16 v[54:57], v[224:227], v[162:165], v[54:57]
	s_waitcnt lgkmcnt(1)
	v_mfma_f32_16x16x32_bf16 v[42:45], v[228:231], v[162:165], v[42:45]
	v_mfma_f32_16x16x32_bf16 v[50:53], v[216:219], v[166:169], v[50:53]
	ds_read_b128 v[162:165], v241 offset:6144
	s_add_i32 s89, s88, 0x2000
	s_mov_b32 s90, m0
	s_mov_b32 m0, s89
	s_nop 0
	global_load_lds_dwordx4 v214, s[18:19]
	s_mov_b32 m0, s90
	v_mfma_f32_16x16x32_bf16 v[46:49], v[220:223], v[166:169], v[46:49]
	v_mfma_f32_16x16x32_bf16 v[38:41], v[224:227], v[166:169], v[38:41]
	v_mfma_f32_16x16x32_bf16 v[34:37], v[228:231], v[166:169], v[34:37]
	s_waitcnt lgkmcnt(1)
	v_mfma_f32_16x16x32_bf16 v[66:69], v[216:219], v[232:235], v[66:69]
	ds_read_b128 v[166:169], v241 offset:8192
	s_add_i32 s89, s88, 0x4000
	s_mov_b32 s90, m0
	s_mov_b32 m0, s89
	s_nop 0
	global_load_lds_dwordx4 v213, s[18:19]
	s_mov_b32 m0, s90
	v_mfma_f32_16x16x32_bf16 v[70:73], v[220:223], v[232:235], v[70:73]
	v_mfma_f32_16x16x32_bf16 v[74:77], v[224:227], v[232:235], v[74:77]
	v_mfma_f32_16x16x32_bf16 v[78:81], v[228:231], v[232:235], v[78:81]
	s_waitcnt lgkmcnt(1)
	v_mfma_f32_16x16x32_bf16 v[82:85], v[216:219], v[162:165], v[82:85]
	ds_read_b128 v[232:235], v241 offset:10240
	s_addk_i32 s88, 0x6000
	s_mov_b32 s89, m0
	s_mov_b32 m0, s88
	s_nop 0
	global_load_lds_dwordx4 v212, s[18:19]
	s_mov_b32 m0, s89
	v_mfma_f32_16x16x32_bf16 v[86:89], v[220:223], v[162:165], v[86:89]
	v_mfma_f32_16x16x32_bf16 v[90:93], v[224:227], v[162:165], v[90:93]
	v_mfma_f32_16x16x32_bf16 v[94:97], v[228:231], v[162:165], v[94:97]
	ds_read_b128 v[236:239], v241 offset:12288
	ds_read_b64_tr_b16 v[162:163], v240 offset:16384
	ds_read_b64_tr_b16 v[164:165], v240 offset:18432
	s_waitcnt lgkmcnt(4)
	v_mfma_f32_16x16x32_bf16 v[98:101], v[216:219], v[166:169], v[98:101]
	v_mfma_f32_16x16x32_bf16 v[102:105], v[220:223], v[166:169], v[102:105]
	v_mfma_f32_16x16x32_bf16 v[106:109], v[224:227], v[166:169], v[106:109]
	v_mfma_f32_16x16x32_bf16 v[110:113], v[228:231], v[166:169], v[110:113]
	ds_read_b128 v[240:243], v241 offset:14336
	ds_read_b64_tr_b16 v[166:167], v244 offset:16384
	ds_read_b64_tr_b16 v[168:169], v244 offset:18432
	s_waitcnt lgkmcnt(6)
	v_mfma_f32_16x16x32_bf16 v[114:117], v[216:219], v[232:235], v[114:117]
	v_mfma_f32_16x16x32_bf16 v[118:121], v[220:223], v[232:235], v[118:121]
	v_mfma_f32_16x16x32_bf16 v[122:125], v[224:227], v[232:235], v[122:125]
	v_mfma_f32_16x16x32_bf16 v[126:129], v[228:231], v[232:235], v[126:129]
	v_add_u32_e32 v249, s86, v187
	ds_read_b128 v[232:235], v249
	ds_read_b64_tr_b16 v[244:245], v246 offset:16384
	ds_read_b64_tr_b16 v[246:247], v246 offset:18432
	s_waitcnt lgkmcnt(8)
	v_mfma_f32_16x16x32_bf16 v[130:133], v[216:219], v[236:239], v[130:133]
	v_mfma_f32_16x16x32_bf16 v[134:137], v[220:223], v[236:239], v[134:137]
	v_mfma_f32_16x16x32_bf16 v[138:141], v[224:227], v[236:239], v[138:141]
	v_mfma_f32_16x16x32_bf16 v[142:145], v[228:231], v[236:239], v[142:145]
	s_waitcnt lgkmcnt(5)
	v_mfma_f32_16x16x32_bf16 v[146:149], v[216:219], v[240:243], v[146:149]
	v_mfma_f32_16x16x32_bf16 v[150:153], v[220:223], v[240:243], v[150:153]
	ds_read_b128 v[216:219], v249 offset:2048
	ds_read_b64_tr_b16 v[220:221], v248 offset:16384
	ds_read_b64_tr_b16 v[222:223], v248 offset:18432
	v_mfma_f32_16x16x32_bf16 v[154:157], v[224:227], v[240:243], v[154:157]
	v_mfma_f32_16x16x32_bf16 v[158:161], v[228:231], v[240:243], v[158:161]
	ds_read_b128 v[224:227], v249 offset:4096
	s_waitcnt lgkmcnt(6)
	v_mfma_f32_16x16x32_bf16 v[62:65], v[162:165], v[232:235], v[62:65]
	s_add_u32 s88, s40, s2
	s_waitcnt vmcnt(11)
	s_addc_u32 s89, s41, s3
	v_mfma_f32_16x16x32_bf16 v[58:61], v[166:169], v[232:235], v[58:61]
	v_cvt_pk_bf16_f32 v30, v30, v31
	v_cvt_pk_bf16_f32 v31, v32, v33
	v_add_u32_e32 v236, s87, v189
	s_waitcnt lgkmcnt(4)
	v_mfma_f32_16x16x32_bf16 v[54:57], v[244:247], v[232:235], v[54:57]
	s_add_u32 s86, s88, 0x160000
	ds_write_b64 v236, v[30:31]
	s_addc_u32 s87, s89, 0
	s_waitcnt lgkmcnt(2)
	v_mfma_f32_16x16x32_bf16 v[42:45], v[220:223], v[232:235], v[42:45]
	global_load_dwordx4 v[30:33], v199, s[86:87]
	v_mfma_f32_16x16x32_bf16 v[50:53], v[162:165], v[216:219], v[50:53]
	ds_read_b128 v[228:231], v249 offset:6144
	s_waitcnt vmcnt(11)
	s_add_u32 s86, s88, 0x18c000
	v_mfma_f32_16x16x32_bf16 v[46:49], v[166:169], v[216:219], v[46:49]
	v_cvt_pk_bf16_f32 v26, v26, v27
	v_cvt_pk_bf16_f32 v27, v28, v29
	ds_write_b64 v236, v[26:27] offset:8192
	v_mfma_f32_16x16x32_bf16 v[38:41], v[244:247], v[216:219], v[38:41]
	s_addc_u32 s87, s89, 0
	global_load_dwordx4 v[26:29], v199, s[86:87]
	v_mfma_f32_16x16x32_bf16 v[34:37], v[220:223], v[216:219], v[34:37]
	s_waitcnt lgkmcnt(3)
	v_mfma_f32_16x16x32_bf16 v[66:69], v[162:165], v[224:227], v[66:69]
	ds_read_b128 v[216:219], v249 offset:8192
	s_waitcnt vmcnt(11)
	s_add_u32 s86, s88, 0x1b8000
	v_mfma_f32_16x16x32_bf16 v[70:73], v[166:169], v[224:227], v[70:73]
	v_cvt_pk_bf16_f32 v22, v22, v23
	v_cvt_pk_bf16_f32 v23, v24, v25
	ds_write_b64 v236, v[22:23] offset:16384
	v_mfma_f32_16x16x32_bf16 v[74:77], v[244:247], v[224:227], v[74:77]
	s_addc_u32 s87, s89, 0
	global_load_dwordx4 v[22:25], v199, s[86:87]
	v_mfma_f32_16x16x32_bf16 v[78:81], v[220:223], v[224:227], v[78:81]
	s_waitcnt lgkmcnt(3)
	v_mfma_f32_16x16x32_bf16 v[82:85], v[162:165], v[228:231], v[82:85]
	ds_read_b128 v[224:227], v249 offset:10240
	s_waitcnt vmcnt(11)
	s_add_u32 s86, s88, 0x1e4000
	v_mfma_f32_16x16x32_bf16 v[86:89], v[166:169], v[228:231], v[86:89]
	v_cvt_pk_bf16_f32 v18, v18, v19
	v_cvt_pk_bf16_f32 v19, v20, v21
	ds_write_b64 v236, v[18:19] offset:24576
	v_mfma_f32_16x16x32_bf16 v[90:93], v[244:247], v[228:231], v[90:93]
	s_addc_u32 s87, s89, 0
	global_load_dwordx4 v[18:21], v199, s[86:87]
	v_mfma_f32_16x16x32_bf16 v[94:97], v[220:223], v[228:231], v[94:97]
	ds_read_b128 v[228:231], v249 offset:12288
	s_waitcnt lgkmcnt(4)
	v_mfma_f32_16x16x32_bf16 v[98:101], v[162:165], v[216:219], v[98:101]
	s_add_u32 s88, s38, s2
	s_waitcnt vmcnt(11)
	s_addc_u32 s89, s39, s3
	v_mfma_f32_16x16x32_bf16 v[102:105], v[166:169], v[216:219], v[102:105]
	v_cvt_pk_bf16_f32 v14, v14, v15
	v_cvt_pk_bf16_f32 v15, v16, v17
	s_add_u32 s86, s88, 0x160000
	v_mfma_f32_16x16x32_bf16 v[106:109], v[244:247], v[216:219], v[106:109]
	ds_write_b64 v236, v[14:15] offset:256
	s_addc_u32 s87, s89, 0
	global_load_dwordx4 v[14:17], v199, s[86:87]
	v_mfma_f32_16x16x32_bf16 v[110:113], v[220:223], v[216:219], v[110:113]
	s_waitcnt lgkmcnt(3)
	v_mfma_f32_16x16x32_bf16 v[114:117], v[162:165], v[224:227], v[114:117]
	ds_read_b128 v[216:219], v249 offset:14336
	s_waitcnt vmcnt(11)
	s_add_u32 s86, s88, 0x18c000
	v_mfma_f32_16x16x32_bf16 v[118:121], v[166:169], v[224:227], v[118:121]
	v_cvt_pk_bf16_f32 v10, v10, v11
	v_cvt_pk_bf16_f32 v11, v12, v13
	ds_write_b64 v236, v[10:11] offset:8448
	v_mfma_f32_16x16x32_bf16 v[122:125], v[244:247], v[224:227], v[122:125]
	s_addc_u32 s87, s89, 0
	global_load_dwordx4 v[10:13], v199, s[86:87]
	v_mfma_f32_16x16x32_bf16 v[126:129], v[220:223], v[224:227], v[126:129]
	s_waitcnt lgkmcnt(3)
	v_mfma_f32_16x16x32_bf16 v[130:133], v[162:165], v[228:231], v[130:133]
	s_waitcnt vmcnt(11)
	s_add_u32 s86, s88, 0x1b8000
	v_cvt_pk_bf16_f32 v6, v6, v7
	v_mfma_f32_16x16x32_bf16 v[134:137], v[166:169], v[228:231], v[134:137]
	v_cvt_pk_bf16_f32 v7, v8, v9
	ds_write_b64 v236, v[6:7] offset:16640
	s_addc_u32 s87, s89, 0
	v_mfma_f32_16x16x32_bf16 v[138:141], v[244:247], v[228:231], v[138:141]
	global_load_dwordx4 v[6:9], v199, s[86:87]
	v_mfma_f32_16x16x32_bf16 v[142:145], v[220:223], v[228:231], v[142:145]
	s_waitcnt lgkmcnt(2)
	v_mfma_f32_16x16x32_bf16 v[146:149], v[162:165], v[216:219], v[146:149]
	s_waitcnt vmcnt(11)
	s_add_u32 s86, s88, 0x1e4000
	v_cvt_pk_bf16_f32 v2, v2, v3
	v_mfma_f32_16x16x32_bf16 v[150:153], v[166:169], v[216:219], v[150:153]
	v_cvt_pk_bf16_f32 v3, v4, v5
	ds_write_b64 v236, v[2:3] offset:24832
	s_addc_u32 s87, s89, 0
	v_mfma_f32_16x16x32_bf16 v[154:157], v[244:247], v[216:219], v[154:157]
	global_load_dwordx4 v[2:5], v199, s[86:87]
	v_mfma_f32_16x16x32_bf16 v[158:161], v[220:223], v[216:219], v[158:161]
	s_add_i32 s86, s85, 0x8000
	s_cmp_lg_u32 s85, 0x10000
	s_cselect_b32 s85, s86, 0
	s_add_i32 s86, s84, 0x8000
	s_cmp_lg_u32 s84, 0x10000
	s_cselect_b32 s84, s86, 0
	s_add_u32 s2, s2, 0xb0000
	s_addc_u32 s3, s3, 0
	s_add_i32 s37, s37, 0x8000
	v_add_u32_e32 v212, 0x80, v212
	v_add_u32_e32 v213, 0x80, v213
	v_add_u32_e32 v214, 0x80, v214
	v_add_u32_e32 v215, 0x80, v215
	s_add_i32 s87, s37, 0xffff8000
	s_and_b32 s87, s87, 0x8000
	s_add_i32 s87, s87, 0
	s_add_i32 s86, s85, 0
	s_add_i32 s87, s87, 0x18000
	v_add_u32_e32 v240, s87, v185
	v_add_u32_e32 v241, s86, v183
	v_add_u32_e32 v246, s87, v181
	v_add_u32_e32 v248, s87, v172
	v_add_u32_e32 v244, s87, v184
	s_waitcnt lgkmcnt(0)
	s_cmp_lg_u32 s2, 0xb00000
	s_cbranch_scc1 .Lrot_mo_head
	s_barrier
	v_add_u32_e32 v189, s52, v185
	v_add_u32_e32 v236, 0, v183
	v_add_u32_e32 v242, s52, v181
	v_add_u32_e32 v244, s52, v172
	v_add_u32_e32 v238, s52, v184
	ds_read_b64_tr_b16 v[162:163], v189
	ds_read_b64_tr_b16 v[164:165], v189 offset:2048
	ds_read_b64_tr_b16 v[166:167], v238
	ds_read_b64_tr_b16 v[168:169], v238 offset:2048
	ds_read_b128 v[212:215], v236 offset:32768
	ds_read_b128 v[216:219], v236 offset:34816
	ds_read_b64_tr_b16 v[220:221], v242
	ds_read_b64_tr_b16 v[222:223], v242 offset:2048
	ds_read_b64_tr_b16 v[224:225], v244
	ds_read_b64_tr_b16 v[226:227], v244 offset:2048
	s_waitcnt lgkmcnt(5)
	v_mfma_f32_16x16x32_bf16 v[62:65], v[162:165], v[212:215], v[62:65]
	ds_read_b128 v[228:231], v236 offset:36864
	v_mfma_f32_16x16x32_bf16 v[58:61], v[166:169], v[212:215], v[58:61]
	s_waitcnt lgkmcnt(3)
	v_mfma_f32_16x16x32_bf16 v[54:57], v[220:223], v[212:215], v[54:57]
	s_waitcnt lgkmcnt(1)
	v_mfma_f32_16x16x32_bf16 v[42:45], v[224:227], v[212:215], v[42:45]
	v_mfma_f32_16x16x32_bf16 v[50:53], v[162:165], v[216:219], v[50:53]
	ds_read_b128 v[212:215], v236 offset:38912
	v_mfma_f32_16x16x32_bf16 v[46:49], v[166:169], v[216:219], v[46:49]
	v_mfma_f32_16x16x32_bf16 v[38:41], v[220:223], v[216:219], v[38:41]
	v_mfma_f32_16x16x32_bf16 v[34:37], v[224:227], v[216:219], v[34:37]
	s_waitcnt lgkmcnt(1)
	v_mfma_f32_16x16x32_bf16 v[66:69], v[162:165], v[228:231], v[66:69]
	ds_read_b128 v[216:219], v236 offset:40960
	v_mfma_f32_16x16x32_bf16 v[70:73], v[166:169], v[228:231], v[70:73]
	v_mfma_f32_16x16x32_bf16 v[74:77], v[220:223], v[228:231], v[74:77]
	v_mfma_f32_16x16x32_bf16 v[78:81], v[224:227], v[228:231], v[78:81]
	s_waitcnt lgkmcnt(1)
	v_mfma_f32_16x16x32_bf16 v[82:85], v[162:165], v[212:215], v[82:85]
	ds_read_b128 v[228:231], v236 offset:43008
	v_mfma_f32_16x16x32_bf16 v[86:89], v[166:169], v[212:215], v[86:89]
	v_mfma_f32_16x16x32_bf16 v[90:93], v[220:223], v[212:215], v[90:93]
	v_mfma_f32_16x16x32_bf16 v[94:97], v[224:227], v[212:215], v[94:97]
	ds_read_b128 v[212:215], v236 offset:45056
	ds_read_b64_tr_b16 v[232:233], v189 offset:16384
	ds_read_b64_tr_b16 v[234:235], v189 offset:18432
	s_waitcnt lgkmcnt(4)
	v_mfma_f32_16x16x32_bf16 v[98:101], v[162:165], v[216:219], v[98:101]
	v_mfma_f32_16x16x32_bf16 v[102:105], v[166:169], v[216:219], v[102:105]
	v_mfma_f32_16x16x32_bf16 v[106:109], v[220:223], v[216:219], v[106:109]
	v_mfma_f32_16x16x32_bf16 v[110:113], v[224:227], v[216:219], v[110:113]
	ds_read_b128 v[216:219], v236 offset:47104
	ds_read_b64_tr_b16 v[236:237], v238 offset:16384
	ds_read_b64_tr_b16 v[238:239], v238 offset:18432
	s_waitcnt lgkmcnt(6)
	v_mfma_f32_16x16x32_bf16 v[114:117], v[162:165], v[228:231], v[114:117]
	v_mfma_f32_16x16x32_bf16 v[118:121], v[166:169], v[228:231], v[118:121]
	v_mfma_f32_16x16x32_bf16 v[122:125], v[220:223], v[228:231], v[122:125]
	v_mfma_f32_16x16x32_bf16 v[126:129], v[224:227], v[228:231], v[126:129]
	v_add_u32_e32 v189, 0, v187
	ds_read_b128 v[228:231], v189 offset:32768
	ds_read_b64_tr_b16 v[240:241], v242 offset:16384
	ds_read_b64_tr_b16 v[242:243], v242 offset:18432
	s_waitcnt lgkmcnt(8)
	v_mfma_f32_16x16x32_bf16 v[130:133], v[162:165], v[212:215], v[130:133]
	v_mfma_f32_16x16x32_bf16 v[134:137], v[166:169], v[212:215], v[134:137]
	v_mfma_f32_16x16x32_bf16 v[138:141], v[220:223], v[212:215], v[138:141]
	v_mfma_f32_16x16x32_bf16 v[142:145], v[224:227], v[212:215], v[142:145]
	s_waitcnt lgkmcnt(5)
	v_mfma_f32_16x16x32_bf16 v[146:149], v[162:165], v[216:219], v[146:149]
	v_mfma_f32_16x16x32_bf16 v[150:153], v[166:169], v[216:219], v[150:153]
	ds_read_b128 v[162:165], v189 offset:34816
	ds_read_b64_tr_b16 v[166:167], v244 offset:16384
	ds_read_b64_tr_b16 v[168:169], v244 offset:18432
	v_mfma_f32_16x16x32_bf16 v[154:157], v[220:223], v[216:219], v[154:157]
	v_mfma_f32_16x16x32_bf16 v[158:161], v[224:227], v[216:219], v[158:161]
	ds_read_b128 v[212:215], v189 offset:36864
	s_waitcnt vmcnt(7)
	v_add_u32_e32 v188, s56, v188
	v_cvt_pk_bf16_f32 v30, v30, v31
	v_cvt_pk_bf16_f32 v31, v32, v33
	s_waitcnt lgkmcnt(6)
	v_mfma_f32_16x16x32_bf16 v[62:65], v[232:235], v[228:231], v[62:65]
	ds_write_b64 v188, v[30:31]
	v_mfma_f32_16x16x32_bf16 v[58:61], v[236:239], v[228:231], v[58:61]
	s_waitcnt lgkmcnt(5)
	v_mfma_f32_16x16x32_bf16 v[54:57], v[240:243], v[228:231], v[54:57]
	s_waitcnt lgkmcnt(2)
	v_mfma_f32_16x16x32_bf16 v[30:33], v[166:169], v[228:231], v[42:45]
	v_mfma_f32_16x16x32_bf16 v[42:45], v[232:235], v[162:165], v[50:53]
	s_nop 2
	ds_read_b128 v[50:53], v189 offset:38912
	s_waitcnt vmcnt(6)
	v_mfma_f32_16x16x32_bf16 v[46:49], v[236:239], v[162:165], v[46:49]
	v_cvt_pk_bf16_f32 v26, v26, v27
	v_cvt_pk_bf16_f32 v27, v28, v29
	ds_write_b64 v188, v[26:27] offset:8192
	v_mfma_f32_16x16x32_bf16 v[38:41], v[240:243], v[162:165], v[38:41]
	v_mfma_f32_16x16x32_bf16 v[26:29], v[166:169], v[162:165], v[34:37]
	s_waitcnt lgkmcnt(3)
	v_mfma_f32_16x16x32_bf16 v[34:37], v[232:235], v[212:215], v[66:69]
	v_mfma_f32_16x16x32_bf16 v[66:69], v[236:239], v[212:215], v[70:73]
	s_nop 2
	ds_read_b128 v[70:73], v189 offset:40960
	s_waitcnt vmcnt(5)
	v_mfma_f32_16x16x32_bf16 v[74:77], v[240:243], v[212:215], v[74:77]
	v_cvt_pk_bf16_f32 v22, v22, v23
	v_cvt_pk_bf16_f32 v23, v24, v25
	ds_write_b64 v188, v[22:23] offset:16384
	v_mfma_f32_16x16x32_bf16 v[22:25], v[166:169], v[212:215], v[78:81]
	s_waitcnt lgkmcnt(3)
	v_mfma_f32_16x16x32_bf16 v[78:81], v[232:235], v[50:53], v[82:85]
	v_mfma_f32_16x16x32_bf16 v[82:85], v[236:239], v[50:53], v[86:89]
	s_nop 2
	ds_read_b128 v[86:89], v189 offset:43008
	s_waitcnt vmcnt(4)
	v_mfma_f32_16x16x32_bf16 v[90:93], v[240:243], v[50:53], v[90:93]
	v_cvt_pk_bf16_f32 v18, v18, v19
	v_cvt_pk_bf16_f32 v19, v20, v21
	ds_write_b64 v188, v[18:19] offset:24576
	v_mfma_f32_16x16x32_bf16 v[18:21], v[166:169], v[50:53], v[94:97]
	s_waitcnt lgkmcnt(3)
	v_mfma_f32_16x16x32_bf16 v[50:53], v[232:235], v[70:73], v[98:101]
	v_add_u32_e32 v162, s56, v186
	s_nop 1
	ds_read_b128 v[98:101], v189 offset:45056
	s_waitcnt vmcnt(3)
	v_mfma_f32_16x16x32_bf16 v[94:97], v[236:239], v[70:73], v[102:105]
	v_cvt_pk_bf16_f32 v14, v14, v15
	v_cvt_pk_bf16_f32 v15, v16, v17
	ds_write_b64 v162, v[14:15]
	v_mfma_f32_16x16x32_bf16 v[102:105], v[240:243], v[70:73], v[106:109]
	v_mfma_f32_16x16x32_bf16 v[14:17], v[166:169], v[70:73], v[110:113]
	s_nop 2
	ds_read_b128 v[110:113], v189 offset:47104
	s_waitcnt vmcnt(2)
	s_waitcnt lgkmcnt(4)
	v_mfma_f32_16x16x32_bf16 v[70:73], v[232:235], v[86:89], v[114:117]
	v_cvt_pk_bf16_f32 v10, v10, v11
	v_cvt_pk_bf16_f32 v11, v12, v13
	ds_write_b64 v162, v[10:11] offset:8192
	v_mfma_f32_16x16x32_bf16 v[106:109], v[236:239], v[86:89], v[118:121]
	v_mfma_f32_16x16x32_bf16 v[114:117], v[240:243], v[86:89], v[122:125]
	v_mfma_f32_16x16x32_bf16 v[10:13], v[166:169], v[86:89], v[126:129]
	s_waitcnt vmcnt(1)
	s_waitcnt lgkmcnt(3)
	v_mfma_f32_16x16x32_bf16 v[86:89], v[232:235], v[98:101], v[130:133]
	v_cvt_pk_bf16_f32 v6, v6, v7
	v_cvt_pk_bf16_f32 v7, v8, v9
	ds_write_b64 v162, v[6:7] offset:16384
	v_mfma_f32_16x16x32_bf16 v[118:121], v[236:239], v[98:101], v[134:137]
	v_mfma_f32_16x16x32_bf16 v[122:125], v[240:243], v[98:101], v[138:141]
	v_mfma_f32_16x16x32_bf16 v[6:9], v[166:169], v[98:101], v[142:145]
	s_waitcnt vmcnt(0)
	s_waitcnt lgkmcnt(2)
	v_mfma_f32_16x16x32_bf16 v[98:101], v[232:235], v[110:113], v[146:149]
	v_cvt_pk_bf16_f32 v2, v2, v3
	v_cvt_pk_bf16_f32 v3, v4, v5
	ds_write_b64 v162, v[2:3] offset:24576
	v_mfma_f32_16x16x32_bf16 v[126:129], v[236:239], v[110:113], v[150:153]
	v_mfma_f32_16x16x32_bf16 v[2:5], v[166:169], v[110:113], v[158:161]
	v_mfma_f32_16x16x32_bf16 v[130:133], v[240:243], v[110:113], v[154:157]
	s_add_i32 s2, 0, 0x10000
	s_waitcnt lgkmcnt(0)
	s_barrier
	v_add_u32_e32 v168, s56, v185
	v_add_u32_e32 v183, s2, v183
	v_add_u32_e32 v181, s56, v181
	v_add_u32_e32 v172, s56, v172
	v_add_u32_e32 v184, s56, v184
	ds_read_b64_tr_b16 v[110:111], v168
	ds_read_b64_tr_b16 v[112:113], v168 offset:2048
	ds_read_b64_tr_b16 v[134:135], v184
	ds_read_b64_tr_b16 v[136:137], v184 offset:2048
	ds_read_b128 v[138:141], v183
	ds_read_b128 v[142:145], v183 offset:2048
	ds_read_b64_tr_b16 v[146:147], v181
	ds_read_b64_tr_b16 v[148:149], v181 offset:2048
	ds_read_b64_tr_b16 v[150:151], v172
	ds_read_b64_tr_b16 v[152:153], v172 offset:2048
	s_waitcnt lgkmcnt(5)
	v_mfma_f32_16x16x32_bf16 v[62:65], v[110:113], v[138:141], v[62:65]
	ds_read_b128 v[154:157], v183 offset:4096
	v_mfma_f32_16x16x32_bf16 v[58:61], v[134:137], v[138:141], v[58:61]
	s_waitcnt lgkmcnt(3)
	v_mfma_f32_16x16x32_bf16 v[54:57], v[146:149], v[138:141], v[54:57]
	s_waitcnt lgkmcnt(1)
	v_mfma_f32_16x16x32_bf16 v[30:33], v[150:153], v[138:141], v[30:33]
	v_mfma_f32_16x16x32_bf16 v[42:45], v[110:113], v[142:145], v[42:45]
	ds_read_b128 v[138:141], v183 offset:6144
	v_mfma_f32_16x16x32_bf16 v[46:49], v[134:137], v[142:145], v[46:49]
	v_mfma_f32_16x16x32_bf16 v[38:41], v[146:149], v[142:145], v[38:41]
	v_mfma_f32_16x16x32_bf16 v[26:29], v[150:153], v[142:145], v[26:29]
	s_waitcnt lgkmcnt(1)
	v_mfma_f32_16x16x32_bf16 v[34:37], v[110:113], v[154:157], v[34:37]
	ds_read_b128 v[142:145], v183 offset:8192
	v_mfma_f32_16x16x32_bf16 v[66:69], v[134:137], v[154:157], v[66:69]
	v_mfma_f32_16x16x32_bf16 v[74:77], v[146:149], v[154:157], v[74:77]
	v_mfma_f32_16x16x32_bf16 v[22:25], v[150:153], v[154:157], v[22:25]
	s_waitcnt lgkmcnt(1)
	v_mfma_f32_16x16x32_bf16 v[154:157], v[134:137], v[138:141], v[82:85]
	s_nop 2
	ds_read_b128 v[82:85], v183 offset:10240
	v_mfma_f32_16x16x32_bf16 v[78:81], v[110:113], v[138:141], v[78:81]
	v_mfma_f32_16x16x32_bf16 v[18:21], v[150:153], v[138:141], v[18:21]
	v_mfma_f32_16x16x32_bf16 v[158:161], v[146:149], v[138:141], v[90:93]
	s_nop 2
	ds_read_b128 v[90:93], v183 offset:12288
	ds_read_b64_tr_b16 v[166:167], v168 offset:16384
	ds_read_b64_tr_b16 v[168:169], v168 offset:18432
	s_waitcnt lgkmcnt(4)
	v_mfma_f32_16x16x32_bf16 v[50:53], v[110:113], v[142:145], v[50:53]
	v_mfma_f32_16x16x32_bf16 v[14:17], v[150:153], v[142:145], v[14:17]
	v_mfma_f32_16x16x32_bf16 v[138:141], v[134:137], v[142:145], v[94:97]
	v_mfma_f32_16x16x32_bf16 v[162:165], v[146:149], v[142:145], v[102:105]
	s_waitcnt lgkmcnt(3)
	v_mfma_f32_16x16x32_bf16 v[142:145], v[110:113], v[82:85], v[70:73]
	s_nop 2
	ds_read_b128 v[70:73], v183 offset:14336
	ds_read_b64_tr_b16 v[220:221], v184 offset:16384
	ds_read_b64_tr_b16 v[222:223], v184 offset:18432
	v_mfma_f32_16x16x32_bf16 v[10:13], v[150:153], v[82:85], v[10:13]
	v_mfma_f32_16x16x32_bf16 v[212:215], v[134:137], v[82:85], v[106:109]
	v_mfma_f32_16x16x32_bf16 v[216:219], v[146:149], v[82:85], v[114:117]
	v_add_u32_e32 v183, s2, v187
	ds_read_b128 v[82:85], v183
	ds_read_b64_tr_b16 v[232:233], v181 offset:16384
	ds_read_b64_tr_b16 v[234:235], v181 offset:18432
	s_waitcnt lgkmcnt(8)
	v_mfma_f32_16x16x32_bf16 v[6:9], v[150:153], v[90:93], v[6:9]
	v_mfma_f32_16x16x32_bf16 v[224:227], v[110:113], v[90:93], v[86:89]
	v_mfma_f32_16x16x32_bf16 v[228:231], v[134:137], v[90:93], v[118:121]
	v_mfma_f32_16x16x32_bf16 v[184:187], v[146:149], v[90:93], v[122:125]
	s_waitcnt lgkmcnt(5)
	v_mfma_f32_16x16x32_bf16 v[130:133], v[146:149], v[70:73], v[130:133]
	ds_read_b128 v[86:89], v183 offset:2048
	ds_read_b64_tr_b16 v[146:147], v172 offset:16384
	ds_read_b64_tr_b16 v[148:149], v172 offset:18432
	v_mfma_f32_16x16x32_bf16 v[2:5], v[150:153], v[70:73], v[2:5]
	v_mfma_f32_16x16x32_bf16 v[236:239], v[110:113], v[70:73], v[98:101]
	v_mfma_f32_16x16x32_bf16 v[134:137], v[134:137], v[70:73], v[126:129]
	s_waitcnt lgkmcnt(3)
	v_mfma_f32_16x16x32_bf16 v[122:125], v[232:235], v[82:85], v[54:57]
	s_nop 2
	ds_read_b128 v[54:57], v183 offset:4096
	v_mfma_f32_16x16x32_bf16 v[126:129], v[166:169], v[82:85], v[62:65]
	v_mfma_f32_16x16x32_bf16 v[118:121], v[220:223], v[82:85], v[58:61]
	s_waitcnt lgkmcnt(1)
	v_mfma_f32_16x16x32_bf16 v[114:117], v[146:149], v[82:85], v[30:33]
	s_nop 2
	ds_read_b128 v[30:33], v183 offset:6144
	v_mfma_f32_16x16x32_bf16 v[110:113], v[166:169], v[86:89], v[42:45]
	v_mfma_f32_16x16x32_bf16 v[102:105], v[220:223], v[86:89], v[46:49]
	v_mfma_f32_16x16x32_bf16 v[106:109], v[232:235], v[86:89], v[38:41]
	v_mfma_f32_16x16x32_bf16 v[98:101], v[146:149], v[86:89], v[26:29]
	s_nop 2
	ds_read_b128 v[26:29], v183 offset:8192
	s_waitcnt lgkmcnt(2)
	v_mfma_f32_16x16x32_bf16 v[94:97], v[166:169], v[54:57], v[34:37]
	v_mfma_f32_16x16x32_bf16 v[86:89], v[220:223], v[54:57], v[66:69]
	v_mfma_f32_16x16x32_bf16 v[90:93], v[232:235], v[54:57], v[74:77]
	v_mfma_f32_16x16x32_bf16 v[82:85], v[146:149], v[54:57], v[22:25]
	s_nop 2
	ds_read_b128 v[22:25], v183 offset:10240
	s_waitcnt lgkmcnt(2)
	v_mfma_f32_16x16x32_bf16 v[78:81], v[166:169], v[30:33], v[78:81]
	v_mfma_f32_16x16x32_bf16 v[70:73], v[220:223], v[30:33], v[154:157]
	v_mfma_f32_16x16x32_bf16 v[74:77], v[232:235], v[30:33], v[158:161]
	v_mfma_f32_16x16x32_bf16 v[66:69], v[146:149], v[30:33], v[18:21]
	s_nop 2
	ds_read_b128 v[18:21], v183 offset:12288
	s_waitcnt lgkmcnt(2)
	v_mfma_f32_16x16x32_bf16 v[62:65], v[166:169], v[26:29], v[50:53]
	v_mfma_f32_16x16x32_bf16 v[54:57], v[220:223], v[26:29], v[138:141]
	v_mfma_f32_16x16x32_bf16 v[58:61], v[232:235], v[26:29], v[162:165]
	v_mfma_f32_16x16x32_bf16 v[50:53], v[146:149], v[26:29], v[14:17]
	s_waitcnt lgkmcnt(1)
	v_mfma_f32_16x16x32_bf16 v[46:49], v[166:169], v[22:25], v[142:145]
	ds_read_b128 v[138:141], v183 offset:14336
	v_mfma_f32_16x16x32_bf16 v[38:41], v[220:223], v[22:25], v[212:215]
	v_mfma_f32_16x16x32_bf16 v[42:45], v[232:235], v[22:25], v[216:219]
	v_mfma_f32_16x16x32_bf16 v[34:37], v[146:149], v[22:25], v[10:13]
	s_waitcnt lgkmcnt(1)
	v_mfma_f32_16x16x32_bf16 v[30:33], v[166:169], v[18:21], v[224:227]
	v_mfma_f32_16x16x32_bf16 v[22:25], v[220:223], v[18:21], v[228:231]
	v_mfma_f32_16x16x32_bf16 v[26:29], v[232:235], v[18:21], v[184:187]
	v_mfma_f32_16x16x32_bf16 v[18:21], v[146:149], v[18:21], v[6:9]
	s_waitcnt lgkmcnt(0)
	v_mfma_f32_16x16x32_bf16 v[14:17], v[166:169], v[138:141], v[236:239]
	v_mfma_f32_16x16x32_bf16 v[6:9], v[220:223], v[138:141], v[134:137]
	v_mfma_f32_16x16x32_bf16 v[10:13], v[232:235], v[138:141], v[130:133]
	v_mfma_f32_16x16x32_bf16 v[2:5], v[146:149], v[138:141], v[2:5]
	s_waitcnt lgkmcnt(0)
	s_barrier
	s_and_saveexec_b64 s[2:3], s[0:1]
	s_cbranch_execz .LBB0_1467
	global_load_dword v130, v173, s[6:7] sc1
	s_waitcnt vmcnt(0)
	v_cmp_ne_u32_e32 vcc, 0, v130
	s_cbranch_vccnz .LBB0_1466
	s_mov_b32 s84, 1
	s_branch .LBB0_1451

.LBB0_1478:
	s_add_i32 s59, s34, 0xffff8000
	s_and_b32 s59, s59, 0x8000
	s_add_i32 s59, s59, 0
	s_add_i32 s41, s40, 0
	s_add_i32 s59, s59, 0x18000
	v_add_u32_e32 v236, s59, v184
	v_add_u32_e32 v237, s41, v187
	v_add_u32_e32 v242, s59, v181
	v_add_u32_e32 v244, s59, v172
	v_add_u32_e32 v240, s59, v183
	s_branch .Lrot_mh

.Lrot_mh:
	ds_read_b64_tr_b16 v[212:213], v236
	ds_read_b64_tr_b16 v[214:215], v236 offset:2048
	ds_read_b64_tr_b16 v[216:217], v240
	ds_read_b64_tr_b16 v[218:219], v240 offset:2048
	ds_read_b128 v[162:165], v237
	ds_read_b128 v[166:169], v237 offset:2048
	ds_read_b64_tr_b16 v[220:221], v242
	ds_read_b64_tr_b16 v[222:223], v242 offset:2048
	ds_read_b64_tr_b16 v[224:225], v244
	ds_read_b64_tr_b16 v[226:227], v244 offset:2048
	s_waitcnt lgkmcnt(5)
	v_mfma_f32_16x16x32_bf16 v[62:65], v[212:215], v[162:165], v[62:65]
	ds_read_b128 v[228:231], v237 offset:4096
	s_and_b32 s59, s34, 0x8000
	s_add_i32 s73, s33, s39
	v_mfma_f32_16x16x32_bf16 v[58:61], v[216:219], v[162:165], v[58:61]
	s_mov_b32 s74, m0
	s_mov_b32 m0, s73
	s_nop 0
	global_load_lds_dwordx4 v208, s[18:19]
	s_mov_b32 m0, s74
	s_waitcnt lgkmcnt(3)
	v_mfma_f32_16x16x32_bf16 v[54:57], v[220:223], v[162:165], v[54:57]
	s_waitcnt lgkmcnt(1)
	v_mfma_f32_16x16x32_bf16 v[42:45], v[224:227], v[162:165], v[42:45]
	v_mfma_f32_16x16x32_bf16 v[50:53], v[212:215], v[166:169], v[50:53]
	ds_read_b128 v[162:165], v237 offset:6144
	s_add_i32 s74, s73, 0x2000
	s_mov_b32 s75, m0
	s_mov_b32 m0, s74
	s_nop 0
	global_load_lds_dwordx4 v209, s[18:19]
	s_mov_b32 m0, s75
	v_mfma_f32_16x16x32_bf16 v[46:49], v[216:219], v[166:169], v[46:49]
	v_mfma_f32_16x16x32_bf16 v[38:41], v[220:223], v[166:169], v[38:41]
	v_mfma_f32_16x16x32_bf16 v[34:37], v[224:227], v[166:169], v[34:37]
	s_waitcnt lgkmcnt(1)
	v_mfma_f32_16x16x32_bf16 v[66:69], v[212:215], v[228:231], v[66:69]
	ds_read_b128 v[166:169], v237 offset:8192
	s_add_i32 s74, s73, 0x4000
	s_mov_b32 s75, m0
	s_mov_b32 m0, s74
	s_nop 0
	global_load_lds_dwordx4 v210, s[18:19]
	s_mov_b32 m0, s75
	v_mfma_f32_16x16x32_bf16 v[70:73], v[216:219], v[228:231], v[70:73]
	v_mfma_f32_16x16x32_bf16 v[74:77], v[220:223], v[228:231], v[74:77]
	v_mfma_f32_16x16x32_bf16 v[78:81], v[224:227], v[228:231], v[78:81]
	s_waitcnt lgkmcnt(1)
	v_mfma_f32_16x16x32_bf16 v[82:85], v[212:215], v[162:165], v[82:85]
	ds_read_b128 v[228:231], v237 offset:10240
	s_addk_i32 s73, 0x6000
	s_mov_b32 s74, m0
	s_mov_b32 m0, s73
	s_nop 0
	global_load_lds_dwordx4 v211, s[18:19]
	s_mov_b32 m0, s74
	v_mfma_f32_16x16x32_bf16 v[86:89], v[216:219], v[162:165], v[86:89]
	v_mfma_f32_16x16x32_bf16 v[90:93], v[220:223], v[162:165], v[90:93]
	v_mfma_f32_16x16x32_bf16 v[94:97], v[224:227], v[162:165], v[94:97]
	ds_read_b128 v[232:235], v237 offset:12288
	ds_read_b64_tr_b16 v[162:163], v236 offset:16384
	ds_read_b64_tr_b16 v[164:165], v236 offset:18432
	s_waitcnt lgkmcnt(4)
	v_mfma_f32_16x16x32_bf16 v[98:101], v[212:215], v[166:169], v[98:101]
	v_mfma_f32_16x16x32_bf16 v[102:105], v[216:219], v[166:169], v[102:105]
	v_mfma_f32_16x16x32_bf16 v[106:109], v[220:223], v[166:169], v[106:109]
	v_mfma_f32_16x16x32_bf16 v[110:113], v[224:227], v[166:169], v[110:113]
	ds_read_b128 v[236:239], v237 offset:14336
	ds_read_b64_tr_b16 v[166:167], v240 offset:16384
	ds_read_b64_tr_b16 v[168:169], v240 offset:18432
	s_waitcnt lgkmcnt(6)
	v_mfma_f32_16x16x32_bf16 v[114:117], v[212:215], v[228:231], v[114:117]
	v_mfma_f32_16x16x32_bf16 v[118:121], v[216:219], v[228:231], v[118:121]
	v_mfma_f32_16x16x32_bf16 v[122:125], v[220:223], v[228:231], v[122:125]
	v_mfma_f32_16x16x32_bf16 v[126:129], v[224:227], v[228:231], v[126:129]
	v_add_u32_e32 v245, s41, v188
	ds_read_b128 v[228:231], v245
	ds_read_b64_tr_b16 v[240:241], v242 offset:16384
	ds_read_b64_tr_b16 v[242:243], v242 offset:18432
	s_waitcnt lgkmcnt(8)
	v_mfma_f32_16x16x32_bf16 v[130:133], v[212:215], v[232:235], v[130:133]
	v_mfma_f32_16x16x32_bf16 v[134:137], v[216:219], v[232:235], v[134:137]
	v_mfma_f32_16x16x32_bf16 v[138:141], v[220:223], v[232:235], v[138:141]
	v_mfma_f32_16x16x32_bf16 v[142:145], v[224:227], v[232:235], v[142:145]
	s_waitcnt lgkmcnt(5)
	v_mfma_f32_16x16x32_bf16 v[146:149], v[212:215], v[236:239], v[146:149]
	v_mfma_f32_16x16x32_bf16 v[150:153], v[216:219], v[236:239], v[150:153]
	ds_read_b128 v[212:215], v245 offset:2048
	ds_read_b64_tr_b16 v[216:217], v244 offset:16384
	ds_read_b64_tr_b16 v[218:219], v244 offset:18432
	v_mfma_f32_16x16x32_bf16 v[154:157], v[220:223], v[236:239], v[154:157]
	v_mfma_f32_16x16x32_bf16 v[158:161], v[224:227], v[236:239], v[158:161]
	ds_read_b128 v[220:223], v245 offset:4096
	s_waitcnt lgkmcnt(6)
	v_mfma_f32_16x16x32_bf16 v[62:65], v[162:165], v[228:231], v[62:65]
	s_add_u32 s41, s37, s2
	s_waitcnt vmcnt(11)
	v_add_u32_e32 v232, s59, v189
	v_mfma_f32_16x16x32_bf16 v[58:61], v[166:169], v[228:231], v[58:61]
	s_addc_u32 s59, s38, s3
	v_cvt_pk_bf16_f32 v30, v30, v31
	v_cvt_pk_bf16_f32 v31, v32, v33
	s_waitcnt lgkmcnt(4)
	v_mfma_f32_16x16x32_bf16 v[54:57], v[240:243], v[228:231], v[54:57]
	s_add_u32 s74, s41, 0x160000
	ds_write_b64 v232, v[30:31]
	s_addc_u32 s75, s59, 0
	s_waitcnt lgkmcnt(2)
	v_mfma_f32_16x16x32_bf16 v[42:45], v[216:219], v[228:231], v[42:45]
	global_load_dwordx4 v[30:33], v199, s[74:75]
	v_mfma_f32_16x16x32_bf16 v[50:53], v[162:165], v[212:215], v[50:53]
	ds_read_b128 v[224:227], v245 offset:6144
	s_waitcnt vmcnt(11)
	s_add_u32 s74, s41, 0x18c000
	v_mfma_f32_16x16x32_bf16 v[46:49], v[166:169], v[212:215], v[46:49]
	v_cvt_pk_bf16_f32 v26, v26, v27
	v_cvt_pk_bf16_f32 v27, v28, v29
	ds_write_b64 v232, v[26:27] offset:8192
	v_mfma_f32_16x16x32_bf16 v[38:41], v[240:243], v[212:215], v[38:41]
	s_addc_u32 s75, s59, 0
	global_load_dwordx4 v[26:29], v199, s[74:75]
	v_mfma_f32_16x16x32_bf16 v[34:37], v[216:219], v[212:215], v[34:37]
	s_waitcnt lgkmcnt(3)
	v_mfma_f32_16x16x32_bf16 v[66:69], v[162:165], v[220:223], v[66:69]
	ds_read_b128 v[212:215], v245 offset:8192
	s_waitcnt vmcnt(11)
	s_add_u32 s74, s41, 0x1b8000
	v_mfma_f32_16x16x32_bf16 v[70:73], v[166:169], v[220:223], v[70:73]
	v_cvt_pk_bf16_f32 v22, v22, v23
	v_cvt_pk_bf16_f32 v23, v24, v25
	ds_write_b64 v232, v[22:23] offset:16384
	v_mfma_f32_16x16x32_bf16 v[74:77], v[240:243], v[220:223], v[74:77]
	s_addc_u32 s75, s59, 0
	global_load_dwordx4 v[22:25], v199, s[74:75]
	v_mfma_f32_16x16x32_bf16 v[78:81], v[216:219], v[220:223], v[78:81]
	s_waitcnt lgkmcnt(3)
	v_mfma_f32_16x16x32_bf16 v[82:85], v[162:165], v[224:227], v[82:85]
	ds_read_b128 v[220:223], v245 offset:10240
	s_waitcnt vmcnt(11)
	s_add_u32 s74, s41, 0x1e4000
	v_mfma_f32_16x16x32_bf16 v[86:89], v[166:169], v[224:227], v[86:89]
	v_cvt_pk_bf16_f32 v18, v18, v19
	v_cvt_pk_bf16_f32 v19, v20, v21
	ds_write_b64 v232, v[18:19] offset:24576
	v_mfma_f32_16x16x32_bf16 v[90:93], v[240:243], v[224:227], v[90:93]
	s_addc_u32 s75, s59, 0
	global_load_dwordx4 v[18:21], v199, s[74:75]
	v_mfma_f32_16x16x32_bf16 v[94:97], v[216:219], v[224:227], v[94:97]
	ds_read_b128 v[224:227], v245 offset:12288
	s_waitcnt lgkmcnt(4)
	v_mfma_f32_16x16x32_bf16 v[98:101], v[162:165], v[212:215], v[98:101]
	s_add_u32 s41, s35, s2
	s_waitcnt vmcnt(11)
	s_addc_u32 s59, s36, s3
	v_mfma_f32_16x16x32_bf16 v[102:105], v[166:169], v[212:215], v[102:105]
	v_cvt_pk_bf16_f32 v14, v14, v15
	v_cvt_pk_bf16_f32 v15, v16, v17
	s_add_u32 s74, s41, 0x160000
	v_mfma_f32_16x16x32_bf16 v[106:109], v[240:243], v[212:215], v[106:109]
	ds_write_b64 v232, v[14:15] offset:256
	s_addc_u32 s75, s59, 0
	global_load_dwordx4 v[14:17], v199, s[74:75]
	v_mfma_f32_16x16x32_bf16 v[110:113], v[216:219], v[212:215], v[110:113]
	s_waitcnt lgkmcnt(3)
	v_mfma_f32_16x16x32_bf16 v[114:117], v[162:165], v[220:223], v[114:117]
	ds_read_b128 v[212:215], v245 offset:14336
	s_waitcnt vmcnt(11)
	s_add_u32 s74, s41, 0x18c000
	v_mfma_f32_16x16x32_bf16 v[118:121], v[166:169], v[220:223], v[118:121]
	v_cvt_pk_bf16_f32 v10, v10, v11
	v_cvt_pk_bf16_f32 v11, v12, v13
	ds_write_b64 v232, v[10:11] offset:8448
	v_mfma_f32_16x16x32_bf16 v[122:125], v[240:243], v[220:223], v[122:125]
	s_addc_u32 s75, s59, 0
	global_load_dwordx4 v[10:13], v199, s[74:75]
	v_mfma_f32_16x16x32_bf16 v[126:129], v[216:219], v[220:223], v[126:129]
	s_waitcnt lgkmcnt(3)
	v_mfma_f32_16x16x32_bf16 v[130:133], v[162:165], v[224:227], v[130:133]
	s_waitcnt vmcnt(11)
	s_add_u32 s74, s41, 0x1b8000
	v_cvt_pk_bf16_f32 v6, v6, v7
	v_mfma_f32_16x16x32_bf16 v[134:137], v[166:169], v[224:227], v[134:137]
	v_cvt_pk_bf16_f32 v7, v8, v9
	ds_write_b64 v232, v[6:7] offset:16640
	s_addc_u32 s75, s59, 0
	v_mfma_f32_16x16x32_bf16 v[138:141], v[240:243], v[224:227], v[138:141]
	global_load_dwordx4 v[6:9], v199, s[74:75]
	v_mfma_f32_16x16x32_bf16 v[142:145], v[216:219], v[224:227], v[142:145]
	s_waitcnt lgkmcnt(2)
	v_mfma_f32_16x16x32_bf16 v[146:149], v[162:165], v[212:215], v[146:149]
	s_waitcnt vmcnt(11)
	s_add_u32 s74, s41, 0x1e4000
	v_cvt_pk_bf16_f32 v2, v2, v3
	v_mfma_f32_16x16x32_bf16 v[150:153], v[166:169], v[212:215], v[150:153]
	v_cvt_pk_bf16_f32 v3, v4, v5
	ds_write_b64 v232, v[2:3] offset:24832
	s_addc_u32 s75, s59, 0
	v_mfma_f32_16x16x32_bf16 v[154:157], v[240:243], v[212:215], v[154:157]
	global_load_dwordx4 v[2:5], v199, s[74:75]
	v_mfma_f32_16x16x32_bf16 v[158:161], v[216:219], v[212:215], v[158:161]
	s_add_i32 s41, s40, 0x8000
	s_cmp_lg_u32 s40, 0x10000
	s_cselect_b32 s40, s41, 0
	s_add_i32 s41, s39, 0x8000
	s_cmp_lg_u32 s39, 0x10000
	s_cselect_b32 s39, s41, 0
	s_add_u32 s2, s2, 0xb0000
	s_addc_u32 s3, s3, 0
	s_add_i32 s34, s34, 0x8000
	v_add_u32_e32 v211, 0x80, v211
	v_add_u32_e32 v210, 0x80, v210
	v_add_u32_e32 v209, 0x80, v209
	v_add_u32_e32 v208, 0x80, v208
	s_add_i32 s59, s34, 0xffff8000
	s_and_b32 s59, s59, 0x8000
	s_add_i32 s59, s59, 0
	s_add_i32 s41, s40, 0
	s_add_i32 s59, s59, 0x18000
	v_add_u32_e32 v236, s59, v184
	v_add_u32_e32 v237, s41, v187
	v_add_u32_e32 v242, s59, v181
	v_add_u32_e32 v244, s59, v172
	v_add_u32_e32 v240, s59, v183
	s_waitcnt lgkmcnt(0)
	s_cmp_lg_u32 s2, 0x840000
	s_cbranch_scc1 .Lrot_mh_head
	s_barrier
	v_add_u32_e32 v189, s52, v184
	v_add_u32_e32 v187, 0, v187
	v_add_u32_e32 v238, s52, v181
	v_add_u32_e32 v240, s52, v172
	v_add_u32_e32 v234, s52, v183
	ds_read_b64_tr_b16 v[162:163], v189
	ds_read_b64_tr_b16 v[164:165], v189 offset:2048
	ds_read_b64_tr_b16 v[166:167], v234
	ds_read_b64_tr_b16 v[168:169], v234 offset:2048
	ds_read_b128 v[208:211], v187
	ds_read_b128 v[212:215], v187 offset:2048
	ds_read_b64_tr_b16 v[216:217], v238
	ds_read_b64_tr_b16 v[218:219], v238 offset:2048
	ds_read_b64_tr_b16 v[220:221], v240
	ds_read_b64_tr_b16 v[222:223], v240 offset:2048
	ds_read_b128 v[224:227], v187 offset:4096
	s_waitcnt lgkmcnt(6)
	v_mfma_f32_16x16x32_bf16 v[62:65], v[162:165], v[208:211], v[62:65]
	v_mfma_f32_16x16x32_bf16 v[58:61], v[166:169], v[208:211], v[58:61]
	s_waitcnt lgkmcnt(3)
	v_mfma_f32_16x16x32_bf16 v[54:57], v[216:219], v[208:211], v[54:57]
	s_waitcnt lgkmcnt(1)
	v_mfma_f32_16x16x32_bf16 v[42:45], v[220:223], v[208:211], v[42:45]
	ds_read_b128 v[208:211], v187 offset:6144
	v_mfma_f32_16x16x32_bf16 v[50:53], v[162:165], v[212:215], v[50:53]
	v_mfma_f32_16x16x32_bf16 v[46:49], v[166:169], v[212:215], v[46:49]
	v_mfma_f32_16x16x32_bf16 v[38:41], v[216:219], v[212:215], v[38:41]
	v_mfma_f32_16x16x32_bf16 v[34:37], v[220:223], v[212:215], v[34:37]
	ds_read_b128 v[212:215], v187 offset:8192
	s_waitcnt lgkmcnt(2)
	v_mfma_f32_16x16x32_bf16 v[66:69], v[162:165], v[224:227], v[66:69]
	v_mfma_f32_16x16x32_bf16 v[70:73], v[166:169], v[224:227], v[70:73]
	v_mfma_f32_16x16x32_bf16 v[74:77], v[216:219], v[224:227], v[74:77]
	v_mfma_f32_16x16x32_bf16 v[78:81], v[220:223], v[224:227], v[78:81]
	ds_read_b128 v[224:227], v187 offset:10240
	s_waitcnt lgkmcnt(2)
	v_mfma_f32_16x16x32_bf16 v[82:85], v[162:165], v[208:211], v[82:85]
	v_mfma_f32_16x16x32_bf16 v[86:89], v[166:169], v[208:211], v[86:89]
	v_mfma_f32_16x16x32_bf16 v[90:93], v[216:219], v[208:211], v[90:93]
	v_mfma_f32_16x16x32_bf16 v[94:97], v[220:223], v[208:211], v[94:97]
	ds_read_b128 v[208:211], v187 offset:12288
	ds_read_b64_tr_b16 v[228:229], v189 offset:16384
	ds_read_b64_tr_b16 v[230:231], v189 offset:18432
	s_waitcnt lgkmcnt(4)
	v_mfma_f32_16x16x32_bf16 v[98:101], v[162:165], v[212:215], v[98:101]
	v_mfma_f32_16x16x32_bf16 v[102:105], v[166:169], v[212:215], v[102:105]
	v_mfma_f32_16x16x32_bf16 v[106:109], v[216:219], v[212:215], v[106:109]
	v_mfma_f32_16x16x32_bf16 v[110:113], v[220:223], v[212:215], v[110:113]
	ds_read_b128 v[212:215], v187 offset:14336
	ds_read_b64_tr_b16 v[232:233], v234 offset:16384
	ds_read_b64_tr_b16 v[234:235], v234 offset:18432
	s_waitcnt lgkmcnt(6)
	v_mfma_f32_16x16x32_bf16 v[114:117], v[162:165], v[224:227], v[114:117]
	v_mfma_f32_16x16x32_bf16 v[118:121], v[166:169], v[224:227], v[118:121]
	v_mfma_f32_16x16x32_bf16 v[122:125], v[216:219], v[224:227], v[122:125]
	v_mfma_f32_16x16x32_bf16 v[126:129], v[220:223], v[224:227], v[126:129]
	v_add_u32_e32 v188, 0, v188
	ds_read_b128 v[224:227], v188
	ds_read_b64_tr_b16 v[236:237], v238 offset:16384
	ds_read_b64_tr_b16 v[238:239], v238 offset:18432
	s_waitcnt lgkmcnt(8)
	v_mfma_f32_16x16x32_bf16 v[130:133], v[162:165], v[208:211], v[130:133]
	v_mfma_f32_16x16x32_bf16 v[134:137], v[166:169], v[208:211], v[134:137]
	v_mfma_f32_16x16x32_bf16 v[138:141], v[216:219], v[208:211], v[138:141]
	v_mfma_f32_16x16x32_bf16 v[142:145], v[220:223], v[208:211], v[142:145]
	s_waitcnt lgkmcnt(5)
	v_mfma_f32_16x16x32_bf16 v[146:149], v[162:165], v[212:215], v[146:149]
	v_mfma_f32_16x16x32_bf16 v[150:153], v[166:169], v[212:215], v[150:153]
	ds_read_b128 v[162:165], v188 offset:2048
	ds_read_b64_tr_b16 v[166:167], v240 offset:16384
	ds_read_b64_tr_b16 v[168:169], v240 offset:18432
	v_mfma_f32_16x16x32_bf16 v[154:157], v[216:219], v[212:215], v[154:157]
	v_mfma_f32_16x16x32_bf16 v[158:161], v[220:223], v[212:215], v[158:161]
	ds_read_b128 v[208:211], v188 offset:4096
	s_waitcnt vmcnt(7)
	v_add_u32_e32 v186, s56, v186
	v_cvt_pk_bf16_f32 v30, v30, v31
	v_cvt_pk_bf16_f32 v31, v32, v33
	s_waitcnt lgkmcnt(6)
	v_mfma_f32_16x16x32_bf16 v[62:65], v[228:231], v[224:227], v[62:65]
	ds_write_b64 v186, v[30:31]
	v_mfma_f32_16x16x32_bf16 v[58:61], v[232:235], v[224:227], v[58:61]
	s_waitcnt lgkmcnt(5)
	v_mfma_f32_16x16x32_bf16 v[54:57], v[236:239], v[224:227], v[54:57]
	s_waitcnt lgkmcnt(2)
	v_mfma_f32_16x16x32_bf16 v[30:33], v[166:169], v[224:227], v[42:45]
	v_mfma_f32_16x16x32_bf16 v[42:45], v[228:231], v[162:165], v[50:53]
	s_nop 2
	ds_read_b128 v[50:53], v188 offset:6144
	s_waitcnt vmcnt(6)
	v_mfma_f32_16x16x32_bf16 v[46:49], v[232:235], v[162:165], v[46:49]
	v_cvt_pk_bf16_f32 v26, v26, v27
	v_cvt_pk_bf16_f32 v27, v28, v29
	ds_write_b64 v186, v[26:27] offset:8192
	v_mfma_f32_16x16x32_bf16 v[38:41], v[236:239], v[162:165], v[38:41]
	v_mfma_f32_16x16x32_bf16 v[26:29], v[166:169], v[162:165], v[34:37]
	s_waitcnt lgkmcnt(3)
	v_mfma_f32_16x16x32_bf16 v[34:37], v[228:231], v[208:211], v[66:69]
	v_mfma_f32_16x16x32_bf16 v[66:69], v[232:235], v[208:211], v[70:73]
	s_nop 2
	ds_read_b128 v[70:73], v188 offset:8192
	s_waitcnt vmcnt(5)
	v_mfma_f32_16x16x32_bf16 v[74:77], v[236:239], v[208:211], v[74:77]
	v_cvt_pk_bf16_f32 v22, v22, v23
	v_cvt_pk_bf16_f32 v23, v24, v25
	ds_write_b64 v186, v[22:23] offset:16384
	v_mfma_f32_16x16x32_bf16 v[22:25], v[166:169], v[208:211], v[78:81]
	s_waitcnt lgkmcnt(3)
	v_mfma_f32_16x16x32_bf16 v[78:81], v[228:231], v[50:53], v[82:85]
	v_mfma_f32_16x16x32_bf16 v[82:85], v[232:235], v[50:53], v[86:89]
	s_nop 2
	ds_read_b128 v[86:89], v188 offset:10240
	s_waitcnt vmcnt(4)
	v_mfma_f32_16x16x32_bf16 v[90:93], v[236:239], v[50:53], v[90:93]
	v_cvt_pk_bf16_f32 v18, v18, v19
	v_cvt_pk_bf16_f32 v19, v20, v21
	ds_write_b64 v186, v[18:19] offset:24576
	v_mfma_f32_16x16x32_bf16 v[18:21], v[166:169], v[50:53], v[94:97]
	s_waitcnt lgkmcnt(3)
	v_mfma_f32_16x16x32_bf16 v[50:53], v[228:231], v[70:73], v[98:101]
	v_add_u32_e32 v162, s56, v185
	s_nop 1
	ds_read_b128 v[98:101], v188 offset:12288
	s_waitcnt vmcnt(3)
	v_mfma_f32_16x16x32_bf16 v[94:97], v[232:235], v[70:73], v[102:105]
	v_cvt_pk_bf16_f32 v14, v14, v15
	v_cvt_pk_bf16_f32 v15, v16, v17
	ds_write_b64 v162, v[14:15]
	v_mfma_f32_16x16x32_bf16 v[102:105], v[236:239], v[70:73], v[106:109]
	v_mfma_f32_16x16x32_bf16 v[14:17], v[166:169], v[70:73], v[110:113]
	s_nop 2
	ds_read_b128 v[110:113], v188 offset:14336
	s_waitcnt vmcnt(2)
	s_waitcnt lgkmcnt(4)
	v_mfma_f32_16x16x32_bf16 v[70:73], v[228:231], v[86:89], v[114:117]
	v_cvt_pk_bf16_f32 v10, v10, v11
	v_cvt_pk_bf16_f32 v11, v12, v13
	ds_write_b64 v162, v[10:11] offset:8192
	v_mfma_f32_16x16x32_bf16 v[106:109], v[232:235], v[86:89], v[118:121]
	v_mfma_f32_16x16x32_bf16 v[114:117], v[236:239], v[86:89], v[122:125]
	v_mfma_f32_16x16x32_bf16 v[10:13], v[166:169], v[86:89], v[126:129]
	s_waitcnt vmcnt(1)
	s_waitcnt lgkmcnt(3)
	v_mfma_f32_16x16x32_bf16 v[86:89], v[228:231], v[98:101], v[130:133]
	v_cvt_pk_bf16_f32 v6, v6, v7
	v_cvt_pk_bf16_f32 v7, v8, v9
	ds_write_b64 v162, v[6:7] offset:16384
	v_mfma_f32_16x16x32_bf16 v[118:121], v[232:235], v[98:101], v[134:137]
	v_mfma_f32_16x16x32_bf16 v[122:125], v[236:239], v[98:101], v[138:141]
	v_mfma_f32_16x16x32_bf16 v[6:9], v[166:169], v[98:101], v[142:145]
	s_waitcnt vmcnt(0)
	s_waitcnt lgkmcnt(2)
	v_mfma_f32_16x16x32_bf16 v[98:101], v[228:231], v[110:113], v[146:149]
	v_cvt_pk_bf16_f32 v2, v2, v3
	v_cvt_pk_bf16_f32 v3, v4, v5
	ds_write_b64 v162, v[2:3] offset:24576
	v_mfma_f32_16x16x32_bf16 v[126:129], v[232:235], v[110:113], v[150:153]
	v_mfma_f32_16x16x32_bf16 v[130:133], v[236:239], v[110:113], v[154:157]
	v_mfma_f32_16x16x32_bf16 v[2:5], v[166:169], v[110:113], v[158:161]
	s_waitcnt lgkmcnt(0)
	s_barrier
	s_nop 1
	v_add_u32_e32 v160, s56, v184
	v_add_u32_e32 v164, s56, v183
	v_add_u32_e32 v168, s56, v181
	ds_read_b64_tr_b16 v[110:111], v160
	ds_read_b64_tr_b16 v[112:113], v160 offset:2048
	ds_read_b64_tr_b16 v[134:135], v164
	ds_read_b64_tr_b16 v[136:137], v164 offset:2048
	ds_read_b128 v[138:141], v187 offset:32768
	ds_read_b64_tr_b16 v[142:143], v168
	ds_read_b128 v[146:149], v187 offset:34816
	ds_read_b128 v[150:153], v187 offset:36864
	ds_read_b64_tr_b16 v[144:145], v168 offset:2048
	v_add_u32_e32 v172, s56, v172
	ds_read_b64_tr_b16 v[154:155], v172
	ds_read_b64_tr_b16 v[156:157], v172 offset:2048
	s_waitcnt lgkmcnt(6)
	v_mfma_f32_16x16x32_bf16 v[62:65], v[110:113], v[138:141], v[62:65]
	v_mfma_f32_16x16x32_bf16 v[58:61], v[134:137], v[138:141], v[58:61]
	s_waitcnt lgkmcnt(2)
	v_mfma_f32_16x16x32_bf16 v[54:57], v[142:145], v[138:141], v[54:57]
	s_waitcnt lgkmcnt(0)
	v_mfma_f32_16x16x32_bf16 v[30:33], v[154:157], v[138:141], v[30:33]
	ds_read_b128 v[138:141], v187 offset:38912
	v_mfma_f32_16x16x32_bf16 v[42:45], v[110:113], v[146:149], v[42:45]
	v_mfma_f32_16x16x32_bf16 v[46:49], v[134:137], v[146:149], v[46:49]
	v_mfma_f32_16x16x32_bf16 v[38:41], v[142:145], v[146:149], v[38:41]
	v_mfma_f32_16x16x32_bf16 v[26:29], v[154:157], v[146:149], v[26:29]
	ds_read_b128 v[146:149], v187 offset:40960
	v_mfma_f32_16x16x32_bf16 v[34:37], v[110:113], v[150:153], v[34:37]
	v_mfma_f32_16x16x32_bf16 v[66:69], v[134:137], v[150:153], v[66:69]
	v_mfma_f32_16x16x32_bf16 v[74:77], v[142:145], v[150:153], v[74:77]
	v_mfma_f32_16x16x32_bf16 v[22:25], v[154:157], v[150:153], v[22:25]
	ds_read_b128 v[150:153], v187 offset:43008
	s_waitcnt lgkmcnt(2)
	v_mfma_f32_16x16x32_bf16 v[78:81], v[110:113], v[138:141], v[78:81]
	v_mfma_f32_16x16x32_bf16 v[82:85], v[134:137], v[138:141], v[82:85]
	v_mfma_f32_16x16x32_bf16 v[90:93], v[142:145], v[138:141], v[90:93]
	v_mfma_f32_16x16x32_bf16 v[18:21], v[154:157], v[138:141], v[18:21]
	ds_read_b128 v[138:141], v187 offset:45056
	ds_read_b64_tr_b16 v[158:159], v160 offset:16384
	ds_read_b64_tr_b16 v[160:161], v160 offset:18432
	s_waitcnt lgkmcnt(4)
	v_mfma_f32_16x16x32_bf16 v[50:53], v[110:113], v[146:149], v[50:53]
	v_mfma_f32_16x16x32_bf16 v[94:97], v[134:137], v[146:149], v[94:97]
	v_mfma_f32_16x16x32_bf16 v[102:105], v[142:145], v[146:149], v[102:105]
	v_mfma_f32_16x16x32_bf16 v[14:17], v[154:157], v[146:149], v[14:17]
	ds_read_b128 v[146:149], v187 offset:47104
	ds_read_b64_tr_b16 v[162:163], v164 offset:16384
	ds_read_b64_tr_b16 v[164:165], v164 offset:18432
	s_waitcnt lgkmcnt(6)
	v_mfma_f32_16x16x32_bf16 v[70:73], v[110:113], v[150:153], v[70:73]
	v_mfma_f32_16x16x32_bf16 v[106:109], v[134:137], v[150:153], v[106:109]
	v_mfma_f32_16x16x32_bf16 v[114:117], v[142:145], v[150:153], v[114:117]
	v_mfma_f32_16x16x32_bf16 v[10:13], v[154:157], v[150:153], v[10:13]
	ds_read_b128 v[150:153], v188 offset:32768
	ds_read_b64_tr_b16 v[166:167], v168 offset:16384
	ds_read_b64_tr_b16 v[168:169], v168 offset:18432
	s_waitcnt lgkmcnt(8)
	v_mfma_f32_16x16x32_bf16 v[86:89], v[110:113], v[138:141], v[86:89]
	v_mfma_f32_16x16x32_bf16 v[118:121], v[134:137], v[138:141], v[118:121]
	v_mfma_f32_16x16x32_bf16 v[122:125], v[142:145], v[138:141], v[122:125]
	v_mfma_f32_16x16x32_bf16 v[6:9], v[154:157], v[138:141], v[6:9]
	s_waitcnt lgkmcnt(5)
	v_mfma_f32_16x16x32_bf16 v[98:101], v[110:113], v[146:149], v[98:101]
	v_mfma_f32_16x16x32_bf16 v[110:113], v[134:137], v[146:149], v[126:129]
	v_mfma_f32_16x16x32_bf16 v[126:129], v[142:145], v[146:149], v[130:133]
	s_nop 2
	ds_read_b128 v[130:133], v188 offset:34816
	ds_read_b64_tr_b16 v[134:135], v172 offset:16384
	ds_read_b64_tr_b16 v[136:137], v172 offset:18432
	v_mfma_f32_16x16x32_bf16 v[2:5], v[154:157], v[146:149], v[2:5]
	ds_read_b128 v[138:141], v188 offset:36864
	s_waitcnt lgkmcnt(6)
	v_mfma_f32_16x16x32_bf16 v[62:65], v[158:161], v[150:153], v[62:65]
	v_mfma_f32_16x16x32_bf16 v[58:61], v[162:165], v[150:153], v[58:61]
	s_waitcnt lgkmcnt(4)
	v_mfma_f32_16x16x32_bf16 v[54:57], v[166:169], v[150:153], v[54:57]
	s_waitcnt lgkmcnt(1)
	v_mfma_f32_16x16x32_bf16 v[30:33], v[134:137], v[150:153], v[30:33]
	ds_read_b128 v[142:145], v188 offset:38912
	v_mfma_f32_16x16x32_bf16 v[42:45], v[158:161], v[130:133], v[42:45]
	v_mfma_f32_16x16x32_bf16 v[46:49], v[162:165], v[130:133], v[46:49]
	v_mfma_f32_16x16x32_bf16 v[38:41], v[166:169], v[130:133], v[38:41]
	v_mfma_f32_16x16x32_bf16 v[26:29], v[134:137], v[130:133], v[26:29]
	ds_read_b128 v[130:133], v188 offset:40960
	s_waitcnt lgkmcnt(2)
	v_mfma_f32_16x16x32_bf16 v[34:37], v[158:161], v[138:141], v[34:37]
	v_mfma_f32_16x16x32_bf16 v[66:69], v[162:165], v[138:141], v[66:69]
	v_mfma_f32_16x16x32_bf16 v[74:77], v[166:169], v[138:141], v[74:77]
	v_mfma_f32_16x16x32_bf16 v[22:25], v[134:137], v[138:141], v[22:25]
	ds_read_b128 v[138:141], v188 offset:43008
	s_waitcnt lgkmcnt(2)
	v_mfma_f32_16x16x32_bf16 v[78:81], v[158:161], v[142:145], v[78:81]
	v_mfma_f32_16x16x32_bf16 v[82:85], v[162:165], v[142:145], v[82:85]
	v_mfma_f32_16x16x32_bf16 v[90:93], v[166:169], v[142:145], v[90:93]
	v_mfma_f32_16x16x32_bf16 v[18:21], v[134:137], v[142:145], v[18:21]
	ds_read_b128 v[142:145], v188 offset:45056
	s_waitcnt lgkmcnt(2)
	v_mfma_f32_16x16x32_bf16 v[50:53], v[158:161], v[130:133], v[50:53]
	v_mfma_f32_16x16x32_bf16 v[94:97], v[162:165], v[130:133], v[94:97]
	v_mfma_f32_16x16x32_bf16 v[102:105], v[166:169], v[130:133], v[102:105]
	v_mfma_f32_16x16x32_bf16 v[14:17], v[134:137], v[130:133], v[14:17]
	ds_read_b128 v[130:133], v188 offset:47104
	s_waitcnt lgkmcnt(2)
	v_mfma_f32_16x16x32_bf16 v[70:73], v[158:161], v[138:141], v[70:73]
	v_mfma_f32_16x16x32_bf16 v[106:109], v[162:165], v[138:141], v[106:109]
	v_mfma_f32_16x16x32_bf16 v[114:117], v[166:169], v[138:141], v[114:117]
	v_mfma_f32_16x16x32_bf16 v[10:13], v[134:137], v[138:141], v[10:13]
	s_waitcnt lgkmcnt(1)
	v_mfma_f32_16x16x32_bf16 v[86:89], v[158:161], v[142:145], v[86:89]
	v_mfma_f32_16x16x32_bf16 v[118:121], v[162:165], v[142:145], v[118:121]
	v_mfma_f32_16x16x32_bf16 v[122:125], v[166:169], v[142:145], v[122:125]
	v_mfma_f32_16x16x32_bf16 v[138:141], v[134:137], v[142:145], v[6:9]
	s_waitcnt lgkmcnt(0)
	v_mfma_f32_16x16x32_bf16 v[98:101], v[158:161], v[130:133], v[98:101]
	v_mfma_f32_16x16x32_bf16 v[6:9], v[162:165], v[130:133], v[110:113]
	v_mfma_f32_16x16x32_bf16 v[110:113], v[166:169], v[130:133], v[126:129]
	v_mfma_f32_16x16x32_bf16 v[2:5], v[134:137], v[130:133], v[2:5]
	s_nop 1
	v_mov_b32_e32 v126, v192
	v_mov_b32_e32 v127, v1
	s_waitcnt lgkmcnt(0)
	s_barrier
	s_add_i32 s5, s5, s29
	s_lshl_b32 s2, s4, 5
	v_add_u32_e32 v127, s5, v127
	s_or_b32 s2, s2, s28
	v_lshl_add_u32 v132, v126, 2, s2
	v_lshlrev_b32_e32 v126, 8, v127
	v_and_b32_e32 v172, 0xff00, v126
	v_and_b32_e32 v128, 0x7c, v132
	v_lshlrev_b32_e32 v133, 7, v127
	v_lshl_add_u64 v[126:127], s[30:31], 0, v[172:173]
	v_lshlrev_b32_e32 v172, 1, v128
	v_lshl_add_u64 v[128:129], v[126:127], 0, v[172:173]
	v_cvt_pk_bf16_f32 v62, v62, v63
	v_cvt_pk_bf16_f32 v63, v64, v65
	v_cvt_pk_bf16_f32 v54, v54, v55
	global_store_dwordx2 v[128:129], v[62:63], off sc1
	s_nop 1
	v_lshl_add_u64 v[130:131], v[128:129], 0, s[22:23]
	v_cvt_pk_bf16_f32 v55, v56, v57
	global_store_dwordx2 v[130:131], v[54:55], off sc1
	s_nop 1
	v_add_u32_e32 v54, 16, v132
	v_and_b32_e32 v54, 0x7c, v54
	v_lshlrev_b32_e32 v54, 1, v54
	v_mov_b32_e32 v55, v173
	v_lshl_add_u64 v[56:57], v[126:127], 0, v[54:55]
	v_cvt_pk_bf16_f32 v58, v58, v59
	v_cvt_pk_bf16_f32 v59, v60, v61
	v_cvt_pk_bf16_f32 v30, v30, v31
	global_store_dwordx2 v[56:57], v[58:59], off sc1
	s_nop 1
	v_lshl_add_u64 v[62:63], v[56:57], 0, s[22:23]
	v_cvt_pk_bf16_f32 v31, v32, v33
	global_store_dwordx2 v[62:63], v[30:31], off sc1
	s_nop 1
	v_add_u32_e32 v30, 0x800, v133
	v_and_b32_e32 v30, 0x7f80, v30
	v_lshlrev_b32_e32 v30, 1, v30
	v_mov_b32_e32 v31, v173
	v_lshl_add_u64 v[30:31], s[30:31], 0, v[30:31]
	v_lshl_add_u64 v[32:33], v[30:31], 0, v[172:173]
	v_cvt_pk_bf16_f32 v42, v42, v43
	v_cvt_pk_bf16_f32 v43, v44, v45
	global_store_dwordx2 v[32:33], v[42:43], off sc1
	s_nop 1
	v_lshl_add_u64 v[56:57], v[32:33], 0, s[22:23]
	v_cvt_pk_bf16_f32 v38, v38, v39
	v_cvt_pk_bf16_f32 v39, v40, v41
	global_store_dwordx2 v[56:57], v[38:39], off sc1
	s_nop 1
	v_lshl_add_u64 v[30:31], v[30:31], 0, v[54:55]
	v_cvt_pk_bf16_f32 v38, v46, v47
	v_cvt_pk_bf16_f32 v39, v48, v49
	v_cvt_pk_bf16_f32 v26, v26, v27
	global_store_dwordx2 v[30:31], v[38:39], off sc1
	s_nop 1
	v_lshl_add_u64 v[32:33], v[30:31], 0, s[22:23]
	v_cvt_pk_bf16_f32 v27, v28, v29
	global_store_dwordx2 v[32:33], v[26:27], off sc1
	s_nop 1
	v_add_u32_e32 v26, 0x1000, v133
	v_and_b32_e32 v26, 0x7f80, v26
	v_lshlrev_b32_e32 v26, 1, v26
	v_mov_b32_e32 v27, v173
	v_lshl_add_u64 v[26:27], s[30:31], 0, v[26:27]
	v_lshl_add_u64 v[28:29], v[26:27], 0, v[172:173]
	v_cvt_pk_bf16_f32 v32, v34, v35
	v_cvt_pk_bf16_f32 v33, v36, v37
	global_store_dwordx2 v[28:29], v[32:33], off sc1
	s_nop 1
	v_lshl_add_u64 v[30:31], v[28:29], 0, s[22:23]
	v_cvt_pk_bf16_f32 v34, v74, v75
	v_cvt_pk_bf16_f32 v35, v76, v77
	global_store_dwordx2 v[30:31], v[34:35], off sc1
	s_nop 1
	v_lshl_add_u64 v[26:27], v[26:27], 0, v[54:55]
	v_cvt_pk_bf16_f32 v30, v66, v67
	v_cvt_pk_bf16_f32 v31, v68, v69
	v_cvt_pk_bf16_f32 v22, v22, v23
	global_store_dwordx2 v[26:27], v[30:31], off sc1
	s_nop 1
	v_lshl_add_u64 v[28:29], v[26:27], 0, s[22:23]
	v_cvt_pk_bf16_f32 v23, v24, v25
	global_store_dwordx2 v[28:29], v[22:23], off sc1
	s_nop 1
	v_add_u32_e32 v22, 0x1800, v133
	v_and_b32_e32 v22, 0x7f80, v22
	v_lshlrev_b32_e32 v22, 1, v22
	v_mov_b32_e32 v23, v173
	v_lshl_add_u64 v[22:23], s[30:31], 0, v[22:23]
	v_lshl_add_u64 v[24:25], v[22:23], 0, v[172:173]
	v_cvt_pk_bf16_f32 v28, v78, v79
	v_cvt_pk_bf16_f32 v29, v80, v81
	global_store_dwordx2 v[24:25], v[28:29], off sc1
	s_nop 1
	v_lshl_add_u64 v[26:27], v[24:25], 0, s[22:23]
	v_cvt_pk_bf16_f32 v30, v90, v91
	v_cvt_pk_bf16_f32 v31, v92, v93
	global_store_dwordx2 v[26:27], v[30:31], off sc1
	s_nop 1
	v_lshl_add_u64 v[22:23], v[22:23], 0, v[54:55]
	v_cvt_pk_bf16_f32 v26, v82, v83
	v_cvt_pk_bf16_f32 v27, v84, v85
	v_cvt_pk_bf16_f32 v18, v18, v19
	global_store_dwordx2 v[22:23], v[26:27], off sc1
	s_nop 1
	v_lshl_add_u64 v[24:25], v[22:23], 0, s[22:23]
	v_cvt_pk_bf16_f32 v19, v20, v21
	global_store_dwordx2 v[24:25], v[18:19], off sc1
	s_nop 1
	v_add_u32_e32 v18, 0x2000, v133
	v_and_b32_e32 v18, 0x7f80, v18
	v_lshlrev_b32_e32 v18, 1, v18
	v_mov_b32_e32 v19, v173
	v_lshl_add_u64 v[18:19], s[30:31], 0, v[18:19]
	v_lshl_add_u64 v[20:21], v[18:19], 0, v[172:173]
	v_cvt_pk_bf16_f32 v24, v50, v51
	v_cvt_pk_bf16_f32 v25, v52, v53
	global_store_dwordx2 v[20:21], v[24:25], off sc1
	s_nop 1
	v_lshl_add_u64 v[22:23], v[20:21], 0, s[22:23]
	v_cvt_pk_bf16_f32 v26, v102, v103
	v_cvt_pk_bf16_f32 v27, v104, v105
	global_store_dwordx2 v[22:23], v[26:27], off sc1
	s_nop 1
	v_lshl_add_u64 v[18:19], v[18:19], 0, v[54:55]
	v_cvt_pk_bf16_f32 v22, v94, v95
	v_cvt_pk_bf16_f32 v23, v96, v97
	v_cvt_pk_bf16_f32 v14, v14, v15
	global_store_dwordx2 v[18:19], v[22:23], off sc1
	s_nop 1
	v_lshl_add_u64 v[20:21], v[18:19], 0, s[22:23]
	v_cvt_pk_bf16_f32 v15, v16, v17
	global_store_dwordx2 v[20:21], v[14:15], off sc1
	s_nop 1
	v_add_u32_e32 v14, 0x2800, v133
	v_and_b32_e32 v14, 0x7f80, v14
	v_lshlrev_b32_e32 v14, 1, v14
	v_mov_b32_e32 v15, v173
	v_lshl_add_u64 v[14:15], s[30:31], 0, v[14:15]
	v_lshl_add_u64 v[16:17], v[14:15], 0, v[172:173]
	v_cvt_pk_bf16_f32 v20, v70, v71
	v_cvt_pk_bf16_f32 v21, v72, v73
	global_store_dwordx2 v[16:17], v[20:21], off sc1
	s_nop 1
	v_lshl_add_u64 v[18:19], v[16:17], 0, s[22:23]
	v_cvt_pk_bf16_f32 v22, v114, v115
	v_cvt_pk_bf16_f32 v23, v116, v117
	global_store_dwordx2 v[18:19], v[22:23], off sc1
	s_nop 1
	v_lshl_add_u64 v[14:15], v[14:15], 0, v[54:55]
	v_cvt_pk_bf16_f32 v18, v106, v107
	v_cvt_pk_bf16_f32 v19, v108, v109
	v_cvt_pk_bf16_f32 v10, v10, v11
	global_store_dwordx2 v[14:15], v[18:19], off sc1
	s_nop 1
	v_lshl_add_u64 v[16:17], v[14:15], 0, s[22:23]
	v_cvt_pk_bf16_f32 v11, v12, v13
	global_store_dwordx2 v[16:17], v[10:11], off sc1
	s_nop 1
	v_add_u32_e32 v10, 0x3000, v133
	v_and_b32_e32 v10, 0x7f80, v10
	v_lshlrev_b32_e32 v10, 1, v10
	v_mov_b32_e32 v11, v173
	v_lshl_add_u64 v[10:11], s[30:31], 0, v[10:11]
	v_lshl_add_u64 v[12:13], v[10:11], 0, v[172:173]
	v_cvt_pk_bf16_f32 v16, v86, v87
	v_cvt_pk_bf16_f32 v17, v88, v89
	global_store_dwordx2 v[12:13], v[16:17], off sc1
	s_nop 1
	v_lshl_add_u64 v[14:15], v[12:13], 0, s[22:23]
	v_cvt_pk_bf16_f32 v18, v122, v123
	v_cvt_pk_bf16_f32 v19, v124, v125
	global_store_dwordx2 v[14:15], v[18:19], off sc1
	s_nop 1
	v_lshl_add_u64 v[10:11], v[10:11], 0, v[54:55]
	v_lshl_add_u64 v[12:13], v[10:11], 0, s[22:23]
	v_cvt_pk_bf16_f32 v14, v118, v119
	v_cvt_pk_bf16_f32 v15, v120, v121
	global_store_dwordx2 v[10:11], v[14:15], off sc1
	s_nop 1
	v_add_u32_e32 v10, 0x3800, v133
	v_and_b32_e32 v10, 0x7f80, v10
	v_lshlrev_b32_e32 v10, 1, v10
	v_mov_b32_e32 v11, v173
	v_cvt_pk_bf16_f32 v16, v138, v139
	v_cvt_pk_bf16_f32 v17, v140, v141
	global_store_dwordx2 v[12:13], v[16:17], off sc1
	s_nop 1
	v_lshl_add_u64 v[10:11], s[30:31], 0, v[10:11]
	v_lshl_add_u64 v[12:13], v[10:11], 0, v[172:173]
	v_cvt_pk_bf16_f32 v16, v98, v99
	v_cvt_pk_bf16_f32 v17, v100, v101
	global_store_dwordx2 v[12:13], v[16:17], off sc1
	s_nop 1
	v_lshl_add_u64 v[14:15], v[12:13], 0, s[22:23]
	v_cvt_pk_bf16_f32 v18, v110, v111
	v_cvt_pk_bf16_f32 v19, v112, v113
	global_store_dwordx2 v[14:15], v[18:19], off sc1
	s_nop 1
	v_lshl_add_u64 v[10:11], v[10:11], 0, v[54:55]
	v_cvt_pk_bf16_f32 v6, v6, v7
	v_cvt_pk_bf16_f32 v7, v8, v9
	global_store_dwordx2 v[10:11], v[6:7], off sc1
	s_nop 1
	v_lshl_add_u64 v[12:13], v[10:11], 0, s[22:23]
	v_cvt_pk_bf16_f32 v2, v2, v3
	v_cvt_pk_bf16_f32 v3, v4, v5
	global_store_dwordx2 v[12:13], v[2:3], off sc1
	s_nop 1
	s_waitcnt vmcnt(0)
	s_barrier
	s_and_saveexec_b64 s[2:3], s[0:1]
	s_cbranch_execz .LBB0_1419
	v_mov_b32_e32 v2, 1
	global_store_dword v173, v2, s[6:7] sc1
	s_branch .LBB0_1419

.LBB0_1540:
	s_add_i32 s42, s37, 0xffff8000
	s_and_b32 s42, s42, 0x8000
	s_add_i32 s41, s40, 0
	s_add_i32 s42, s24, s42
	v_add_u32_e32 v234, s42, v183
	v_add_u32_e32 v235, s41, v207
	v_add_u32_e32 v240, s42, v179
	v_add_u32_e32 v242, s42, v172
	v_add_u32_e32 v238, s42, v181
	s_branch .Lrot_m2

.Lrot_m2:
	ds_read_b64_tr_b16 v[210:211], v234
	ds_read_b64_tr_b16 v[212:213], v234 offset:2048
	ds_read_b64_tr_b16 v[214:215], v238
	ds_read_b64_tr_b16 v[216:217], v238 offset:2048
	ds_read_b128 v[162:165], v235
	ds_read_b128 v[166:169], v235 offset:2048
	ds_read_b64_tr_b16 v[218:219], v240
	ds_read_b64_tr_b16 v[220:221], v240 offset:2048
	ds_read_b64_tr_b16 v[222:223], v242
	ds_read_b64_tr_b16 v[224:225], v242 offset:2048
	s_waitcnt lgkmcnt(5)
	v_mfma_f32_16x16x32_bf16 v[34:37], v[210:213], v[162:165], v[34:37]
	ds_read_b128 v[226:229], v235 offset:4096
	s_and_b32 s42, s37, 0x8000
	v_add_u32_e32 v230, 0xffef8000, v209
	v_mfma_f32_16x16x32_bf16 v[38:41], v[214:217], v[162:165], v[38:41]
	s_add_i32 s43, s36, s39
	s_mov_b32 s44, m0
	s_mov_b32 m0, s43
	s_nop 0
	global_load_lds_dwordx4 v230, s[14:15]
	s_mov_b32 m0, s44
	s_waitcnt lgkmcnt(3)
	v_mfma_f32_16x16x32_bf16 v[42:45], v[218:221], v[162:165], v[42:45]
	s_waitcnt lgkmcnt(1)
	v_mfma_f32_16x16x32_bf16 v[46:49], v[222:225], v[162:165], v[46:49]
	v_mfma_f32_16x16x32_bf16 v[50:53], v[210:213], v[166:169], v[50:53]
	ds_read_b128 v[162:165], v235 offset:6144
	v_add_u32_e32 v230, 0xfff50000, v209
	s_add_i32 s44, s43, 0x2000
	v_mfma_f32_16x16x32_bf16 v[54:57], v[214:217], v[166:169], v[54:57]
	s_mov_b32 s45, m0
	s_mov_b32 m0, s44
	s_nop 0
	global_load_lds_dwordx4 v230, s[14:15]
	s_mov_b32 m0, s45
	v_mfma_f32_16x16x32_bf16 v[58:61], v[218:221], v[166:169], v[58:61]
	v_mfma_f32_16x16x32_bf16 v[62:65], v[222:225], v[166:169], v[62:65]
	s_waitcnt lgkmcnt(1)
	v_mfma_f32_16x16x32_bf16 v[66:69], v[210:213], v[226:229], v[66:69]
	ds_read_b128 v[166:169], v235 offset:8192
	v_add_u32_e32 v230, 0xfffa8000, v209
	s_add_i32 s44, s43, 0x4000
	v_mfma_f32_16x16x32_bf16 v[70:73], v[214:217], v[226:229], v[70:73]
	s_mov_b32 s45, m0
	s_mov_b32 m0, s44
	s_nop 0
	global_load_lds_dwordx4 v230, s[14:15]
	s_mov_b32 m0, s45
	v_mfma_f32_16x16x32_bf16 v[74:77], v[218:221], v[226:229], v[74:77]
	v_mfma_f32_16x16x32_bf16 v[78:81], v[222:225], v[226:229], v[78:81]
	s_waitcnt lgkmcnt(1)
	v_mfma_f32_16x16x32_bf16 v[82:85], v[210:213], v[162:165], v[82:85]
	ds_read_b128 v[226:229], v235 offset:10240
	s_addk_i32 s43, 0x6000
	s_mov_b32 s44, m0
	s_mov_b32 m0, s43
	s_nop 0
	global_load_lds_dwordx4 v209, s[14:15]
	s_mov_b32 m0, s44
	v_mfma_f32_16x16x32_bf16 v[86:89], v[214:217], v[162:165], v[86:89]
	v_mfma_f32_16x16x32_bf16 v[90:93], v[218:221], v[162:165], v[90:93]
	v_mfma_f32_16x16x32_bf16 v[94:97], v[222:225], v[162:165], v[94:97]
	ds_read_b128 v[230:233], v235 offset:12288
	ds_read_b64_tr_b16 v[162:163], v234 offset:16384
	ds_read_b64_tr_b16 v[164:165], v234 offset:18432
	s_waitcnt lgkmcnt(4)
	v_mfma_f32_16x16x32_bf16 v[98:101], v[210:213], v[166:169], v[98:101]
	v_mfma_f32_16x16x32_bf16 v[102:105], v[214:217], v[166:169], v[102:105]
	v_mfma_f32_16x16x32_bf16 v[106:109], v[218:221], v[166:169], v[106:109]
	v_mfma_f32_16x16x32_bf16 v[110:113], v[222:225], v[166:169], v[110:113]
	ds_read_b128 v[234:237], v235 offset:14336
	ds_read_b64_tr_b16 v[166:167], v238 offset:16384
	ds_read_b64_tr_b16 v[168:169], v238 offset:18432
	s_waitcnt lgkmcnt(6)
	v_mfma_f32_16x16x32_bf16 v[114:117], v[210:213], v[226:229], v[114:117]
	v_mfma_f32_16x16x32_bf16 v[118:121], v[214:217], v[226:229], v[118:121]
	v_mfma_f32_16x16x32_bf16 v[122:125], v[218:221], v[226:229], v[122:125]
	v_mfma_f32_16x16x32_bf16 v[126:129], v[222:225], v[226:229], v[126:129]
	v_add_u32_e32 v243, s41, v208
	ds_read_b128 v[226:229], v243
	ds_read_b64_tr_b16 v[238:239], v240 offset:16384
	ds_read_b64_tr_b16 v[240:241], v240 offset:18432
	s_waitcnt lgkmcnt(8)
	v_mfma_f32_16x16x32_bf16 v[130:133], v[210:213], v[230:233], v[130:133]
	v_mfma_f32_16x16x32_bf16 v[134:137], v[214:217], v[230:233], v[134:137]
	v_mfma_f32_16x16x32_bf16 v[138:141], v[218:221], v[230:233], v[138:141]
	v_mfma_f32_16x16x32_bf16 v[142:145], v[222:225], v[230:233], v[142:145]
	s_waitcnt lgkmcnt(5)
	v_mfma_f32_16x16x32_bf16 v[146:149], v[210:213], v[234:237], v[146:149]
	ds_read_b128 v[210:213], v243 offset:2048
	s_add_i32 s41, s24, s42
	v_mfma_f32_16x16x32_bf16 v[150:153], v[214:217], v[234:237], v[150:153]
	ds_read_b64_tr_b16 v[214:215], v242 offset:16384
	ds_read_b64_tr_b16 v[216:217], v242 offset:18432
	v_mfma_f32_16x16x32_bf16 v[158:161], v[218:221], v[234:237], v[158:161]
	v_mfma_f32_16x16x32_bf16 v[154:157], v[222:225], v[234:237], v[154:157]
	ds_read_b128 v[218:221], v243 offset:4096
	s_waitcnt lgkmcnt(6)
	v_mfma_f32_16x16x32_bf16 v[34:37], v[162:165], v[226:229], v[34:37]
	s_add_u32 s44, s2, s16
	s_waitcnt vmcnt(11)
	s_addc_u32 s45, s38, s17
	v_mfma_f32_16x16x32_bf16 v[38:41], v[166:169], v[226:229], v[38:41]
	v_cvt_pk_bf16_f32 v30, v30, v31
	v_cvt_pk_bf16_f32 v31, v32, v33
	v_add_u32_e32 v230, s41, v206
	s_waitcnt lgkmcnt(4)
	v_mfma_f32_16x16x32_bf16 v[42:45], v[238:241], v[226:229], v[42:45]
	s_add_u32 s42, s44, 0x100000
	ds_write_b64 v230, v[30:31]
	s_addc_u32 s43, s45, 0
	s_waitcnt lgkmcnt(2)
	v_mfma_f32_16x16x32_bf16 v[46:49], v[214:217], v[226:229], v[46:49]
	global_load_dwordx4 v[30:33], v199, s[42:43] nt
	v_mfma_f32_16x16x32_bf16 v[50:53], v[162:165], v[210:213], v[50:53]
	ds_read_b128 v[222:225], v243 offset:6144
	s_waitcnt vmcnt(11)
	v_add_u32_e32 v226, s41, v205
	v_mfma_f32_16x16x32_bf16 v[54:57], v[166:169], v[210:213], v[54:57]
	v_cvt_pk_bf16_f32 v26, v26, v27
	v_cvt_pk_bf16_f32 v27, v28, v29
	s_add_u32 s42, s44, 0x110000
	v_mfma_f32_16x16x32_bf16 v[58:61], v[238:241], v[210:213], v[58:61]
	ds_write_b64 v226, v[26:27] offset:4096
	s_addc_u32 s43, s45, 0
	global_load_dwordx4 v[26:29], v199, s[42:43] nt
	v_mfma_f32_16x16x32_bf16 v[62:65], v[214:217], v[210:213], v[62:65]
	s_waitcnt lgkmcnt(3)
	v_mfma_f32_16x16x32_bf16 v[66:69], v[162:165], v[218:221], v[66:69]
	ds_read_b128 v[210:213], v243 offset:8192
	s_waitcnt vmcnt(11)
	s_add_u32 s42, s44, 0x120000
	v_mfma_f32_16x16x32_bf16 v[70:73], v[166:169], v[218:221], v[70:73]
	v_cvt_pk_bf16_f32 v22, v22, v23
	v_cvt_pk_bf16_f32 v23, v24, v25
	ds_write_b64 v230, v[22:23] offset:8192
	v_mfma_f32_16x16x32_bf16 v[74:77], v[238:241], v[218:221], v[74:77]
	s_addc_u32 s43, s45, 0
	global_load_dwordx4 v[22:25], v199, s[42:43] nt
	v_mfma_f32_16x16x32_bf16 v[78:81], v[214:217], v[218:221], v[78:81]
	s_waitcnt lgkmcnt(3)
	v_mfma_f32_16x16x32_bf16 v[82:85], v[162:165], v[222:225], v[82:85]
	ds_read_b128 v[218:221], v243 offset:10240
	s_waitcnt vmcnt(11)
	s_add_u32 s42, s44, 0x130000
	v_mfma_f32_16x16x32_bf16 v[86:89], v[166:169], v[222:225], v[86:89]
	v_cvt_pk_bf16_f32 v18, v18, v19
	v_cvt_pk_bf16_f32 v19, v20, v21
	ds_write_b64 v226, v[18:19] offset:12288
	v_mfma_f32_16x16x32_bf16 v[90:93], v[238:241], v[222:225], v[90:93]
	s_addc_u32 s43, s45, 0
	global_load_dwordx4 v[18:21], v199, s[42:43] nt
	v_mfma_f32_16x16x32_bf16 v[94:97], v[214:217], v[222:225], v[94:97]
	s_waitcnt lgkmcnt(3)
	v_mfma_f32_16x16x32_bf16 v[98:101], v[162:165], v[210:213], v[98:101]
	ds_read_b128 v[222:225], v243 offset:12288
	s_waitcnt vmcnt(11)
	s_add_u32 s42, s44, 0x140000
	v_mfma_f32_16x16x32_bf16 v[102:105], v[166:169], v[210:213], v[102:105]
	v_cvt_pk_bf16_f32 v14, v14, v15
	v_cvt_pk_bf16_f32 v15, v16, v17
	ds_write_b64 v230, v[14:15] offset:16384
	v_mfma_f32_16x16x32_bf16 v[106:109], v[238:241], v[210:213], v[106:109]
	s_addc_u32 s43, s45, 0
	global_load_dwordx4 v[14:17], v199, s[42:43] nt
	v_mfma_f32_16x16x32_bf16 v[110:113], v[214:217], v[210:213], v[110:113]
	s_waitcnt lgkmcnt(3)
	v_mfma_f32_16x16x32_bf16 v[114:117], v[162:165], v[218:221], v[114:117]
	ds_read_b128 v[210:213], v243 offset:14336
	s_waitcnt vmcnt(11)
	s_add_u32 s42, s44, 0x150000
	v_mfma_f32_16x16x32_bf16 v[118:121], v[166:169], v[218:221], v[118:121]
	v_cvt_pk_bf16_f32 v10, v10, v11
	v_cvt_pk_bf16_f32 v11, v12, v13
	ds_write_b64 v226, v[10:11] offset:20480
	v_mfma_f32_16x16x32_bf16 v[122:125], v[238:241], v[218:221], v[122:125]
	s_addc_u32 s43, s45, 0
	global_load_dwordx4 v[10:13], v199, s[42:43] nt
	v_mfma_f32_16x16x32_bf16 v[126:129], v[214:217], v[218:221], v[126:129]
	s_waitcnt lgkmcnt(3)
	v_mfma_f32_16x16x32_bf16 v[130:133], v[162:165], v[222:225], v[130:133]
	s_waitcnt vmcnt(11)
	s_add_u32 s42, s44, 0x160000
	v_cvt_pk_bf16_f32 v6, v6, v7
	v_mfma_f32_16x16x32_bf16 v[134:137], v[166:169], v[222:225], v[134:137]
	v_cvt_pk_bf16_f32 v7, v8, v9
	ds_write_b64 v230, v[6:7] offset:24576
	s_addc_u32 s43, s45, 0
	v_mfma_f32_16x16x32_bf16 v[138:141], v[238:241], v[222:225], v[138:141]
	global_load_dwordx4 v[6:9], v199, s[42:43] nt
	v_mfma_f32_16x16x32_bf16 v[142:145], v[214:217], v[222:225], v[142:145]
	s_waitcnt lgkmcnt(2)
	v_mfma_f32_16x16x32_bf16 v[146:149], v[162:165], v[210:213], v[146:149]
	s_waitcnt vmcnt(11)
	s_add_u32 s42, s44, 0x170000
	v_cvt_pk_bf16_f32 v2, v2, v3
	v_mfma_f32_16x16x32_bf16 v[150:153], v[166:169], v[210:213], v[150:153]
	v_cvt_pk_bf16_f32 v3, v4, v5
	ds_write_b64 v226, v[2:3] offset:28672
	s_addc_u32 s43, s45, 0
	v_mfma_f32_16x16x32_bf16 v[158:161], v[238:241], v[210:213], v[158:161]
	global_load_dwordx4 v[2:5], v199, s[42:43] nt
	v_mfma_f32_16x16x32_bf16 v[154:157], v[214:217], v[210:213], v[154:157]
	s_add_i32 s41, s40, 0x8000
	s_cmp_lg_u32 s40, 0x10000
	s_cselect_b32 s40, s41, 0
	s_add_i32 s41, s39, 0x8000
	s_cmp_lg_u32 s39, 0x10000
	s_cselect_b32 s39, s41, 0
	s_add_u32 s16, s16, 0x80000
	s_addc_u32 s17, s17, 0
	s_add_i32 s37, s37, 0x8000
	v_add_u32_e32 v209, 0x80, v209
	s_add_i32 s42, s37, 0xffff8000
	s_and_b32 s42, s42, 0x8000
	s_add_i32 s41, s40, 0
	s_add_i32 s42, s24, s42
	v_add_u32_e32 v234, s42, v183
	v_add_u32_e32 v235, s41, v207
	v_add_u32_e32 v240, s42, v179
	v_add_u32_e32 v242, s42, v172
	v_add_u32_e32 v238, s42, v181
	s_waitcnt lgkmcnt(0)
	s_cmp_lg_u32 s16, 0x1500000
	s_cbranch_scc1 .Lrot_m2_head
	s_barrier
	v_add_u32_e32 v209, s24, v183
	v_add_u32_e32 v242, 0, v207
	v_add_u32_e32 v207, s24, v179
	v_add_u32_e32 v243, s24, v172
	v_add_u32_e32 v236, s24, v181
	ds_read_b64_tr_b16 v[162:163], v209
	ds_read_b64_tr_b16 v[164:165], v209 offset:2048
	ds_read_b64_tr_b16 v[166:167], v236
	ds_read_b64_tr_b16 v[168:169], v236 offset:2048
	ds_read_b128 v[210:213], v242
	ds_read_b128 v[214:217], v242 offset:2048
	ds_read_b64_tr_b16 v[218:219], v207
	ds_read_b64_tr_b16 v[220:221], v207 offset:2048
	ds_read_b64_tr_b16 v[222:223], v243
	ds_read_b64_tr_b16 v[224:225], v243 offset:2048
	s_waitcnt lgkmcnt(5)
	v_mfma_f32_16x16x32_bf16 v[34:37], v[162:165], v[210:213], v[34:37]
	ds_read_b128 v[226:229], v242 offset:4096
	v_mfma_f32_16x16x32_bf16 v[38:41], v[166:169], v[210:213], v[38:41]
	s_waitcnt lgkmcnt(3)
	v_mfma_f32_16x16x32_bf16 v[42:45], v[218:221], v[210:213], v[42:45]
	s_waitcnt lgkmcnt(1)
	v_mfma_f32_16x16x32_bf16 v[46:49], v[222:225], v[210:213], v[46:49]
	v_mfma_f32_16x16x32_bf16 v[50:53], v[162:165], v[214:217], v[50:53]
	ds_read_b128 v[210:213], v242 offset:6144
	v_mfma_f32_16x16x32_bf16 v[54:57], v[166:169], v[214:217], v[54:57]
	v_mfma_f32_16x16x32_bf16 v[58:61], v[218:221], v[214:217], v[58:61]
	v_mfma_f32_16x16x32_bf16 v[62:65], v[222:225], v[214:217], v[62:65]
	s_waitcnt lgkmcnt(1)
	v_mfma_f32_16x16x32_bf16 v[66:69], v[162:165], v[226:229], v[66:69]
	ds_read_b128 v[214:217], v242 offset:8192
	v_mfma_f32_16x16x32_bf16 v[70:73], v[166:169], v[226:229], v[70:73]
	v_mfma_f32_16x16x32_bf16 v[74:77], v[218:221], v[226:229], v[74:77]
	v_mfma_f32_16x16x32_bf16 v[78:81], v[222:225], v[226:229], v[78:81]
	s_waitcnt lgkmcnt(1)
	v_mfma_f32_16x16x32_bf16 v[82:85], v[162:165], v[210:213], v[82:85]
	ds_read_b128 v[226:229], v242 offset:10240
	v_mfma_f32_16x16x32_bf16 v[86:89], v[166:169], v[210:213], v[86:89]
	v_mfma_f32_16x16x32_bf16 v[90:93], v[218:221], v[210:213], v[90:93]
	v_mfma_f32_16x16x32_bf16 v[94:97], v[222:225], v[210:213], v[94:97]
	ds_read_b128 v[210:213], v242 offset:12288
	ds_read_b64_tr_b16 v[230:231], v209 offset:16384
	ds_read_b64_tr_b16 v[232:233], v209 offset:18432
	s_waitcnt lgkmcnt(4)
	v_mfma_f32_16x16x32_bf16 v[98:101], v[162:165], v[214:217], v[98:101]
	v_mfma_f32_16x16x32_bf16 v[102:105], v[166:169], v[214:217], v[102:105]
	v_mfma_f32_16x16x32_bf16 v[106:109], v[218:221], v[214:217], v[106:109]
	v_mfma_f32_16x16x32_bf16 v[110:113], v[222:225], v[214:217], v[110:113]
	ds_read_b128 v[214:217], v242 offset:14336
	ds_read_b64_tr_b16 v[234:235], v236 offset:16384
	ds_read_b64_tr_b16 v[236:237], v236 offset:18432
	s_waitcnt lgkmcnt(6)
	v_mfma_f32_16x16x32_bf16 v[114:117], v[162:165], v[226:229], v[114:117]
	v_mfma_f32_16x16x32_bf16 v[118:121], v[166:169], v[226:229], v[118:121]
	v_mfma_f32_16x16x32_bf16 v[122:125], v[218:221], v[226:229], v[122:125]
	v_mfma_f32_16x16x32_bf16 v[126:129], v[222:225], v[226:229], v[126:129]
	v_add_u32_e32 v244, 0, v208
	ds_read_b128 v[226:229], v244
	ds_read_b64_tr_b16 v[238:239], v207 offset:16384
	ds_read_b64_tr_b16 v[240:241], v207 offset:18432
	s_waitcnt lgkmcnt(8)
	v_mfma_f32_16x16x32_bf16 v[130:133], v[162:165], v[210:213], v[130:133]
	v_mfma_f32_16x16x32_bf16 v[134:137], v[166:169], v[210:213], v[134:137]
	v_mfma_f32_16x16x32_bf16 v[138:141], v[218:221], v[210:213], v[138:141]
	v_mfma_f32_16x16x32_bf16 v[142:145], v[222:225], v[210:213], v[142:145]
	s_waitcnt lgkmcnt(5)
	v_mfma_f32_16x16x32_bf16 v[146:149], v[162:165], v[214:217], v[146:149]
	v_mfma_f32_16x16x32_bf16 v[150:153], v[166:169], v[214:217], v[150:153]
	ds_read_b128 v[162:165], v244 offset:2048
	ds_read_b64_tr_b16 v[166:167], v243 offset:16384
	ds_read_b64_tr_b16 v[168:169], v243 offset:18432
	v_mfma_f32_16x16x32_bf16 v[158:161], v[218:221], v[214:217], v[158:161]
	v_mfma_f32_16x16x32_bf16 v[154:157], v[222:225], v[214:217], v[154:157]
	ds_read_b128 v[208:211], v244 offset:4096
	s_waitcnt vmcnt(7)
	v_add_u32_e32 v206, s25, v206
	v_cvt_pk_bf16_f32 v30, v30, v31
	v_cvt_pk_bf16_f32 v31, v32, v33
	s_waitcnt lgkmcnt(6)
	v_mfma_f32_16x16x32_bf16 v[34:37], v[230:233], v[226:229], v[34:37]
	ds_write_b64 v206, v[30:31]
	v_mfma_f32_16x16x32_bf16 v[38:41], v[234:237], v[226:229], v[38:41]
	s_waitcnt lgkmcnt(5)
	v_mfma_f32_16x16x32_bf16 v[42:45], v[238:241], v[226:229], v[42:45]
	s_waitcnt lgkmcnt(2)
	v_mfma_f32_16x16x32_bf16 v[30:33], v[166:169], v[226:229], v[46:49]
	v_mfma_f32_16x16x32_bf16 v[46:49], v[230:233], v[162:165], v[50:53]
	v_add_u32_e32 v205, s25, v205
	v_mfma_f32_16x16x32_bf16 v[50:53], v[234:237], v[162:165], v[54:57]
	s_nop 2
	ds_read_b128 v[54:57], v244 offset:6144
	s_waitcnt vmcnt(6)
	v_mfma_f32_16x16x32_bf16 v[58:61], v[238:241], v[162:165], v[58:61]
	v_cvt_pk_bf16_f32 v26, v26, v27
	v_cvt_pk_bf16_f32 v27, v28, v29
	ds_write_b64 v205, v[26:27] offset:4096
	v_mfma_f32_16x16x32_bf16 v[26:29], v[166:169], v[162:165], v[62:65]
	s_waitcnt lgkmcnt(3)
	v_mfma_f32_16x16x32_bf16 v[62:65], v[230:233], v[208:211], v[66:69]
	v_mfma_f32_16x16x32_bf16 v[66:69], v[234:237], v[208:211], v[70:73]
	s_nop 2
	ds_read_b128 v[70:73], v244 offset:8192
	s_waitcnt vmcnt(5)
	v_mfma_f32_16x16x32_bf16 v[74:77], v[238:241], v[208:211], v[74:77]
	v_cvt_pk_bf16_f32 v22, v22, v23
	v_cvt_pk_bf16_f32 v23, v24, v25
	ds_write_b64 v206, v[22:23] offset:8192
	v_mfma_f32_16x16x32_bf16 v[22:25], v[166:169], v[208:211], v[78:81]
	s_waitcnt lgkmcnt(3)
	v_mfma_f32_16x16x32_bf16 v[78:81], v[230:233], v[54:57], v[82:85]
	v_mfma_f32_16x16x32_bf16 v[82:85], v[234:237], v[54:57], v[86:89]
	s_nop 2
	ds_read_b128 v[86:89], v244 offset:10240
	s_waitcnt vmcnt(4)
	v_mfma_f32_16x16x32_bf16 v[90:93], v[238:241], v[54:57], v[90:93]
	v_cvt_pk_bf16_f32 v18, v18, v19
	v_cvt_pk_bf16_f32 v19, v20, v21
	ds_write_b64 v205, v[18:19] offset:12288
	v_mfma_f32_16x16x32_bf16 v[18:21], v[166:169], v[54:57], v[94:97]
	s_waitcnt lgkmcnt(3)
	v_mfma_f32_16x16x32_bf16 v[54:57], v[230:233], v[70:73], v[98:101]
	s_nop 2
	ds_read_b128 v[98:101], v244 offset:12288
	s_waitcnt vmcnt(3)
	v_mfma_f32_16x16x32_bf16 v[94:97], v[234:237], v[70:73], v[102:105]
	v_cvt_pk_bf16_f32 v14, v14, v15
	v_cvt_pk_bf16_f32 v15, v16, v17
	ds_write_b64 v206, v[14:15] offset:16384
	v_mfma_f32_16x16x32_bf16 v[102:105], v[238:241], v[70:73], v[106:109]
	v_mfma_f32_16x16x32_bf16 v[14:17], v[166:169], v[70:73], v[110:113]
	s_nop 2
	ds_read_b128 v[110:113], v244 offset:14336
	s_waitcnt vmcnt(2)
	s_waitcnt lgkmcnt(4)
	v_mfma_f32_16x16x32_bf16 v[70:73], v[230:233], v[86:89], v[114:117]
	v_cvt_pk_bf16_f32 v10, v10, v11
	v_cvt_pk_bf16_f32 v11, v12, v13
	ds_write_b64 v205, v[10:11] offset:20480
	v_mfma_f32_16x16x32_bf16 v[106:109], v[234:237], v[86:89], v[118:121]
	v_mfma_f32_16x16x32_bf16 v[114:117], v[238:241], v[86:89], v[122:125]
	v_mfma_f32_16x16x32_bf16 v[10:13], v[166:169], v[86:89], v[126:129]
	s_waitcnt vmcnt(1)
	s_waitcnt lgkmcnt(3)
	v_mfma_f32_16x16x32_bf16 v[86:89], v[230:233], v[98:101], v[130:133]
	v_cvt_pk_bf16_f32 v6, v6, v7
	v_cvt_pk_bf16_f32 v7, v8, v9
	ds_write_b64 v206, v[6:7] offset:24576
	v_mfma_f32_16x16x32_bf16 v[118:121], v[234:237], v[98:101], v[134:137]
	v_mfma_f32_16x16x32_bf16 v[122:125], v[238:241], v[98:101], v[138:141]
	v_mfma_f32_16x16x32_bf16 v[6:9], v[166:169], v[98:101], v[142:145]
	s_waitcnt vmcnt(0)
	s_waitcnt lgkmcnt(2)
	v_mfma_f32_16x16x32_bf16 v[98:101], v[230:233], v[110:113], v[146:149]
	v_cvt_pk_bf16_f32 v2, v2, v3
	v_cvt_pk_bf16_f32 v3, v4, v5
	ds_write_b64 v205, v[2:3] offset:28672
	v_mfma_f32_16x16x32_bf16 v[126:129], v[234:237], v[110:113], v[150:153]
	v_mfma_f32_16x16x32_bf16 v[130:133], v[238:241], v[110:113], v[158:161]
	v_mfma_f32_16x16x32_bf16 v[2:5], v[166:169], v[110:113], v[154:157]
	s_waitcnt lgkmcnt(0)
	s_barrier
	v_add_u32_e32 v168, s25, v183
	v_add_u32_e32 v181, s25, v181
	v_add_u32_e32 v179, s25, v179
	ds_read_b64_tr_b16 v[110:111], v168
	ds_read_b64_tr_b16 v[112:113], v168 offset:2048
	ds_read_b64_tr_b16 v[134:135], v181
	ds_read_b64_tr_b16 v[136:137], v181 offset:2048
	ds_read_b128 v[138:141], v242 offset:32768
	ds_read_b64_tr_b16 v[142:143], v179
	ds_read_b128 v[146:149], v242 offset:34816
	ds_read_b128 v[150:153], v242 offset:36864
	ds_read_b64_tr_b16 v[144:145], v179 offset:2048
	v_add_u32_e32 v172, s25, v172
	ds_read_b64_tr_b16 v[154:155], v172
	ds_read_b64_tr_b16 v[156:157], v172 offset:2048
	s_waitcnt lgkmcnt(6)
	v_mfma_f32_16x16x32_bf16 v[34:37], v[110:113], v[138:141], v[34:37]
	v_mfma_f32_16x16x32_bf16 v[38:41], v[134:137], v[138:141], v[38:41]
	s_waitcnt lgkmcnt(2)
	v_mfma_f32_16x16x32_bf16 v[42:45], v[142:145], v[138:141], v[42:45]
	s_waitcnt lgkmcnt(0)
	v_mfma_f32_16x16x32_bf16 v[30:33], v[154:157], v[138:141], v[30:33]
	v_mfma_f32_16x16x32_bf16 v[46:49], v[110:113], v[146:149], v[46:49]
	ds_read_b128 v[138:141], v242 offset:38912
	v_mfma_f32_16x16x32_bf16 v[50:53], v[134:137], v[146:149], v[50:53]
	v_mfma_f32_16x16x32_bf16 v[58:61], v[142:145], v[146:149], v[58:61]
	v_mfma_f32_16x16x32_bf16 v[26:29], v[154:157], v[146:149], v[26:29]
	v_mfma_f32_16x16x32_bf16 v[62:65], v[110:113], v[150:153], v[62:65]
	ds_read_b128 v[146:149], v242 offset:40960
	v_mfma_f32_16x16x32_bf16 v[66:69], v[134:137], v[150:153], v[66:69]
	v_mfma_f32_16x16x32_bf16 v[74:77], v[142:145], v[150:153], v[74:77]
	v_mfma_f32_16x16x32_bf16 v[22:25], v[154:157], v[150:153], v[22:25]
	s_waitcnt lgkmcnt(1)
	v_mfma_f32_16x16x32_bf16 v[150:153], v[134:137], v[138:141], v[82:85]
	s_nop 2
	ds_read_b128 v[82:85], v242 offset:43008
	v_mfma_f32_16x16x32_bf16 v[78:81], v[110:113], v[138:141], v[78:81]
	v_mfma_f32_16x16x32_bf16 v[18:21], v[154:157], v[138:141], v[18:21]
	v_mfma_f32_16x16x32_bf16 v[158:161], v[142:145], v[138:141], v[90:93]
	s_nop 2
	ds_read_b128 v[90:93], v242 offset:45056
	ds_read_b64_tr_b16 v[166:167], v168 offset:16384
	ds_read_b64_tr_b16 v[168:169], v168 offset:18432
	s_waitcnt lgkmcnt(4)
	v_mfma_f32_16x16x32_bf16 v[54:57], v[110:113], v[146:149], v[54:57]
	v_mfma_f32_16x16x32_bf16 v[14:17], v[154:157], v[146:149], v[14:17]
	v_mfma_f32_16x16x32_bf16 v[138:141], v[134:137], v[146:149], v[94:97]
	v_mfma_f32_16x16x32_bf16 v[162:165], v[142:145], v[146:149], v[102:105]
	s_waitcnt lgkmcnt(3)
	v_mfma_f32_16x16x32_bf16 v[146:149], v[110:113], v[82:85], v[70:73]
	s_nop 2
	ds_read_b128 v[70:73], v242 offset:47104
	ds_read_b64_tr_b16 v[214:215], v181 offset:16384
	ds_read_b64_tr_b16 v[216:217], v181 offset:18432
	v_mfma_f32_16x16x32_bf16 v[10:13], v[154:157], v[82:85], v[10:13]
	v_mfma_f32_16x16x32_bf16 v[206:209], v[134:137], v[82:85], v[106:109]
	v_mfma_f32_16x16x32_bf16 v[210:213], v[142:145], v[82:85], v[114:117]
	ds_read_b128 v[82:85], v244 offset:32768
	ds_read_b64_tr_b16 v[230:231], v179 offset:16384
	ds_read_b64_tr_b16 v[232:233], v179 offset:18432
	s_waitcnt lgkmcnt(8)
	v_mfma_f32_16x16x32_bf16 v[6:9], v[154:157], v[90:93], v[6:9]
	v_mfma_f32_16x16x32_bf16 v[218:221], v[110:113], v[90:93], v[86:89]
	v_mfma_f32_16x16x32_bf16 v[222:225], v[134:137], v[90:93], v[118:121]
	v_mfma_f32_16x16x32_bf16 v[226:229], v[142:145], v[90:93], v[122:125]
	s_waitcnt lgkmcnt(5)
	v_mfma_f32_16x16x32_bf16 v[130:133], v[142:145], v[70:73], v[130:133]
	ds_read_b128 v[86:89], v244 offset:34816
	ds_read_b64_tr_b16 v[142:143], v172 offset:16384
	ds_read_b64_tr_b16 v[144:145], v172 offset:18432
	v_mfma_f32_16x16x32_bf16 v[134:137], v[134:137], v[70:73], v[126:129]
	v_mfma_f32_16x16x32_bf16 v[2:5], v[154:157], v[70:73], v[2:5]
	v_mfma_f32_16x16x32_bf16 v[234:237], v[110:113], v[70:73], v[98:101]
	s_waitcnt lgkmcnt(5)
	v_mfma_f32_16x16x32_bf16 v[126:129], v[166:169], v[82:85], v[34:37]
	s_nop 2
	ds_read_b128 v[34:37], v244 offset:36864
	v_mfma_f32_16x16x32_bf16 v[122:125], v[214:217], v[82:85], v[38:41]
	s_waitcnt lgkmcnt(4)
	v_mfma_f32_16x16x32_bf16 v[118:121], v[230:233], v[82:85], v[42:45]
	s_waitcnt lgkmcnt(1)
	v_mfma_f32_16x16x32_bf16 v[114:117], v[142:145], v[82:85], v[30:33]
	s_nop 2
	ds_read_b128 v[30:33], v244 offset:38912
	v_mfma_f32_16x16x32_bf16 v[110:113], v[166:169], v[86:89], v[46:49]
	v_mfma_f32_16x16x32_bf16 v[106:109], v[214:217], v[86:89], v[50:53]
	v_mfma_f32_16x16x32_bf16 v[102:105], v[230:233], v[86:89], v[58:61]
	v_mfma_f32_16x16x32_bf16 v[98:101], v[142:145], v[86:89], v[26:29]
	s_nop 2
	ds_read_b128 v[26:29], v244 offset:40960
	s_waitcnt lgkmcnt(2)
	v_mfma_f32_16x16x32_bf16 v[94:97], v[166:169], v[34:37], v[62:65]
	v_mfma_f32_16x16x32_bf16 v[90:93], v[214:217], v[34:37], v[66:69]
	v_mfma_f32_16x16x32_bf16 v[86:89], v[230:233], v[34:37], v[74:77]
	v_mfma_f32_16x16x32_bf16 v[82:85], v[142:145], v[34:37], v[22:25]
	s_nop 2
	ds_read_b128 v[22:25], v244 offset:43008
	s_waitcnt lgkmcnt(2)
	v_mfma_f32_16x16x32_bf16 v[78:81], v[166:169], v[30:33], v[78:81]
	v_mfma_f32_16x16x32_bf16 v[74:77], v[214:217], v[30:33], v[150:153]
	v_mfma_f32_16x16x32_bf16 v[70:73], v[230:233], v[30:33], v[158:161]
	v_mfma_f32_16x16x32_bf16 v[66:69], v[142:145], v[30:33], v[18:21]
	s_nop 2
	ds_read_b128 v[18:21], v244 offset:45056
	s_waitcnt lgkmcnt(2)
	v_mfma_f32_16x16x32_bf16 v[62:65], v[166:169], v[26:29], v[54:57]
	v_mfma_f32_16x16x32_bf16 v[58:61], v[214:217], v[26:29], v[138:141]
	v_mfma_f32_16x16x32_bf16 v[54:57], v[230:233], v[26:29], v[162:165]
	v_mfma_f32_16x16x32_bf16 v[50:53], v[142:145], v[26:29], v[14:17]
	s_waitcnt lgkmcnt(1)
	v_mfma_f32_16x16x32_bf16 v[46:49], v[166:169], v[22:25], v[146:149]
	ds_read_b128 v[138:141], v244 offset:47104
	v_mfma_f32_16x16x32_bf16 v[42:45], v[214:217], v[22:25], v[206:209]
	v_mfma_f32_16x16x32_bf16 v[38:41], v[230:233], v[22:25], v[210:213]
	v_mfma_f32_16x16x32_bf16 v[34:37], v[142:145], v[22:25], v[10:13]
	s_waitcnt lgkmcnt(1)
	v_mfma_f32_16x16x32_bf16 v[30:33], v[166:169], v[18:21], v[218:221]
	v_mfma_f32_16x16x32_bf16 v[26:29], v[214:217], v[18:21], v[222:225]
	v_mfma_f32_16x16x32_bf16 v[22:25], v[230:233], v[18:21], v[226:229]
	v_mfma_f32_16x16x32_bf16 v[18:21], v[142:145], v[18:21], v[6:9]
	s_waitcnt lgkmcnt(0)
	v_mfma_f32_16x16x32_bf16 v[14:17], v[166:169], v[138:141], v[234:237]
	v_mfma_f32_16x16x32_bf16 v[10:13], v[214:217], v[138:141], v[134:137]
	v_mfma_f32_16x16x32_bf16 v[6:9], v[230:233], v[138:141], v[130:133]
	v_mfma_f32_16x16x32_bf16 v[2:5], v[142:145], v[138:141], v[2:5]
	s_waitcnt lgkmcnt(0)
	s_barrier
	s_nop 0
	v_mov_b32_e32 v131, 0
	s_andn2_b64 vcc, exec, s[12:13]
	v_mov_b32_e32 v133, 0
	v_mov_b32_e32 v134, 0
	s_cbranch_vccnz .LBB0_1536
	global_load_dword v131, v[184:185], off
	global_load_dword v133, v[186:187], off
	global_load_dword v134, v[188:189], off
	s_branch .LBB0_1536
